# v59 + saddr-form LDS-DMA addressing in the fp8 loops (no per-load 64-bit VALU address adds)
# speedup vs baseline: 1.0143x; 1.0036x over previous
; #define PG8_STAGE(bufoff, gbase, voff) do { _Pragma("unroll") for (int _i = 0; _i < 2; ++_i) \
;         __builtin_amdgcn_global_load_lds((const unsigned*)((const char*)(gbase) + (voff)[_i]), (PG8_LAS unsigned*)(lds + (bufoff) + ldsw + _i * 8192), 16, 0, 0); } while (0)
; #define PG8_WAIT_V(n) asm volatile("s_waitcnt vmcnt(" #n ")" ::: "memory")
; #define PG8_WAIT_L(n) asm volatile("s_waitcnt lgkmcnt(" #n ")" ::: "memory")
; #define PG8_BAR __builtin_amdgcn_s_barrier()
; #define PG8_SCHED __builtin_amdgcn_sched_barrier(0)
; template <class Epi, class Sched, bool ALIGN_EPI = true, bool F8 = false>
; __device__ __forceinline__ void gemm_phase(PG8_LAS unsigned char* lds, const Sched& S, const Epi& E) {
;     ...
;         for (int t = 0; t < nt; t += 2) {
;             const bool last = (t == nt - 2);
;             if constexpr (Sched::GATHER) { if (last && has_next) S.a_off(nxt, Rs, Cs, voffAn); }
;             const char* a1 = cA + (size_t)(t + 1) * kstep;
;             const char* a2 = last ? nA : cA + (size_t)(t + 2) * kstep; const char* b2 = last ? nB : cB + (size_t)(t + 2) * kstepB;
;             const char* a3 = a2 + kstep; const char* b3 = b2 + kstepB;
;             unsigned vA2[2][2];
; #pragma unroll
;             for (int h = 0; h < 2; ++h)
; #pragma unroll
;                 for (int i = 0; i < 2; ++i) { if constexpr (Sched::GATHER) vA2[h][i] = (last && has_next) ? voffAn[h][i] : voffA[h][i]; else vA2[h][i] = voffA[h][i]; }
;             PG8_LDB(B0, 0, 0); PG8_LDB(B1, 0, 1); PG8_SCHED; PG8_LDA(At, 0, 0); PG8_STAGE(PG8_SA(1, 1), a1, voffA[1]);
;             PG8_WAIT_V(8); PG8_WAIT_L(0); PG8_BAR; PG8_MMA(0, 0, At, B0); PG8_MMA(0, 1, At, B1); PG8_BAR; PG8_SCHED;
;             PG8_LDA(At, 0, 1); PG8_STAGE(PG8_SB(0, 0), b2, voffB[0]); PG8_STAGE(PG8_SB(0, 1), b2, voffB[1]); PG8_STAGE(PG8_SA(0, 0), a2, vA2[0]);
;             PG8_WAIT_V(8); PG8_WAIT_L(0); PG8_BAR; PG8_MMA(1, 0, At, B0); PG8_MMA(1, 1, At, B1); PG8_BAR; PG8_SCHED;
.LBB0_372:
	ds_read_b128 v[18:21], v207
	ds_read_b128 v[22:25], v207 offset:1024
	ds_read_b128 v[26:29], v207 offset:2048
	ds_read_b128 v[30:33], v207 offset:3072
	ds_read_b128 v[2:5], v208
	ds_read_b128 v[6:9], v208 offset:1024
	ds_read_b128 v[10:13], v208 offset:2048
	ds_read_b128 v[14:17], v208 offset:3072
	s_add_u32 s28, s26, 0x8000
	s_addc_u32 s29, s27, 0
	s_cmp_eq_u32 s21, 12
	s_cselect_b32 s40, s22, s28
	s_cselect_b32 s41, s23, s29
	s_cselect_b32 s30, s24, s5
	s_cselect_b32 s31, s25, s19
	s_add_u32 s28, s40, 0x8000
	s_addc_u32 s29, s41, 0
	s_add_i32 m0, s46, 0xc000
	ds_read_b128 v[212:215], v209
	ds_read_b128 v[216:219], v209 offset:1024
	ds_read_b128 v[220:223], v209 offset:2048
	ds_read_b128 v[224:227], v209 offset:3072
	ds_read_b128 v[228:231], v209 offset:4096
	ds_read_b128 v[232:235], v209 offset:5120
	ds_read_b128 v[236:239], v209 offset:6144
	ds_read_b128 v[240:243], v209 offset:7168
	global_load_lds_dwordx4 v190, s[26:27]
	s_add_i32 m0, s46, 0xe000
	s_nop 0
	global_load_lds_dwordx4 v188, s[26:27]
	s_waitcnt vmcnt(8)
	s_waitcnt lgkmcnt(0)
	s_setprio 1
	v_mfma_scale_f32_16x16x128_f8f6f4 v[158:161], v[18:25], v[212:219], v[158:161], v210, v210 op_sel_hi:[0,0,0]
	v_mfma_scale_f32_16x16x128_f8f6f4 v[154:157], v[26:33], v[212:219], v[154:157], v210, v210 op_sel_hi:[0,0,0]
	v_mfma_scale_f32_16x16x128_f8f6f4 v[142:145], v[18:25], v[220:227], v[142:145], v210, v210 op_sel_hi:[0,0,0]
	v_mfma_scale_f32_16x16x128_f8f6f4 v[138:141], v[26:33], v[220:227], v[138:141], v210, v210 op_sel_hi:[0,0,0]
	v_mfma_scale_f32_16x16x128_f8f6f4 v[126:129], v[18:25], v[228:235], v[126:129], v210, v210 op_sel_hi:[0,0,0]
	v_mfma_scale_f32_16x16x128_f8f6f4 v[122:125], v[26:33], v[228:235], v[122:125], v210, v210 op_sel_hi:[0,0,0]
	v_mfma_scale_f32_16x16x128_f8f6f4 v[110:113], v[18:25], v[236:243], v[110:113], v210, v210 op_sel_hi:[0,0,0]
	v_mfma_scale_f32_16x16x128_f8f6f4 v[106:109], v[26:33], v[236:243], v[106:109], v210, v210 op_sel_hi:[0,0,0]
	s_nop 3
	s_setprio 0
	s_setprio 1
	v_mfma_scale_f32_16x16x128_f8f6f4 v[150:153], v[2:9], v[212:219], v[150:153], v210, v210 op_sel_hi:[0,0,0]
	v_mfma_scale_f32_16x16x128_f8f6f4 v[146:149], v[10:17], v[212:219], v[146:149], v210, v210 op_sel_hi:[0,0,0]
	v_mfma_scale_f32_16x16x128_f8f6f4 v[134:137], v[2:9], v[220:227], v[134:137], v210, v210 op_sel_hi:[0,0,0]
	v_mfma_scale_f32_16x16x128_f8f6f4 v[130:133], v[10:17], v[220:227], v[130:133], v210, v210 op_sel_hi:[0,0,0]
	v_mfma_scale_f32_16x16x128_f8f6f4 v[118:121], v[2:9], v[228:235], v[118:121], v210, v210 op_sel_hi:[0,0,0]
	v_mfma_scale_f32_16x16x128_f8f6f4 v[114:117], v[10:17], v[228:235], v[114:117], v210, v210 op_sel_hi:[0,0,0]
	v_mfma_scale_f32_16x16x128_f8f6f4 v[102:105], v[2:9], v[236:243], v[102:105], v210, v210 op_sel_hi:[0,0,0]
	v_mfma_scale_f32_16x16x128_f8f6f4 v[98:101], v[10:17], v[236:243], v[98:101], v210, v210 op_sel_hi:[0,0,0]
	s_setprio 0
	s_barrier
	s_add_i32 s67, s62, s45
	s_mov_b32 m0, s67
	ds_read_b128 v[212:215], v209 offset:16384
	ds_read_b128 v[216:219], v209 offset:17408
	ds_read_b128 v[220:223], v209 offset:18432
	ds_read_b128 v[224:227], v209 offset:19456
	ds_read_b128 v[228:231], v209 offset:20480
	ds_read_b128 v[232:235], v209 offset:21504
	ds_read_b128 v[236:239], v209 offset:22528
	ds_read_b128 v[240:243], v209 offset:23552
	global_load_lds_dwordx4 v164, s[30:31]
	s_add_i32 m0, s67, 0x2000
	s_add_i32 s67, s63, s45
	global_load_lds_dwordx4 v166, s[30:31]
	s_add_u32 s98, s30, s8
	s_addc_u32 s99, s31, s9
	s_mov_b32 m0, s67
	s_nop 0
	global_load_lds_dwordx4 v164, s[98:99]
	s_add_u32 s100, s30, s8
	s_addc_u32 s101, s31, s9
	s_add_i32 m0, s67, 0x2000
	s_nop 0
	global_load_lds_dwordx4 v166, s[100:101]
	s_mov_b32 m0, s46
	s_nop 0
	global_load_lds_dwordx4 v174, s[40:41]
	s_mov_b32 m0, s47
	s_nop 0
	global_load_lds_dwordx4 v176, s[40:41]
	s_waitcnt vmcnt(8)
	s_waitcnt lgkmcnt(0)
	s_setprio 1
	v_mfma_scale_f32_16x16x128_f8f6f4 v[94:97], v[18:25], v[212:219], v[94:97], v210, v210 op_sel_hi:[0,0,0]
	v_mfma_scale_f32_16x16x128_f8f6f4 v[90:93], v[26:33], v[212:219], v[90:93], v210, v210 op_sel_hi:[0,0,0]
	v_mfma_scale_f32_16x16x128_f8f6f4 v[78:81], v[18:25], v[220:227], v[78:81], v210, v210 op_sel_hi:[0,0,0]
	v_mfma_scale_f32_16x16x128_f8f6f4 v[74:77], v[26:33], v[220:227], v[74:77], v210, v210 op_sel_hi:[0,0,0]
	v_mfma_scale_f32_16x16x128_f8f6f4 v[62:65], v[18:25], v[228:235], v[62:65], v210, v210 op_sel_hi:[0,0,0]
	v_mfma_scale_f32_16x16x128_f8f6f4 v[58:61], v[26:33], v[228:235], v[58:61], v210, v210 op_sel_hi:[0,0,0]
	v_mfma_scale_f32_16x16x128_f8f6f4 v[46:49], v[18:25], v[236:243], v[46:49], v210, v210 op_sel_hi:[0,0,0]
	v_mfma_scale_f32_16x16x128_f8f6f4 v[42:45], v[26:33], v[236:243], v[42:45], v210, v210 op_sel_hi:[0,0,0]
	s_nop 3
	s_setprio 0
	s_setprio 1
	v_mfma_scale_f32_16x16x128_f8f6f4 v[86:89], v[2:9], v[212:219], v[86:89], v210, v210 op_sel_hi:[0,0,0]
	v_mfma_scale_f32_16x16x128_f8f6f4 v[82:85], v[10:17], v[212:219], v[82:85], v210, v210 op_sel_hi:[0,0,0]
	v_mfma_scale_f32_16x16x128_f8f6f4 v[70:73], v[2:9], v[220:227], v[70:73], v210, v210 op_sel_hi:[0,0,0]
	v_mfma_scale_f32_16x16x128_f8f6f4 v[66:69], v[10:17], v[220:227], v[66:69], v210, v210 op_sel_hi:[0,0,0]
	v_mfma_scale_f32_16x16x128_f8f6f4 v[54:57], v[2:9], v[228:235], v[54:57], v210, v210 op_sel_hi:[0,0,0]
	v_mfma_scale_f32_16x16x128_f8f6f4 v[50:53], v[10:17], v[228:235], v[50:53], v210, v210 op_sel_hi:[0,0,0]
	v_mfma_scale_f32_16x16x128_f8f6f4 v[38:41], v[2:9], v[236:243], v[38:41], v210, v210 op_sel_hi:[0,0,0]
	v_mfma_scale_f32_16x16x128_f8f6f4 v[34:37], v[10:17], v[236:243], v[34:37], v210, v210 op_sel_hi:[0,0,0]
	s_setprio 0
	s_barrier
; #define PG8_STAGE(bufoff, gbase, voff) do { _Pragma("unroll") for (int _i = 0; _i < 2; ++_i) \
;         __builtin_amdgcn_global_load_lds((const unsigned*)((const char*)(gbase) + (voff)[_i]), (PG8_LAS unsigned*)(lds + (bufoff) + ldsw + _i * 8192), 16, 0, 0); } while (0)
; #define PG8_WAIT_V(n) asm volatile("s_waitcnt vmcnt(" #n ")" ::: "memory")
; #define PG8_WAIT_L(n) asm volatile("s_waitcnt lgkmcnt(" #n ")" ::: "memory")
; #define PG8_BAR __builtin_amdgcn_s_barrier()
; #define PG8_SCHED __builtin_amdgcn_sched_barrier(0)
; template <class Epi, class Sched, bool ALIGN_EPI = true, bool F8 = false>
; __device__ __forceinline__ void gemm_phase(PG8_LAS unsigned char* lds, const Sched& S, const Epi& E) {
;     ...
;         for (int t = 0; t < nt; t += 2) {
;     ...
;             PG8_LDB(B0, 1, 0); PG8_LDB(B1, 1, 1); PG8_SCHED; PG8_LDA(At, 1, 0); PG8_STAGE(PG8_SA(0, 1), a2, vA2[1]);
;             PG8_WAIT_V(8); PG8_WAIT_L(0); PG8_BAR; PG8_MMA(0, 0, At, B0); PG8_MMA(0, 1, At, B1); PG8_BAR; PG8_SCHED;
;             PG8_LDA(At, 1, 1); PG8_STAGE(PG8_SB(1, 0), b3, voffB[0]); PG8_STAGE(PG8_SB(1, 1), b3, voffB[1]); PG8_STAGE(PG8_SA(1, 0), a3, vA2[0]);
;             PG8_WAIT_V(8); PG8_WAIT_L(0); PG8_BAR; PG8_MMA(1, 0, At, B0); PG8_MMA(1, 1, At, B1); PG8_BAR; PG8_SCHED;
	s_add_i32 s67, 0, 0x18000
	s_add_i32 s68, 0, 0x1c000
	v_add_u32_e32 v14, s67, v202
	v_add_u32_e32 v30, s68, v202
	ds_read_b128 v[2:5], v14
	ds_read_b128 v[6:9], v14 offset:1024
	ds_read_b128 v[10:13], v14 offset:2048
	ds_read_b128 v[14:17], v14 offset:3072
	ds_read_b128 v[18:21], v30
	ds_read_b128 v[22:25], v30 offset:1024
	ds_read_b128 v[26:29], v30 offset:2048
	ds_read_b128 v[30:33], v30 offset:3072
	s_mov_b32 m0, s48
	ds_read_b128 v[212:215], v209 offset:32768
	ds_read_b128 v[216:219], v209 offset:33792
	ds_read_b128 v[220:223], v209 offset:34816
	ds_read_b128 v[224:227], v209 offset:35840
	ds_read_b128 v[228:231], v209 offset:36864
	ds_read_b128 v[232:235], v209 offset:37888
	ds_read_b128 v[236:239], v209 offset:38912
	ds_read_b128 v[240:243], v209 offset:39936
	global_load_lds_dwordx4 v178, s[40:41]
	s_mov_b32 m0, s49
	s_nop 0
	global_load_lds_dwordx4 v180, s[40:41]
	s_waitcnt vmcnt(8)
	s_waitcnt lgkmcnt(0)
	s_setprio 1
	v_mfma_scale_f32_16x16x128_f8f6f4 v[158:161], v[2:9], v[212:219], v[158:161], v210, v210 op_sel_hi:[0,0,0]
	v_mfma_scale_f32_16x16x128_f8f6f4 v[154:157], v[10:17], v[212:219], v[154:157], v210, v210 op_sel_hi:[0,0,0]
	v_mfma_scale_f32_16x16x128_f8f6f4 v[142:145], v[2:9], v[220:227], v[142:145], v210, v210 op_sel_hi:[0,0,0]
	v_mfma_scale_f32_16x16x128_f8f6f4 v[138:141], v[10:17], v[220:227], v[138:141], v210, v210 op_sel_hi:[0,0,0]
	v_mfma_scale_f32_16x16x128_f8f6f4 v[126:129], v[2:9], v[228:235], v[126:129], v210, v210 op_sel_hi:[0,0,0]
	v_mfma_scale_f32_16x16x128_f8f6f4 v[122:125], v[10:17], v[228:235], v[122:125], v210, v210 op_sel_hi:[0,0,0]
	v_mfma_scale_f32_16x16x128_f8f6f4 v[110:113], v[2:9], v[236:243], v[110:113], v210, v210 op_sel_hi:[0,0,0]
	v_mfma_scale_f32_16x16x128_f8f6f4 v[106:109], v[10:17], v[236:243], v[106:109], v210, v210 op_sel_hi:[0,0,0]
	s_nop 3
	s_setprio 0
	s_setprio 1
	v_mfma_scale_f32_16x16x128_f8f6f4 v[150:153], v[18:25], v[212:219], v[150:153], v210, v210 op_sel_hi:[0,0,0]
	v_mfma_scale_f32_16x16x128_f8f6f4 v[146:149], v[26:33], v[212:219], v[146:149], v210, v210 op_sel_hi:[0,0,0]
	v_mfma_scale_f32_16x16x128_f8f6f4 v[134:137], v[18:25], v[220:227], v[134:137], v210, v210 op_sel_hi:[0,0,0]
	v_mfma_scale_f32_16x16x128_f8f6f4 v[130:133], v[26:33], v[220:227], v[130:133], v210, v210 op_sel_hi:[0,0,0]
	v_mfma_scale_f32_16x16x128_f8f6f4 v[118:121], v[18:25], v[228:235], v[118:121], v210, v210 op_sel_hi:[0,0,0]
	v_mfma_scale_f32_16x16x128_f8f6f4 v[114:117], v[26:33], v[228:235], v[114:117], v210, v210 op_sel_hi:[0,0,0]
	v_mfma_scale_f32_16x16x128_f8f6f4 v[102:105], v[18:25], v[236:243], v[102:105], v210, v210 op_sel_hi:[0,0,0]
	v_mfma_scale_f32_16x16x128_f8f6f4 v[98:101], v[26:33], v[236:243], v[98:101], v210, v210 op_sel_hi:[0,0,0]
	s_setprio 0
	s_barrier
	s_add_u32 s30, s30, 0x8000
	s_addc_u32 s31, s31, 0
	s_add_i32 s40, s67, s45
	s_mov_b32 m0, s40
	ds_read_b128 v[212:215], v209 offset:49152
	ds_read_b128 v[216:219], v209 offset:50176
	ds_read_b128 v[220:223], v209 offset:51200
	ds_read_b128 v[224:227], v209 offset:52224
	ds_read_b128 v[228:231], v209 offset:53248
	ds_read_b128 v[232:235], v209 offset:54272
	ds_read_b128 v[236:239], v209 offset:55296
	ds_read_b128 v[240:243], v209 offset:56320
	global_load_lds_dwordx4 v164, s[30:31]
	s_add_i32 m0, s40, 0x2000
	s_add_i32 s40, s68, s45
	global_load_lds_dwordx4 v166, s[30:31]
	s_mov_b32 m0, s40
	s_nop 0
	global_load_lds_dwordx4 v168, s[30:31]
	s_add_i32 m0, s40, 0x2000
	s_nop 0
	global_load_lds_dwordx4 v172, s[30:31]
	s_mov_b32 m0, s52
	s_nop 0
	global_load_lds_dwordx4 v174, s[28:29]
	s_mov_b32 m0, s53
	s_nop 0
	global_load_lds_dwordx4 v176, s[28:29]
	s_waitcnt vmcnt(8)
	s_waitcnt lgkmcnt(0)
	s_setprio 1
	v_mfma_scale_f32_16x16x128_f8f6f4 v[94:97], v[2:9], v[212:219], v[94:97], v210, v210 op_sel_hi:[0,0,0]
	v_mfma_scale_f32_16x16x128_f8f6f4 v[90:93], v[10:17], v[212:219], v[90:93], v210, v210 op_sel_hi:[0,0,0]
	v_mfma_scale_f32_16x16x128_f8f6f4 v[78:81], v[2:9], v[220:227], v[78:81], v210, v210 op_sel_hi:[0,0,0]
	v_mfma_scale_f32_16x16x128_f8f6f4 v[74:77], v[10:17], v[220:227], v[74:77], v210, v210 op_sel_hi:[0,0,0]
	v_mfma_scale_f32_16x16x128_f8f6f4 v[62:65], v[2:9], v[228:235], v[62:65], v210, v210 op_sel_hi:[0,0,0]
	v_mfma_scale_f32_16x16x128_f8f6f4 v[58:61], v[10:17], v[228:235], v[58:61], v210, v210 op_sel_hi:[0,0,0]
	v_mfma_scale_f32_16x16x128_f8f6f4 v[46:49], v[2:9], v[236:243], v[46:49], v210, v210 op_sel_hi:[0,0,0]
	v_mfma_scale_f32_16x16x128_f8f6f4 v[42:45], v[10:17], v[236:243], v[42:45], v210, v210 op_sel_hi:[0,0,0]
	s_nop 3
	s_setprio 0
	s_setprio 1
	v_mfma_scale_f32_16x16x128_f8f6f4 v[86:89], v[18:25], v[212:219], v[86:89], v210, v210 op_sel_hi:[0,0,0]
	v_mfma_scale_f32_16x16x128_f8f6f4 v[82:85], v[26:33], v[212:219], v[82:85], v210, v210 op_sel_hi:[0,0,0]
	v_mfma_scale_f32_16x16x128_f8f6f4 v[70:73], v[18:25], v[220:227], v[70:73], v210, v210 op_sel_hi:[0,0,0]
	v_mfma_scale_f32_16x16x128_f8f6f4 v[66:69], v[26:33], v[220:227], v[66:69], v210, v210 op_sel_hi:[0,0,0]
	v_mfma_scale_f32_16x16x128_f8f6f4 v[54:57], v[18:25], v[228:235], v[54:57], v210, v210 op_sel_hi:[0,0,0]
	v_mfma_scale_f32_16x16x128_f8f6f4 v[50:53], v[26:33], v[228:235], v[50:53], v210, v210 op_sel_hi:[0,0,0]
	v_mfma_scale_f32_16x16x128_f8f6f4 v[38:41], v[18:25], v[236:243], v[38:41], v210, v210 op_sel_hi:[0,0,0]
	v_mfma_scale_f32_16x16x128_f8f6f4 v[34:37], v[26:33], v[236:243], v[34:37], v210, v210 op_sel_hi:[0,0,0]
	s_setprio 0
	s_barrier
	s_add_i32 s21, s21, 2
	s_add_u32 s5, s5, 0x10000
	s_addc_u32 s19, s19, 0
	s_add_u32 s26, s26, 0x10000
	s_addc_u32 s27, s27, 0
	s_cmp_gt_u32 s21, 13
	s_cbranch_scc0 .LBB0_372
	s_branch .Lfx_9967
; #define PG8_STAGE(bufoff, gbase, voff) do { _Pragma("unroll") for (int _i = 0; _i < 2; ++_i) \
;         __builtin_amdgcn_global_load_lds((const unsigned*)((const char*)(gbase) + (voff)[_i]), (PG8_LAS unsigned*)(lds + (bufoff) + ldsw + _i * 8192), 16, 0, 0); } while (0)
; #define PG8_WAIT_V(n) asm volatile("s_waitcnt vmcnt(" #n ")" ::: "memory")
; #define PG8_WAIT_L(n) asm volatile("s_waitcnt lgkmcnt(" #n ")" ::: "memory")
; #define PG8_BAR __builtin_amdgcn_s_barrier()
; #define PG8_SCHED __builtin_amdgcn_sched_barrier(0)
; template <class Epi, class Sched, bool ALIGN_EPI = true, bool F8 = false>
; __device__ __forceinline__ void gemm_phase(PG8_LAS unsigned char* lds, const Sched& S, const Epi& E) {
;     ...
;             PG8_LDB(B0, 0, 0); PG8_LDB(B1, 0, 1); PG8_SCHED; PG8_LDA(At, 0, 0); PG8_STAGE(PG8_SA(1, 1), a1, voffA[1]);
;             PG8_WAIT_V(8); PG8_WAIT_L(0); PG8_BAR; PG8_MMA(0, 0, At, B0); PG8_MMA(0, 1, At, B1); PG8_BAR; PG8_SCHED;
;             PG8_LDA(At, 0, 1); PG8_STAGE(PG8_SB(0, 0), b2, voffB[0]); PG8_STAGE(PG8_SB(0, 1), b2, voffB[1]); PG8_STAGE(PG8_SA(0, 0), a2, vA2[0]);
;             PG8_WAIT_V(8); PG8_WAIT_L(0); PG8_BAR; PG8_MMA(1, 0, At, B0); PG8_MMA(1, 1, At, B1); PG8_BAR; PG8_SCHED;
;             PG8_LDB(B0, 1, 0); PG8_LDB(B1, 1, 1); PG8_SCHED; PG8_LDA(At, 1, 0); PG8_STAGE(PG8_SA(0, 1), a2, vA2[1]);
;             PG8_WAIT_V(8); PG8_WAIT_L(0); PG8_BAR; PG8_MMA(0, 0, At, B0); PG8_MMA(0, 1, At, B1); PG8_BAR; PG8_SCHED;
.Lh1e_9967:
.Lh1_372:
	ds_read_b128 v[18:21], v207
	ds_read_b128 v[22:25], v207 offset:1024
	ds_read_b128 v[26:29], v207 offset:2048
	ds_read_b128 v[30:33], v207 offset:3072
	ds_read_b128 v[2:5], v208
	ds_read_b128 v[6:9], v208 offset:1024
	ds_read_b128 v[10:13], v208 offset:2048
	ds_read_b128 v[14:17], v208 offset:3072
	s_add_u32 s28, s26, 0x8000
	s_addc_u32 s29, s27, 0
	s_cmp_eq_u32 s21, 12
	s_cselect_b32 s40, s22, s28
	s_cselect_b32 s41, s23, s29
	s_cselect_b32 s30, s24, s5
	s_cselect_b32 s31, s25, s19
	s_add_u32 s28, s40, 0x8000
	s_addc_u32 s29, s41, 0
	s_add_i32 m0, s46, 0xc000
	ds_read_b128 v[212:215], v209
	ds_read_b128 v[216:219], v209 offset:1024
	ds_read_b128 v[220:223], v209 offset:2048
	ds_read_b128 v[224:227], v209 offset:3072
	ds_read_b128 v[228:231], v209 offset:4096
	ds_read_b128 v[232:235], v209 offset:5120
	ds_read_b128 v[236:239], v209 offset:6144
	ds_read_b128 v[240:243], v209 offset:7168
	global_load_lds_dwordx4 v190, s[26:27]
	s_add_i32 m0, s46, 0xe000
	s_nop 0
	global_load_lds_dwordx4 v188, s[26:27]
	s_waitcnt vmcnt(8)
	s_waitcnt lgkmcnt(0)
	s_barrier
	s_setprio 2
	v_mfma_scale_f32_16x16x128_f8f6f4 v[158:161], v[18:25], v[212:219], v[158:161], v210, v210 op_sel_hi:[0,0,0]
	v_mfma_scale_f32_16x16x128_f8f6f4 v[154:157], v[26:33], v[212:219], v[154:157], v210, v210 op_sel_hi:[0,0,0]
	v_mfma_scale_f32_16x16x128_f8f6f4 v[142:145], v[18:25], v[220:227], v[142:145], v210, v210 op_sel_hi:[0,0,0]
	v_mfma_scale_f32_16x16x128_f8f6f4 v[138:141], v[26:33], v[220:227], v[138:141], v210, v210 op_sel_hi:[0,0,0]
	v_mfma_scale_f32_16x16x128_f8f6f4 v[126:129], v[18:25], v[228:235], v[126:129], v210, v210 op_sel_hi:[0,0,0]
	v_mfma_scale_f32_16x16x128_f8f6f4 v[122:125], v[26:33], v[228:235], v[122:125], v210, v210 op_sel_hi:[0,0,0]
	v_mfma_scale_f32_16x16x128_f8f6f4 v[110:113], v[18:25], v[236:243], v[110:113], v210, v210 op_sel_hi:[0,0,0]
	v_mfma_scale_f32_16x16x128_f8f6f4 v[106:109], v[26:33], v[236:243], v[106:109], v210, v210 op_sel_hi:[0,0,0]
	s_nop 3
	s_setprio 0
	s_setprio 2
	v_mfma_scale_f32_16x16x128_f8f6f4 v[150:153], v[2:9], v[212:219], v[150:153], v210, v210 op_sel_hi:[0,0,0]
	v_mfma_scale_f32_16x16x128_f8f6f4 v[146:149], v[10:17], v[212:219], v[146:149], v210, v210 op_sel_hi:[0,0,0]
	v_mfma_scale_f32_16x16x128_f8f6f4 v[134:137], v[2:9], v[220:227], v[134:137], v210, v210 op_sel_hi:[0,0,0]
	v_mfma_scale_f32_16x16x128_f8f6f4 v[130:133], v[10:17], v[220:227], v[130:133], v210, v210 op_sel_hi:[0,0,0]
	v_mfma_scale_f32_16x16x128_f8f6f4 v[118:121], v[2:9], v[228:235], v[118:121], v210, v210 op_sel_hi:[0,0,0]
	v_mfma_scale_f32_16x16x128_f8f6f4 v[114:117], v[10:17], v[228:235], v[114:117], v210, v210 op_sel_hi:[0,0,0]
	v_mfma_scale_f32_16x16x128_f8f6f4 v[102:105], v[2:9], v[236:243], v[102:105], v210, v210 op_sel_hi:[0,0,0]
	v_mfma_scale_f32_16x16x128_f8f6f4 v[98:101], v[10:17], v[236:243], v[98:101], v210, v210 op_sel_hi:[0,0,0]
	s_setprio 0
	s_add_i32 s67, s62, s45
	s_mov_b32 m0, s67
	ds_read_b128 v[212:215], v209 offset:16384
	ds_read_b128 v[216:219], v209 offset:17408
	ds_read_b128 v[220:223], v209 offset:18432
	ds_read_b128 v[224:227], v209 offset:19456
	ds_read_b128 v[228:231], v209 offset:20480
	ds_read_b128 v[232:235], v209 offset:21504
	ds_read_b128 v[236:239], v209 offset:22528
	ds_read_b128 v[240:243], v209 offset:23552
	global_load_lds_dwordx4 v164, s[30:31]
	s_add_i32 m0, s67, 0x2000
	s_add_i32 s67, s63, s45
	global_load_lds_dwordx4 v166, s[30:31]
	s_add_u32 s98, s30, s8
	s_addc_u32 s99, s31, s9
	s_mov_b32 m0, s67
	s_nop 0
	global_load_lds_dwordx4 v164, s[98:99]
	s_add_u32 s100, s30, s8
	s_addc_u32 s101, s31, s9
	s_add_i32 m0, s67, 0x2000
	s_nop 0
	global_load_lds_dwordx4 v166, s[100:101]
	s_mov_b32 m0, s46
	s_nop 0
	global_load_lds_dwordx4 v174, s[40:41]
	s_mov_b32 m0, s47
	s_nop 0
	global_load_lds_dwordx4 v176, s[40:41]
	s_waitcnt vmcnt(8)
	s_waitcnt lgkmcnt(0)
	s_barrier
	s_setprio 2
	v_mfma_scale_f32_16x16x128_f8f6f4 v[94:97], v[18:25], v[212:219], v[94:97], v210, v210 op_sel_hi:[0,0,0]
	v_mfma_scale_f32_16x16x128_f8f6f4 v[90:93], v[26:33], v[212:219], v[90:93], v210, v210 op_sel_hi:[0,0,0]
	v_mfma_scale_f32_16x16x128_f8f6f4 v[78:81], v[18:25], v[220:227], v[78:81], v210, v210 op_sel_hi:[0,0,0]
	v_mfma_scale_f32_16x16x128_f8f6f4 v[74:77], v[26:33], v[220:227], v[74:77], v210, v210 op_sel_hi:[0,0,0]
	v_mfma_scale_f32_16x16x128_f8f6f4 v[62:65], v[18:25], v[228:235], v[62:65], v210, v210 op_sel_hi:[0,0,0]
	v_mfma_scale_f32_16x16x128_f8f6f4 v[58:61], v[26:33], v[228:235], v[58:61], v210, v210 op_sel_hi:[0,0,0]
	v_mfma_scale_f32_16x16x128_f8f6f4 v[46:49], v[18:25], v[236:243], v[46:49], v210, v210 op_sel_hi:[0,0,0]
	v_mfma_scale_f32_16x16x128_f8f6f4 v[42:45], v[26:33], v[236:243], v[42:45], v210, v210 op_sel_hi:[0,0,0]
	s_nop 3
	s_setprio 0
	s_setprio 2
	v_mfma_scale_f32_16x16x128_f8f6f4 v[86:89], v[2:9], v[212:219], v[86:89], v210, v210 op_sel_hi:[0,0,0]
	v_mfma_scale_f32_16x16x128_f8f6f4 v[82:85], v[10:17], v[212:219], v[82:85], v210, v210 op_sel_hi:[0,0,0]
	v_mfma_scale_f32_16x16x128_f8f6f4 v[70:73], v[2:9], v[220:227], v[70:73], v210, v210 op_sel_hi:[0,0,0]
	v_mfma_scale_f32_16x16x128_f8f6f4 v[66:69], v[10:17], v[220:227], v[66:69], v210, v210 op_sel_hi:[0,0,0]
	v_mfma_scale_f32_16x16x128_f8f6f4 v[54:57], v[2:9], v[228:235], v[54:57], v210, v210 op_sel_hi:[0,0,0]
	v_mfma_scale_f32_16x16x128_f8f6f4 v[50:53], v[10:17], v[228:235], v[50:53], v210, v210 op_sel_hi:[0,0,0]
	v_mfma_scale_f32_16x16x128_f8f6f4 v[38:41], v[2:9], v[236:243], v[38:41], v210, v210 op_sel_hi:[0,0,0]
	v_mfma_scale_f32_16x16x128_f8f6f4 v[34:37], v[10:17], v[236:243], v[34:37], v210, v210 op_sel_hi:[0,0,0]
	s_setprio 0
	s_add_i32 s67, 0, 0x18000
	s_add_i32 s68, 0, 0x1c000
	v_add_u32_e32 v14, s67, v202
	v_add_u32_e32 v30, s68, v202
	ds_read_b128 v[2:5], v14
	ds_read_b128 v[6:9], v14 offset:1024
	ds_read_b128 v[10:13], v14 offset:2048
	ds_read_b128 v[14:17], v14 offset:3072
	ds_read_b128 v[18:21], v30
	ds_read_b128 v[22:25], v30 offset:1024
	ds_read_b128 v[26:29], v30 offset:2048
	ds_read_b128 v[30:33], v30 offset:3072
	s_mov_b32 m0, s48
	ds_read_b128 v[212:215], v209 offset:32768
	ds_read_b128 v[216:219], v209 offset:33792
	ds_read_b128 v[220:223], v209 offset:34816
	ds_read_b128 v[224:227], v209 offset:35840
	ds_read_b128 v[228:231], v209 offset:36864
	ds_read_b128 v[232:235], v209 offset:37888
	ds_read_b128 v[236:239], v209 offset:38912
	ds_read_b128 v[240:243], v209 offset:39936
	global_load_lds_dwordx4 v178, s[40:41]
	s_mov_b32 m0, s49
	s_nop 0
	global_load_lds_dwordx4 v180, s[40:41]
	s_waitcnt vmcnt(8)
	s_waitcnt lgkmcnt(0)
	s_barrier
; #define PG8_STAGE(bufoff, gbase, voff) do { _Pragma("unroll") for (int _i = 0; _i < 2; ++_i) \
;         __builtin_amdgcn_global_load_lds((const unsigned*)((const char*)(gbase) + (voff)[_i]), (PG8_LAS unsigned*)(lds + (bufoff) + ldsw + _i * 8192), 16, 0, 0); } while (0)
; #define PG8_WAIT_V(n) asm volatile("s_waitcnt vmcnt(" #n ")" ::: "memory")
; #define PG8_WAIT_L(n) asm volatile("s_waitcnt lgkmcnt(" #n ")" ::: "memory")
; #define PG8_BAR __builtin_amdgcn_s_barrier()
; #define PG8_SCHED __builtin_amdgcn_sched_barrier(0)
; template <class Epi, class Sched, bool ALIGN_EPI = true, bool F8 = false>
; __device__ __forceinline__ void gemm_phase(PG8_LAS unsigned char* lds, const Sched& S, const Epi& E) {
;     ...
;         for (int t = 0; t < nt; t += 2) {
;     ...
;             PG8_WAIT_V(8); PG8_WAIT_L(0); PG8_BAR; PG8_MMA(0, 0, At, B0); PG8_MMA(0, 1, At, B1); PG8_BAR; PG8_SCHED;
;             PG8_LDA(At, 1, 1); PG8_STAGE(PG8_SB(1, 0), b3, voffB[0]); PG8_STAGE(PG8_SB(1, 1), b3, voffB[1]); PG8_STAGE(PG8_SA(1, 0), a3, vA2[0]);
;             PG8_WAIT_V(8); PG8_WAIT_L(0); PG8_BAR; PG8_MMA(1, 0, At, B0); PG8_MMA(1, 1, At, B1); PG8_BAR; PG8_SCHED;
	s_setprio 2
	v_mfma_scale_f32_16x16x128_f8f6f4 v[158:161], v[2:9], v[212:219], v[158:161], v210, v210 op_sel_hi:[0,0,0]
	v_mfma_scale_f32_16x16x128_f8f6f4 v[154:157], v[10:17], v[212:219], v[154:157], v210, v210 op_sel_hi:[0,0,0]
	v_mfma_scale_f32_16x16x128_f8f6f4 v[142:145], v[2:9], v[220:227], v[142:145], v210, v210 op_sel_hi:[0,0,0]
	v_mfma_scale_f32_16x16x128_f8f6f4 v[138:141], v[10:17], v[220:227], v[138:141], v210, v210 op_sel_hi:[0,0,0]
	v_mfma_scale_f32_16x16x128_f8f6f4 v[126:129], v[2:9], v[228:235], v[126:129], v210, v210 op_sel_hi:[0,0,0]
	v_mfma_scale_f32_16x16x128_f8f6f4 v[122:125], v[10:17], v[228:235], v[122:125], v210, v210 op_sel_hi:[0,0,0]
	v_mfma_scale_f32_16x16x128_f8f6f4 v[110:113], v[2:9], v[236:243], v[110:113], v210, v210 op_sel_hi:[0,0,0]
	v_mfma_scale_f32_16x16x128_f8f6f4 v[106:109], v[10:17], v[236:243], v[106:109], v210, v210 op_sel_hi:[0,0,0]
	s_nop 3
	s_setprio 0
	s_setprio 2
	v_mfma_scale_f32_16x16x128_f8f6f4 v[150:153], v[18:25], v[212:219], v[150:153], v210, v210 op_sel_hi:[0,0,0]
	v_mfma_scale_f32_16x16x128_f8f6f4 v[146:149], v[26:33], v[212:219], v[146:149], v210, v210 op_sel_hi:[0,0,0]
	v_mfma_scale_f32_16x16x128_f8f6f4 v[134:137], v[18:25], v[220:227], v[134:137], v210, v210 op_sel_hi:[0,0,0]
	v_mfma_scale_f32_16x16x128_f8f6f4 v[130:133], v[26:33], v[220:227], v[130:133], v210, v210 op_sel_hi:[0,0,0]
	v_mfma_scale_f32_16x16x128_f8f6f4 v[118:121], v[18:25], v[228:235], v[118:121], v210, v210 op_sel_hi:[0,0,0]
	v_mfma_scale_f32_16x16x128_f8f6f4 v[114:117], v[26:33], v[228:235], v[114:117], v210, v210 op_sel_hi:[0,0,0]
	v_mfma_scale_f32_16x16x128_f8f6f4 v[102:105], v[18:25], v[236:243], v[102:105], v210, v210 op_sel_hi:[0,0,0]
	v_mfma_scale_f32_16x16x128_f8f6f4 v[98:101], v[26:33], v[236:243], v[98:101], v210, v210 op_sel_hi:[0,0,0]
	s_setprio 0
	s_add_u32 s30, s30, 0x8000
	s_addc_u32 s31, s31, 0
	s_add_i32 s40, s67, s45
	s_mov_b32 m0, s40
	ds_read_b128 v[212:215], v209 offset:49152
	ds_read_b128 v[216:219], v209 offset:50176
	ds_read_b128 v[220:223], v209 offset:51200
	ds_read_b128 v[224:227], v209 offset:52224
	ds_read_b128 v[228:231], v209 offset:53248
	ds_read_b128 v[232:235], v209 offset:54272
	ds_read_b128 v[236:239], v209 offset:55296
	ds_read_b128 v[240:243], v209 offset:56320
	global_load_lds_dwordx4 v164, s[30:31]
	s_add_i32 m0, s40, 0x2000
	s_add_i32 s40, s68, s45
	global_load_lds_dwordx4 v166, s[30:31]
	s_mov_b32 m0, s40
	s_nop 0
	global_load_lds_dwordx4 v168, s[30:31]
	s_add_i32 m0, s40, 0x2000
	s_nop 0
	global_load_lds_dwordx4 v172, s[30:31]
	s_mov_b32 m0, s52
	s_nop 0
	global_load_lds_dwordx4 v174, s[28:29]
	s_mov_b32 m0, s53
	s_nop 0
	global_load_lds_dwordx4 v176, s[28:29]
	s_waitcnt vmcnt(8)
	s_waitcnt lgkmcnt(0)
	s_barrier
	s_setprio 2
	v_mfma_scale_f32_16x16x128_f8f6f4 v[94:97], v[2:9], v[212:219], v[94:97], v210, v210 op_sel_hi:[0,0,0]
	v_mfma_scale_f32_16x16x128_f8f6f4 v[90:93], v[10:17], v[212:219], v[90:93], v210, v210 op_sel_hi:[0,0,0]
	v_mfma_scale_f32_16x16x128_f8f6f4 v[78:81], v[2:9], v[220:227], v[78:81], v210, v210 op_sel_hi:[0,0,0]
	v_mfma_scale_f32_16x16x128_f8f6f4 v[74:77], v[10:17], v[220:227], v[74:77], v210, v210 op_sel_hi:[0,0,0]
	v_mfma_scale_f32_16x16x128_f8f6f4 v[62:65], v[2:9], v[228:235], v[62:65], v210, v210 op_sel_hi:[0,0,0]
	v_mfma_scale_f32_16x16x128_f8f6f4 v[58:61], v[10:17], v[228:235], v[58:61], v210, v210 op_sel_hi:[0,0,0]
	v_mfma_scale_f32_16x16x128_f8f6f4 v[46:49], v[2:9], v[236:243], v[46:49], v210, v210 op_sel_hi:[0,0,0]
	v_mfma_scale_f32_16x16x128_f8f6f4 v[42:45], v[10:17], v[236:243], v[42:45], v210, v210 op_sel_hi:[0,0,0]
	s_nop 3
	s_setprio 0
	s_setprio 2
	v_mfma_scale_f32_16x16x128_f8f6f4 v[86:89], v[18:25], v[212:219], v[86:89], v210, v210 op_sel_hi:[0,0,0]
	v_mfma_scale_f32_16x16x128_f8f6f4 v[82:85], v[26:33], v[212:219], v[82:85], v210, v210 op_sel_hi:[0,0,0]
	v_mfma_scale_f32_16x16x128_f8f6f4 v[70:73], v[18:25], v[220:227], v[70:73], v210, v210 op_sel_hi:[0,0,0]
	v_mfma_scale_f32_16x16x128_f8f6f4 v[66:69], v[26:33], v[220:227], v[66:69], v210, v210 op_sel_hi:[0,0,0]
	v_mfma_scale_f32_16x16x128_f8f6f4 v[54:57], v[18:25], v[228:235], v[54:57], v210, v210 op_sel_hi:[0,0,0]
	v_mfma_scale_f32_16x16x128_f8f6f4 v[50:53], v[26:33], v[228:235], v[50:53], v210, v210 op_sel_hi:[0,0,0]
	v_mfma_scale_f32_16x16x128_f8f6f4 v[38:41], v[18:25], v[236:243], v[38:41], v210, v210 op_sel_hi:[0,0,0]
	v_mfma_scale_f32_16x16x128_f8f6f4 v[34:37], v[26:33], v[236:243], v[34:37], v210, v210 op_sel_hi:[0,0,0]
	s_setprio 0
	s_add_i32 s21, s21, 2
	s_add_u32 s5, s5, 0x10000
	s_addc_u32 s19, s19, 0
	s_add_u32 s26, s26, 0x10000
	s_addc_u32 s27, s27, 0
	s_cmp_gt_u32 s21, 13
	s_cbranch_scc0 .Lh1_372

; #define PG8_STAGE(bufoff, gbase, voff) do { _Pragma("unroll") for (int _i = 0; _i < 2; ++_i) \
;         __builtin_amdgcn_global_load_lds((const unsigned*)((const char*)(gbase) + (voff)[_i]), (PG8_LAS unsigned*)(lds + (bufoff) + ldsw + _i * 8192), 16, 0, 0); } while (0)
; #define PG8_WAIT_V(n) asm volatile("s_waitcnt vmcnt(" #n ")" ::: "memory")
; #define PG8_WAIT_L(n) asm volatile("s_waitcnt lgkmcnt(" #n ")" ::: "memory")
; #define PG8_BAR __builtin_amdgcn_s_barrier()
; #define PG8_SCHED __builtin_amdgcn_sched_barrier(0)
; template <class Epi, class Sched, bool ALIGN_EPI = true, bool F8 = false>
; __device__ __forceinline__ void gemm_phase(PG8_LAS unsigned char* lds, const Sched& S, const Epi& E) {
;     ...
;         for (int t = 0; t < nt; t += 2) {
;             const bool last = (t == nt - 2);
;             if constexpr (Sched::GATHER) { if (last && has_next) S.a_off(nxt, Rs, Cs, voffAn); }
;             const char* a1 = cA + (size_t)(t + 1) * kstep;
;             const char* a2 = last ? nA : cA + (size_t)(t + 2) * kstep; const char* b2 = last ? nB : cB + (size_t)(t + 2) * kstepB;
;             const char* a3 = a2 + kstep; const char* b3 = b2 + kstepB;
;             unsigned vA2[2][2];
; #pragma unroll
;             for (int h = 0; h < 2; ++h)
; #pragma unroll
;                 for (int i = 0; i < 2; ++i) { if constexpr (Sched::GATHER) vA2[h][i] = (last && has_next) ? voffAn[h][i] : voffA[h][i]; else vA2[h][i] = voffA[h][i]; }
;             PG8_LDB(B0, 0, 0); PG8_LDB(B1, 0, 1); PG8_SCHED; PG8_LDA(At, 0, 0); PG8_STAGE(PG8_SA(1, 1), a1, voffA[1]);
;             PG8_WAIT_V(8); PG8_WAIT_L(0); PG8_BAR; PG8_MMA(0, 0, At, B0); PG8_MMA(0, 1, At, B1); PG8_BAR; PG8_SCHED;
;             PG8_LDA(At, 0, 1); PG8_STAGE(PG8_SB(0, 0), b2, voffB[0]); PG8_STAGE(PG8_SB(0, 1), b2, voffB[1]); PG8_STAGE(PG8_SA(0, 0), a2, vA2[0]);
;             PG8_WAIT_V(8); PG8_WAIT_L(0); PG8_BAR; PG8_MMA(1, 0, At, B0); PG8_MMA(1, 1, At, B1); PG8_BAR; PG8_SCHED;
.LBB0_428:
	ds_read_b128 v[18:21], v192
	ds_read_b128 v[22:25], v192 offset:1024
	ds_read_b128 v[26:29], v192 offset:2048
	ds_read_b128 v[30:33], v192 offset:3072
	ds_read_b128 v[2:5], v193
	ds_read_b128 v[6:9], v193 offset:1024
	ds_read_b128 v[10:13], v193 offset:2048
	ds_read_b128 v[14:17], v193 offset:3072
	s_add_u32 s26, s24, 0x8000
	s_addc_u32 s27, s25, 0
	s_cmp_eq_u32 s74, 12
	s_cselect_b32 s30, s20, s26
	s_cselect_b32 s31, s21, s27
	s_cselect_b32 s28, s22, s17
	s_cselect_b32 s29, s23, s19
	s_add_u32 s26, s30, 0x8000
	s_addc_u32 s27, s31, 0
	s_add_i32 m0, s48, 0xc000
	ds_read_b128 v[198:201], v194
	ds_read_b128 v[202:205], v194 offset:1024
	ds_read_b128 v[206:209], v194 offset:2048
	ds_read_b128 v[210:213], v194 offset:3072
	ds_read_b128 v[214:217], v194 offset:4096
	ds_read_b128 v[218:221], v194 offset:5120
	ds_read_b128 v[222:225], v194 offset:6144
	ds_read_b128 v[226:229], v194 offset:7168
	global_load_lds_dwordx4 v184, s[24:25]
	s_add_i32 m0, s48, 0xe000
	s_nop 0
	global_load_lds_dwordx4 v182, s[24:25]
	s_waitcnt vmcnt(8)
	s_waitcnt lgkmcnt(0)
	s_setprio 1
	v_mfma_scale_f32_16x16x128_f8f6f4 v[158:161], v[18:25], v[198:205], v[158:161], v195, v195 op_sel_hi:[0,0,0]
	v_mfma_scale_f32_16x16x128_f8f6f4 v[154:157], v[26:33], v[198:205], v[154:157], v195, v195 op_sel_hi:[0,0,0]
	v_mfma_scale_f32_16x16x128_f8f6f4 v[142:145], v[18:25], v[206:213], v[142:145], v195, v195 op_sel_hi:[0,0,0]
	v_mfma_scale_f32_16x16x128_f8f6f4 v[138:141], v[26:33], v[206:213], v[138:141], v195, v195 op_sel_hi:[0,0,0]
	v_mfma_scale_f32_16x16x128_f8f6f4 v[126:129], v[18:25], v[214:221], v[126:129], v195, v195 op_sel_hi:[0,0,0]
	v_mfma_scale_f32_16x16x128_f8f6f4 v[122:125], v[26:33], v[214:221], v[122:125], v195, v195 op_sel_hi:[0,0,0]
	v_mfma_scale_f32_16x16x128_f8f6f4 v[110:113], v[18:25], v[222:229], v[110:113], v195, v195 op_sel_hi:[0,0,0]
	v_mfma_scale_f32_16x16x128_f8f6f4 v[106:109], v[26:33], v[222:229], v[106:109], v195, v195 op_sel_hi:[0,0,0]
	s_nop 3
	s_setprio 0
	s_setprio 1
	v_mfma_scale_f32_16x16x128_f8f6f4 v[150:153], v[2:9], v[198:205], v[150:153], v195, v195 op_sel_hi:[0,0,0]
	v_mfma_scale_f32_16x16x128_f8f6f4 v[146:149], v[10:17], v[198:205], v[146:149], v195, v195 op_sel_hi:[0,0,0]
	v_mfma_scale_f32_16x16x128_f8f6f4 v[134:137], v[2:9], v[206:213], v[134:137], v195, v195 op_sel_hi:[0,0,0]
	v_mfma_scale_f32_16x16x128_f8f6f4 v[130:133], v[10:17], v[206:213], v[130:133], v195, v195 op_sel_hi:[0,0,0]
	v_mfma_scale_f32_16x16x128_f8f6f4 v[118:121], v[2:9], v[214:221], v[118:121], v195, v195 op_sel_hi:[0,0,0]
	v_mfma_scale_f32_16x16x128_f8f6f4 v[114:117], v[10:17], v[214:221], v[114:117], v195, v195 op_sel_hi:[0,0,0]
	v_mfma_scale_f32_16x16x128_f8f6f4 v[102:105], v[2:9], v[222:229], v[102:105], v195, v195 op_sel_hi:[0,0,0]
	v_mfma_scale_f32_16x16x128_f8f6f4 v[98:101], v[10:17], v[222:229], v[98:101], v195, v195 op_sel_hi:[0,0,0]
	s_setprio 0
	s_barrier
	s_add_i32 s75, s65, s47
	s_mov_b32 m0, s75
	ds_read_b128 v[198:201], v194 offset:16384
	ds_read_b128 v[202:205], v194 offset:17408
	ds_read_b128 v[206:209], v194 offset:18432
	ds_read_b128 v[210:213], v194 offset:19456
	ds_read_b128 v[214:217], v194 offset:20480
	ds_read_b128 v[218:221], v194 offset:21504
	ds_read_b128 v[222:225], v194 offset:22528
	ds_read_b128 v[226:229], v194 offset:23552
	global_load_lds_dwordx4 v164, s[28:29]
	s_add_i32 m0, s75, 0x2000
	s_add_i32 s75, s66, s47
	global_load_lds_dwordx4 v166, s[28:29]
	s_add_u32 s98, s28, s4
	s_addc_u32 s99, s29, s5
	s_mov_b32 m0, s75
	s_nop 0
	global_load_lds_dwordx4 v164, s[98:99]
	s_add_u32 s100, s28, s4
	s_addc_u32 s101, s29, s5
	s_add_i32 m0, s75, 0x2000
	s_nop 0
	global_load_lds_dwordx4 v166, s[100:101]
	s_mov_b32 m0, s48
	s_nop 0
	global_load_lds_dwordx4 v174, s[30:31]
	s_mov_b32 m0, s49
	s_nop 0
	global_load_lds_dwordx4 v176, s[30:31]
	s_waitcnt vmcnt(8)
	s_waitcnt lgkmcnt(0)
	s_setprio 1
	v_mfma_scale_f32_16x16x128_f8f6f4 v[94:97], v[18:25], v[198:205], v[94:97], v195, v195 op_sel_hi:[0,0,0]
	v_mfma_scale_f32_16x16x128_f8f6f4 v[90:93], v[26:33], v[198:205], v[90:93], v195, v195 op_sel_hi:[0,0,0]
	v_mfma_scale_f32_16x16x128_f8f6f4 v[78:81], v[18:25], v[206:213], v[78:81], v195, v195 op_sel_hi:[0,0,0]
	v_mfma_scale_f32_16x16x128_f8f6f4 v[74:77], v[26:33], v[206:213], v[74:77], v195, v195 op_sel_hi:[0,0,0]
	v_mfma_scale_f32_16x16x128_f8f6f4 v[62:65], v[18:25], v[214:221], v[62:65], v195, v195 op_sel_hi:[0,0,0]
	v_mfma_scale_f32_16x16x128_f8f6f4 v[58:61], v[26:33], v[214:221], v[58:61], v195, v195 op_sel_hi:[0,0,0]
	v_mfma_scale_f32_16x16x128_f8f6f4 v[46:49], v[18:25], v[222:229], v[46:49], v195, v195 op_sel_hi:[0,0,0]
	v_mfma_scale_f32_16x16x128_f8f6f4 v[42:45], v[26:33], v[222:229], v[42:45], v195, v195 op_sel_hi:[0,0,0]
	s_nop 3
	s_setprio 0
	s_setprio 1
	v_mfma_scale_f32_16x16x128_f8f6f4 v[86:89], v[2:9], v[198:205], v[86:89], v195, v195 op_sel_hi:[0,0,0]
	v_mfma_scale_f32_16x16x128_f8f6f4 v[82:85], v[10:17], v[198:205], v[82:85], v195, v195 op_sel_hi:[0,0,0]
	v_mfma_scale_f32_16x16x128_f8f6f4 v[70:73], v[2:9], v[206:213], v[70:73], v195, v195 op_sel_hi:[0,0,0]
	v_mfma_scale_f32_16x16x128_f8f6f4 v[66:69], v[10:17], v[206:213], v[66:69], v195, v195 op_sel_hi:[0,0,0]
	v_mfma_scale_f32_16x16x128_f8f6f4 v[54:57], v[2:9], v[214:221], v[54:57], v195, v195 op_sel_hi:[0,0,0]
	v_mfma_scale_f32_16x16x128_f8f6f4 v[50:53], v[10:17], v[214:221], v[50:53], v195, v195 op_sel_hi:[0,0,0]
	v_mfma_scale_f32_16x16x128_f8f6f4 v[38:41], v[2:9], v[222:229], v[38:41], v195, v195 op_sel_hi:[0,0,0]
	v_mfma_scale_f32_16x16x128_f8f6f4 v[34:37], v[10:17], v[222:229], v[34:37], v195, v195 op_sel_hi:[0,0,0]
	s_setprio 0
	s_barrier
; #define PG8_STAGE(bufoff, gbase, voff) do { _Pragma("unroll") for (int _i = 0; _i < 2; ++_i) \
;         __builtin_amdgcn_global_load_lds((const unsigned*)((const char*)(gbase) + (voff)[_i]), (PG8_LAS unsigned*)(lds + (bufoff) + ldsw + _i * 8192), 16, 0, 0); } while (0)
; #define PG8_WAIT_V(n) asm volatile("s_waitcnt vmcnt(" #n ")" ::: "memory")
; #define PG8_WAIT_L(n) asm volatile("s_waitcnt lgkmcnt(" #n ")" ::: "memory")
; #define PG8_BAR __builtin_amdgcn_s_barrier()
; #define PG8_SCHED __builtin_amdgcn_sched_barrier(0)
; template <class Epi, class Sched, bool ALIGN_EPI = true, bool F8 = false>
; __device__ __forceinline__ void gemm_phase(PG8_LAS unsigned char* lds, const Sched& S, const Epi& E) {
;     ...
;         for (int t = 0; t < nt; t += 2) {
;     ...
;             PG8_LDB(B0, 1, 0); PG8_LDB(B1, 1, 1); PG8_SCHED; PG8_LDA(At, 1, 0); PG8_STAGE(PG8_SA(0, 1), a2, vA2[1]);
;             PG8_WAIT_V(8); PG8_WAIT_L(0); PG8_BAR; PG8_MMA(0, 0, At, B0); PG8_MMA(0, 1, At, B1); PG8_BAR; PG8_SCHED;
;             PG8_LDA(At, 1, 1); PG8_STAGE(PG8_SB(1, 0), b3, voffB[0]); PG8_STAGE(PG8_SB(1, 1), b3, voffB[1]); PG8_STAGE(PG8_SA(1, 0), a3, vA2[0]);
;             PG8_WAIT_V(8); PG8_WAIT_L(0); PG8_BAR; PG8_MMA(1, 0, At, B0); PG8_MMA(1, 1, At, B1); PG8_BAR; PG8_SCHED;
	s_add_i32 s75, 0, 0x18000
	s_add_i32 s76, 0, 0x1c000
	v_add_u32_e32 v14, s75, v191
	v_add_u32_e32 v30, s76, v191
	ds_read_b128 v[2:5], v14
	ds_read_b128 v[6:9], v14 offset:1024
	ds_read_b128 v[10:13], v14 offset:2048
	ds_read_b128 v[14:17], v14 offset:3072
	ds_read_b128 v[18:21], v30
	ds_read_b128 v[22:25], v30 offset:1024
	ds_read_b128 v[26:29], v30 offset:2048
	ds_read_b128 v[30:33], v30 offset:3072
	s_mov_b32 m0, s50
	ds_read_b128 v[198:201], v194 offset:32768
	ds_read_b128 v[202:205], v194 offset:33792
	ds_read_b128 v[206:209], v194 offset:34816
	ds_read_b128 v[210:213], v194 offset:35840
	ds_read_b128 v[214:217], v194 offset:36864
	ds_read_b128 v[218:221], v194 offset:37888
	ds_read_b128 v[222:225], v194 offset:38912
	ds_read_b128 v[226:229], v194 offset:39936
	global_load_lds_dwordx4 v178, s[30:31]
	s_mov_b32 m0, s51
	s_nop 0
	global_load_lds_dwordx4 v180, s[30:31]
	s_waitcnt vmcnt(8)
	s_waitcnt lgkmcnt(0)
	s_setprio 1
	v_mfma_scale_f32_16x16x128_f8f6f4 v[158:161], v[2:9], v[198:205], v[158:161], v195, v195 op_sel_hi:[0,0,0]
	v_mfma_scale_f32_16x16x128_f8f6f4 v[154:157], v[10:17], v[198:205], v[154:157], v195, v195 op_sel_hi:[0,0,0]
	v_mfma_scale_f32_16x16x128_f8f6f4 v[142:145], v[2:9], v[206:213], v[142:145], v195, v195 op_sel_hi:[0,0,0]
	v_mfma_scale_f32_16x16x128_f8f6f4 v[138:141], v[10:17], v[206:213], v[138:141], v195, v195 op_sel_hi:[0,0,0]
	v_mfma_scale_f32_16x16x128_f8f6f4 v[126:129], v[2:9], v[214:221], v[126:129], v195, v195 op_sel_hi:[0,0,0]
	v_mfma_scale_f32_16x16x128_f8f6f4 v[122:125], v[10:17], v[214:221], v[122:125], v195, v195 op_sel_hi:[0,0,0]
	v_mfma_scale_f32_16x16x128_f8f6f4 v[110:113], v[2:9], v[222:229], v[110:113], v195, v195 op_sel_hi:[0,0,0]
	v_mfma_scale_f32_16x16x128_f8f6f4 v[106:109], v[10:17], v[222:229], v[106:109], v195, v195 op_sel_hi:[0,0,0]
	s_nop 3
	s_setprio 0
	s_setprio 1
	v_mfma_scale_f32_16x16x128_f8f6f4 v[150:153], v[18:25], v[198:205], v[150:153], v195, v195 op_sel_hi:[0,0,0]
	v_mfma_scale_f32_16x16x128_f8f6f4 v[146:149], v[26:33], v[198:205], v[146:149], v195, v195 op_sel_hi:[0,0,0]
	v_mfma_scale_f32_16x16x128_f8f6f4 v[134:137], v[18:25], v[206:213], v[134:137], v195, v195 op_sel_hi:[0,0,0]
	v_mfma_scale_f32_16x16x128_f8f6f4 v[130:133], v[26:33], v[206:213], v[130:133], v195, v195 op_sel_hi:[0,0,0]
	v_mfma_scale_f32_16x16x128_f8f6f4 v[118:121], v[18:25], v[214:221], v[118:121], v195, v195 op_sel_hi:[0,0,0]
	v_mfma_scale_f32_16x16x128_f8f6f4 v[114:117], v[26:33], v[214:221], v[114:117], v195, v195 op_sel_hi:[0,0,0]
	v_mfma_scale_f32_16x16x128_f8f6f4 v[102:105], v[18:25], v[222:229], v[102:105], v195, v195 op_sel_hi:[0,0,0]
	v_mfma_scale_f32_16x16x128_f8f6f4 v[98:101], v[26:33], v[222:229], v[98:101], v195, v195 op_sel_hi:[0,0,0]
	s_setprio 0
	s_barrier
	s_add_u32 s28, s28, 0x8000
	s_addc_u32 s29, s29, 0
	s_add_i32 s30, s75, s47
	s_mov_b32 m0, s30
	ds_read_b128 v[198:201], v194 offset:49152
	ds_read_b128 v[202:205], v194 offset:50176
	ds_read_b128 v[206:209], v194 offset:51200
	ds_read_b128 v[210:213], v194 offset:52224
	ds_read_b128 v[214:217], v194 offset:53248
	ds_read_b128 v[218:221], v194 offset:54272
	ds_read_b128 v[222:225], v194 offset:55296
	ds_read_b128 v[226:229], v194 offset:56320
	global_load_lds_dwordx4 v164, s[28:29]
	s_add_i32 m0, s30, 0x2000
	s_add_i32 s30, s76, s47
	global_load_lds_dwordx4 v166, s[28:29]
	s_mov_b32 m0, s30
	s_nop 0
	global_load_lds_dwordx4 v168, s[28:29]
	s_add_i32 m0, s30, 0x2000
	s_nop 0
	global_load_lds_dwordx4 v172, s[28:29]
	s_mov_b32 m0, s60
	s_nop 0
	global_load_lds_dwordx4 v174, s[26:27]
	s_mov_b32 m0, s61
	s_nop 0
	global_load_lds_dwordx4 v176, s[26:27]
	s_waitcnt vmcnt(8)
	s_waitcnt lgkmcnt(0)
	s_setprio 1
	v_mfma_scale_f32_16x16x128_f8f6f4 v[94:97], v[2:9], v[198:205], v[94:97], v195, v195 op_sel_hi:[0,0,0]
	v_mfma_scale_f32_16x16x128_f8f6f4 v[90:93], v[10:17], v[198:205], v[90:93], v195, v195 op_sel_hi:[0,0,0]
	v_mfma_scale_f32_16x16x128_f8f6f4 v[78:81], v[2:9], v[206:213], v[78:81], v195, v195 op_sel_hi:[0,0,0]
	v_mfma_scale_f32_16x16x128_f8f6f4 v[74:77], v[10:17], v[206:213], v[74:77], v195, v195 op_sel_hi:[0,0,0]
	v_mfma_scale_f32_16x16x128_f8f6f4 v[62:65], v[2:9], v[214:221], v[62:65], v195, v195 op_sel_hi:[0,0,0]
	v_mfma_scale_f32_16x16x128_f8f6f4 v[58:61], v[10:17], v[214:221], v[58:61], v195, v195 op_sel_hi:[0,0,0]
	v_mfma_scale_f32_16x16x128_f8f6f4 v[46:49], v[2:9], v[222:229], v[46:49], v195, v195 op_sel_hi:[0,0,0]
	v_mfma_scale_f32_16x16x128_f8f6f4 v[42:45], v[10:17], v[222:229], v[42:45], v195, v195 op_sel_hi:[0,0,0]
	s_nop 3
	s_setprio 0
	s_setprio 1
	v_mfma_scale_f32_16x16x128_f8f6f4 v[86:89], v[18:25], v[198:205], v[86:89], v195, v195 op_sel_hi:[0,0,0]
	v_mfma_scale_f32_16x16x128_f8f6f4 v[82:85], v[26:33], v[198:205], v[82:85], v195, v195 op_sel_hi:[0,0,0]
	v_mfma_scale_f32_16x16x128_f8f6f4 v[70:73], v[18:25], v[206:213], v[70:73], v195, v195 op_sel_hi:[0,0,0]
	v_mfma_scale_f32_16x16x128_f8f6f4 v[66:69], v[26:33], v[206:213], v[66:69], v195, v195 op_sel_hi:[0,0,0]
	v_mfma_scale_f32_16x16x128_f8f6f4 v[54:57], v[18:25], v[214:221], v[54:57], v195, v195 op_sel_hi:[0,0,0]
	v_mfma_scale_f32_16x16x128_f8f6f4 v[50:53], v[26:33], v[214:221], v[50:53], v195, v195 op_sel_hi:[0,0,0]
	v_mfma_scale_f32_16x16x128_f8f6f4 v[38:41], v[18:25], v[222:229], v[38:41], v195, v195 op_sel_hi:[0,0,0]
	v_mfma_scale_f32_16x16x128_f8f6f4 v[34:37], v[26:33], v[222:229], v[34:37], v195, v195 op_sel_hi:[0,0,0]
	s_setprio 0
	s_barrier
	s_add_i32 s74, s74, 2
	s_add_u32 s17, s17, 0x10000
	s_addc_u32 s19, s19, 0
	s_add_u32 s24, s24, 0x10000
	s_addc_u32 s25, s25, 0
	s_cmp_gt_u32 s74, 13
	s_cbranch_scc0 .LBB0_428
	s_branch .Lfx_11141
; #define PG8_STAGE(bufoff, gbase, voff) do { _Pragma("unroll") for (int _i = 0; _i < 2; ++_i) \
;         __builtin_amdgcn_global_load_lds((const unsigned*)((const char*)(gbase) + (voff)[_i]), (PG8_LAS unsigned*)(lds + (bufoff) + ldsw + _i * 8192), 16, 0, 0); } while (0)
; #define PG8_WAIT_V(n) asm volatile("s_waitcnt vmcnt(" #n ")" ::: "memory")
; #define PG8_WAIT_L(n) asm volatile("s_waitcnt lgkmcnt(" #n ")" ::: "memory")
; #define PG8_BAR __builtin_amdgcn_s_barrier()
; #define PG8_SCHED __builtin_amdgcn_sched_barrier(0)
; template <class Epi, class Sched, bool ALIGN_EPI = true, bool F8 = false>
; __device__ __forceinline__ void gemm_phase(PG8_LAS unsigned char* lds, const Sched& S, const Epi& E) {
;     ...
;             PG8_LDB(B0, 0, 0); PG8_LDB(B1, 0, 1); PG8_SCHED; PG8_LDA(At, 0, 0); PG8_STAGE(PG8_SA(1, 1), a1, voffA[1]);
;             PG8_WAIT_V(8); PG8_WAIT_L(0); PG8_BAR; PG8_MMA(0, 0, At, B0); PG8_MMA(0, 1, At, B1); PG8_BAR; PG8_SCHED;
;             PG8_LDA(At, 0, 1); PG8_STAGE(PG8_SB(0, 0), b2, voffB[0]); PG8_STAGE(PG8_SB(0, 1), b2, voffB[1]); PG8_STAGE(PG8_SA(0, 0), a2, vA2[0]);
;             PG8_WAIT_V(8); PG8_WAIT_L(0); PG8_BAR; PG8_MMA(1, 0, At, B0); PG8_MMA(1, 1, At, B1); PG8_BAR; PG8_SCHED;
;             PG8_LDB(B0, 1, 0); PG8_LDB(B1, 1, 1); PG8_SCHED; PG8_LDA(At, 1, 0); PG8_STAGE(PG8_SA(0, 1), a2, vA2[1]);
;             PG8_WAIT_V(8); PG8_WAIT_L(0); PG8_BAR; PG8_MMA(0, 0, At, B0); PG8_MMA(0, 1, At, B1); PG8_BAR; PG8_SCHED;
.Lh1e_11141:
.Lh1_428:
	ds_read_b128 v[18:21], v192
	ds_read_b128 v[22:25], v192 offset:1024
	ds_read_b128 v[26:29], v192 offset:2048
	ds_read_b128 v[30:33], v192 offset:3072
	ds_read_b128 v[2:5], v193
	ds_read_b128 v[6:9], v193 offset:1024
	ds_read_b128 v[10:13], v193 offset:2048
	ds_read_b128 v[14:17], v193 offset:3072
	s_add_u32 s26, s24, 0x8000
	s_addc_u32 s27, s25, 0
	s_cmp_eq_u32 s74, 12
	s_cselect_b32 s30, s20, s26
	s_cselect_b32 s31, s21, s27
	s_cselect_b32 s28, s22, s17
	s_cselect_b32 s29, s23, s19
	s_add_u32 s26, s30, 0x8000
	s_addc_u32 s27, s31, 0
	s_add_i32 m0, s48, 0xc000
	ds_read_b128 v[198:201], v194
	ds_read_b128 v[202:205], v194 offset:1024
	ds_read_b128 v[206:209], v194 offset:2048
	ds_read_b128 v[210:213], v194 offset:3072
	ds_read_b128 v[214:217], v194 offset:4096
	ds_read_b128 v[218:221], v194 offset:5120
	ds_read_b128 v[222:225], v194 offset:6144
	ds_read_b128 v[226:229], v194 offset:7168
	global_load_lds_dwordx4 v184, s[24:25]
	s_add_i32 m0, s48, 0xe000
	s_nop 0
	global_load_lds_dwordx4 v182, s[24:25]
	s_waitcnt vmcnt(8)
	s_waitcnt lgkmcnt(0)
	s_barrier
	s_setprio 2
	v_mfma_scale_f32_16x16x128_f8f6f4 v[158:161], v[18:25], v[198:205], v[158:161], v195, v195 op_sel_hi:[0,0,0]
	v_mfma_scale_f32_16x16x128_f8f6f4 v[154:157], v[26:33], v[198:205], v[154:157], v195, v195 op_sel_hi:[0,0,0]
	v_mfma_scale_f32_16x16x128_f8f6f4 v[142:145], v[18:25], v[206:213], v[142:145], v195, v195 op_sel_hi:[0,0,0]
	v_mfma_scale_f32_16x16x128_f8f6f4 v[138:141], v[26:33], v[206:213], v[138:141], v195, v195 op_sel_hi:[0,0,0]
	v_mfma_scale_f32_16x16x128_f8f6f4 v[126:129], v[18:25], v[214:221], v[126:129], v195, v195 op_sel_hi:[0,0,0]
	v_mfma_scale_f32_16x16x128_f8f6f4 v[122:125], v[26:33], v[214:221], v[122:125], v195, v195 op_sel_hi:[0,0,0]
	v_mfma_scale_f32_16x16x128_f8f6f4 v[110:113], v[18:25], v[222:229], v[110:113], v195, v195 op_sel_hi:[0,0,0]
	v_mfma_scale_f32_16x16x128_f8f6f4 v[106:109], v[26:33], v[222:229], v[106:109], v195, v195 op_sel_hi:[0,0,0]
	s_nop 3
	s_setprio 0
	s_setprio 2
	v_mfma_scale_f32_16x16x128_f8f6f4 v[150:153], v[2:9], v[198:205], v[150:153], v195, v195 op_sel_hi:[0,0,0]
	v_mfma_scale_f32_16x16x128_f8f6f4 v[146:149], v[10:17], v[198:205], v[146:149], v195, v195 op_sel_hi:[0,0,0]
	v_mfma_scale_f32_16x16x128_f8f6f4 v[134:137], v[2:9], v[206:213], v[134:137], v195, v195 op_sel_hi:[0,0,0]
	v_mfma_scale_f32_16x16x128_f8f6f4 v[130:133], v[10:17], v[206:213], v[130:133], v195, v195 op_sel_hi:[0,0,0]
	v_mfma_scale_f32_16x16x128_f8f6f4 v[118:121], v[2:9], v[214:221], v[118:121], v195, v195 op_sel_hi:[0,0,0]
	v_mfma_scale_f32_16x16x128_f8f6f4 v[114:117], v[10:17], v[214:221], v[114:117], v195, v195 op_sel_hi:[0,0,0]
	v_mfma_scale_f32_16x16x128_f8f6f4 v[102:105], v[2:9], v[222:229], v[102:105], v195, v195 op_sel_hi:[0,0,0]
	v_mfma_scale_f32_16x16x128_f8f6f4 v[98:101], v[10:17], v[222:229], v[98:101], v195, v195 op_sel_hi:[0,0,0]
	s_setprio 0
	s_add_i32 s75, s65, s47
	s_mov_b32 m0, s75
	ds_read_b128 v[198:201], v194 offset:16384
	ds_read_b128 v[202:205], v194 offset:17408
	ds_read_b128 v[206:209], v194 offset:18432
	ds_read_b128 v[210:213], v194 offset:19456
	ds_read_b128 v[214:217], v194 offset:20480
	ds_read_b128 v[218:221], v194 offset:21504
	ds_read_b128 v[222:225], v194 offset:22528
	ds_read_b128 v[226:229], v194 offset:23552
	global_load_lds_dwordx4 v164, s[28:29]
	s_add_i32 m0, s75, 0x2000
	s_add_i32 s75, s66, s47
	global_load_lds_dwordx4 v166, s[28:29]
	s_add_u32 s98, s28, s4
	s_addc_u32 s99, s29, s5
	s_mov_b32 m0, s75
	s_nop 0
	global_load_lds_dwordx4 v164, s[98:99]
	s_add_u32 s100, s28, s4
	s_addc_u32 s101, s29, s5
	s_add_i32 m0, s75, 0x2000
	s_nop 0
	global_load_lds_dwordx4 v166, s[100:101]
	s_mov_b32 m0, s48
	s_nop 0
	global_load_lds_dwordx4 v174, s[30:31]
	s_mov_b32 m0, s49
	s_nop 0
	global_load_lds_dwordx4 v176, s[30:31]
	s_waitcnt vmcnt(8)
	s_waitcnt lgkmcnt(0)
	s_barrier
	s_setprio 2
	v_mfma_scale_f32_16x16x128_f8f6f4 v[94:97], v[18:25], v[198:205], v[94:97], v195, v195 op_sel_hi:[0,0,0]
	v_mfma_scale_f32_16x16x128_f8f6f4 v[90:93], v[26:33], v[198:205], v[90:93], v195, v195 op_sel_hi:[0,0,0]
	v_mfma_scale_f32_16x16x128_f8f6f4 v[78:81], v[18:25], v[206:213], v[78:81], v195, v195 op_sel_hi:[0,0,0]
	v_mfma_scale_f32_16x16x128_f8f6f4 v[74:77], v[26:33], v[206:213], v[74:77], v195, v195 op_sel_hi:[0,0,0]
	v_mfma_scale_f32_16x16x128_f8f6f4 v[62:65], v[18:25], v[214:221], v[62:65], v195, v195 op_sel_hi:[0,0,0]
	v_mfma_scale_f32_16x16x128_f8f6f4 v[58:61], v[26:33], v[214:221], v[58:61], v195, v195 op_sel_hi:[0,0,0]
	v_mfma_scale_f32_16x16x128_f8f6f4 v[46:49], v[18:25], v[222:229], v[46:49], v195, v195 op_sel_hi:[0,0,0]
	v_mfma_scale_f32_16x16x128_f8f6f4 v[42:45], v[26:33], v[222:229], v[42:45], v195, v195 op_sel_hi:[0,0,0]
	s_nop 3
	s_setprio 0
	s_setprio 2
	v_mfma_scale_f32_16x16x128_f8f6f4 v[86:89], v[2:9], v[198:205], v[86:89], v195, v195 op_sel_hi:[0,0,0]
	v_mfma_scale_f32_16x16x128_f8f6f4 v[82:85], v[10:17], v[198:205], v[82:85], v195, v195 op_sel_hi:[0,0,0]
	v_mfma_scale_f32_16x16x128_f8f6f4 v[70:73], v[2:9], v[206:213], v[70:73], v195, v195 op_sel_hi:[0,0,0]
	v_mfma_scale_f32_16x16x128_f8f6f4 v[66:69], v[10:17], v[206:213], v[66:69], v195, v195 op_sel_hi:[0,0,0]
	v_mfma_scale_f32_16x16x128_f8f6f4 v[54:57], v[2:9], v[214:221], v[54:57], v195, v195 op_sel_hi:[0,0,0]
	v_mfma_scale_f32_16x16x128_f8f6f4 v[50:53], v[10:17], v[214:221], v[50:53], v195, v195 op_sel_hi:[0,0,0]
	v_mfma_scale_f32_16x16x128_f8f6f4 v[38:41], v[2:9], v[222:229], v[38:41], v195, v195 op_sel_hi:[0,0,0]
	v_mfma_scale_f32_16x16x128_f8f6f4 v[34:37], v[10:17], v[222:229], v[34:37], v195, v195 op_sel_hi:[0,0,0]
	s_setprio 0
	s_add_i32 s75, 0, 0x18000
	s_add_i32 s76, 0, 0x1c000
	v_add_u32_e32 v14, s75, v191
	v_add_u32_e32 v30, s76, v191
	ds_read_b128 v[2:5], v14
	ds_read_b128 v[6:9], v14 offset:1024
	ds_read_b128 v[10:13], v14 offset:2048
	ds_read_b128 v[14:17], v14 offset:3072
	ds_read_b128 v[18:21], v30
	ds_read_b128 v[22:25], v30 offset:1024
	ds_read_b128 v[26:29], v30 offset:2048
	ds_read_b128 v[30:33], v30 offset:3072
	s_mov_b32 m0, s50
	ds_read_b128 v[198:201], v194 offset:32768
	ds_read_b128 v[202:205], v194 offset:33792
	ds_read_b128 v[206:209], v194 offset:34816
	ds_read_b128 v[210:213], v194 offset:35840
	ds_read_b128 v[214:217], v194 offset:36864
	ds_read_b128 v[218:221], v194 offset:37888
	ds_read_b128 v[222:225], v194 offset:38912
	ds_read_b128 v[226:229], v194 offset:39936
	global_load_lds_dwordx4 v178, s[30:31]
	s_mov_b32 m0, s51
	s_nop 0
	global_load_lds_dwordx4 v180, s[30:31]
	s_waitcnt vmcnt(8)
	s_waitcnt lgkmcnt(0)
	s_barrier
; #define PG8_STAGE(bufoff, gbase, voff) do { _Pragma("unroll") for (int _i = 0; _i < 2; ++_i) \
;         __builtin_amdgcn_global_load_lds((const unsigned*)((const char*)(gbase) + (voff)[_i]), (PG8_LAS unsigned*)(lds + (bufoff) + ldsw + _i * 8192), 16, 0, 0); } while (0)
; #define PG8_WAIT_V(n) asm volatile("s_waitcnt vmcnt(" #n ")" ::: "memory")
; #define PG8_WAIT_L(n) asm volatile("s_waitcnt lgkmcnt(" #n ")" ::: "memory")
; #define PG8_BAR __builtin_amdgcn_s_barrier()
; #define PG8_SCHED __builtin_amdgcn_sched_barrier(0)
; template <class Epi, class Sched, bool ALIGN_EPI = true, bool F8 = false>
; __device__ __forceinline__ void gemm_phase(PG8_LAS unsigned char* lds, const Sched& S, const Epi& E) {
;     ...
;         for (int t = 0; t < nt; t += 2) {
;     ...
;             PG8_WAIT_V(8); PG8_WAIT_L(0); PG8_BAR; PG8_MMA(0, 0, At, B0); PG8_MMA(0, 1, At, B1); PG8_BAR; PG8_SCHED;
;             PG8_LDA(At, 1, 1); PG8_STAGE(PG8_SB(1, 0), b3, voffB[0]); PG8_STAGE(PG8_SB(1, 1), b3, voffB[1]); PG8_STAGE(PG8_SA(1, 0), a3, vA2[0]);
;             PG8_WAIT_V(8); PG8_WAIT_L(0); PG8_BAR; PG8_MMA(1, 0, At, B0); PG8_MMA(1, 1, At, B1); PG8_BAR; PG8_SCHED;
	s_setprio 2
	v_mfma_scale_f32_16x16x128_f8f6f4 v[158:161], v[2:9], v[198:205], v[158:161], v195, v195 op_sel_hi:[0,0,0]
	v_mfma_scale_f32_16x16x128_f8f6f4 v[154:157], v[10:17], v[198:205], v[154:157], v195, v195 op_sel_hi:[0,0,0]
	v_mfma_scale_f32_16x16x128_f8f6f4 v[142:145], v[2:9], v[206:213], v[142:145], v195, v195 op_sel_hi:[0,0,0]
	v_mfma_scale_f32_16x16x128_f8f6f4 v[138:141], v[10:17], v[206:213], v[138:141], v195, v195 op_sel_hi:[0,0,0]
	v_mfma_scale_f32_16x16x128_f8f6f4 v[126:129], v[2:9], v[214:221], v[126:129], v195, v195 op_sel_hi:[0,0,0]
	v_mfma_scale_f32_16x16x128_f8f6f4 v[122:125], v[10:17], v[214:221], v[122:125], v195, v195 op_sel_hi:[0,0,0]
	v_mfma_scale_f32_16x16x128_f8f6f4 v[110:113], v[2:9], v[222:229], v[110:113], v195, v195 op_sel_hi:[0,0,0]
	v_mfma_scale_f32_16x16x128_f8f6f4 v[106:109], v[10:17], v[222:229], v[106:109], v195, v195 op_sel_hi:[0,0,0]
	s_nop 3
	s_setprio 0
	s_setprio 2
	v_mfma_scale_f32_16x16x128_f8f6f4 v[150:153], v[18:25], v[198:205], v[150:153], v195, v195 op_sel_hi:[0,0,0]
	v_mfma_scale_f32_16x16x128_f8f6f4 v[146:149], v[26:33], v[198:205], v[146:149], v195, v195 op_sel_hi:[0,0,0]
	v_mfma_scale_f32_16x16x128_f8f6f4 v[134:137], v[18:25], v[206:213], v[134:137], v195, v195 op_sel_hi:[0,0,0]
	v_mfma_scale_f32_16x16x128_f8f6f4 v[130:133], v[26:33], v[206:213], v[130:133], v195, v195 op_sel_hi:[0,0,0]
	v_mfma_scale_f32_16x16x128_f8f6f4 v[118:121], v[18:25], v[214:221], v[118:121], v195, v195 op_sel_hi:[0,0,0]
	v_mfma_scale_f32_16x16x128_f8f6f4 v[114:117], v[26:33], v[214:221], v[114:117], v195, v195 op_sel_hi:[0,0,0]
	v_mfma_scale_f32_16x16x128_f8f6f4 v[102:105], v[18:25], v[222:229], v[102:105], v195, v195 op_sel_hi:[0,0,0]
	v_mfma_scale_f32_16x16x128_f8f6f4 v[98:101], v[26:33], v[222:229], v[98:101], v195, v195 op_sel_hi:[0,0,0]
	s_setprio 0
	s_add_u32 s28, s28, 0x8000
	s_addc_u32 s29, s29, 0
	s_add_i32 s30, s75, s47
	s_mov_b32 m0, s30
	ds_read_b128 v[198:201], v194 offset:49152
	ds_read_b128 v[202:205], v194 offset:50176
	ds_read_b128 v[206:209], v194 offset:51200
	ds_read_b128 v[210:213], v194 offset:52224
	ds_read_b128 v[214:217], v194 offset:53248
	ds_read_b128 v[218:221], v194 offset:54272
	ds_read_b128 v[222:225], v194 offset:55296
	ds_read_b128 v[226:229], v194 offset:56320
	global_load_lds_dwordx4 v164, s[28:29]
	s_add_i32 m0, s30, 0x2000
	s_add_i32 s30, s76, s47
	global_load_lds_dwordx4 v166, s[28:29]
	s_mov_b32 m0, s30
	s_nop 0
	global_load_lds_dwordx4 v168, s[28:29]
	s_add_i32 m0, s30, 0x2000
	s_nop 0
	global_load_lds_dwordx4 v172, s[28:29]
	s_mov_b32 m0, s60
	s_nop 0
	global_load_lds_dwordx4 v174, s[26:27]
	s_mov_b32 m0, s61
	s_nop 0
	global_load_lds_dwordx4 v176, s[26:27]
	s_waitcnt vmcnt(8)
	s_waitcnt lgkmcnt(0)
	s_barrier
	s_setprio 2
	v_mfma_scale_f32_16x16x128_f8f6f4 v[94:97], v[2:9], v[198:205], v[94:97], v195, v195 op_sel_hi:[0,0,0]
	v_mfma_scale_f32_16x16x128_f8f6f4 v[90:93], v[10:17], v[198:205], v[90:93], v195, v195 op_sel_hi:[0,0,0]
	v_mfma_scale_f32_16x16x128_f8f6f4 v[78:81], v[2:9], v[206:213], v[78:81], v195, v195 op_sel_hi:[0,0,0]
	v_mfma_scale_f32_16x16x128_f8f6f4 v[74:77], v[10:17], v[206:213], v[74:77], v195, v195 op_sel_hi:[0,0,0]
	v_mfma_scale_f32_16x16x128_f8f6f4 v[62:65], v[2:9], v[214:221], v[62:65], v195, v195 op_sel_hi:[0,0,0]
	v_mfma_scale_f32_16x16x128_f8f6f4 v[58:61], v[10:17], v[214:221], v[58:61], v195, v195 op_sel_hi:[0,0,0]
	v_mfma_scale_f32_16x16x128_f8f6f4 v[46:49], v[2:9], v[222:229], v[46:49], v195, v195 op_sel_hi:[0,0,0]
	v_mfma_scale_f32_16x16x128_f8f6f4 v[42:45], v[10:17], v[222:229], v[42:45], v195, v195 op_sel_hi:[0,0,0]
	s_nop 3
	s_setprio 0
	s_setprio 2
	v_mfma_scale_f32_16x16x128_f8f6f4 v[86:89], v[18:25], v[198:205], v[86:89], v195, v195 op_sel_hi:[0,0,0]
	v_mfma_scale_f32_16x16x128_f8f6f4 v[82:85], v[26:33], v[198:205], v[82:85], v195, v195 op_sel_hi:[0,0,0]
	v_mfma_scale_f32_16x16x128_f8f6f4 v[70:73], v[18:25], v[206:213], v[70:73], v195, v195 op_sel_hi:[0,0,0]
	v_mfma_scale_f32_16x16x128_f8f6f4 v[66:69], v[26:33], v[206:213], v[66:69], v195, v195 op_sel_hi:[0,0,0]
	v_mfma_scale_f32_16x16x128_f8f6f4 v[54:57], v[18:25], v[214:221], v[54:57], v195, v195 op_sel_hi:[0,0,0]
	v_mfma_scale_f32_16x16x128_f8f6f4 v[50:53], v[26:33], v[214:221], v[50:53], v195, v195 op_sel_hi:[0,0,0]
	v_mfma_scale_f32_16x16x128_f8f6f4 v[38:41], v[18:25], v[222:229], v[38:41], v195, v195 op_sel_hi:[0,0,0]
	v_mfma_scale_f32_16x16x128_f8f6f4 v[34:37], v[26:33], v[222:229], v[34:37], v195, v195 op_sel_hi:[0,0,0]
	s_setprio 0
	s_add_i32 s74, s74, 2
	s_add_u32 s17, s17, 0x10000
	s_addc_u32 s19, s19, 0
	s_add_u32 s24, s24, 0x10000
	s_addc_u32 s25, s25, 0
	s_cmp_gt_u32 s74, 13
	s_cbranch_scc0 .Lh1_428

; #define PG8_STAGE(bufoff, gbase, voff) do { _Pragma("unroll") for (int _i = 0; _i < 2; ++_i) \
;         __builtin_amdgcn_global_load_lds((const unsigned*)((const char*)(gbase) + (voff)[_i]), (PG8_LAS unsigned*)(lds + (bufoff) + ldsw + _i * 8192), 16, 0, 0); } while (0)
; #define PG8_WAIT_V(n) asm volatile("s_waitcnt vmcnt(" #n ")" ::: "memory")
; #define PG8_WAIT_L(n) asm volatile("s_waitcnt lgkmcnt(" #n ")" ::: "memory")
; #define PG8_BAR __builtin_amdgcn_s_barrier()
; #define PG8_SCHED __builtin_amdgcn_sched_barrier(0)
; template <class Epi, class Sched, bool ALIGN_EPI = true, bool F8 = false>
; __device__ __forceinline__ void gemm_phase(PG8_LAS unsigned char* lds, const Sched& S, const Epi& E) {
;     ...
;         for (int t = 0; t < nt; t += 2) {
;             const bool last = (t == nt - 2);
;             if constexpr (Sched::GATHER) { if (last && has_next) S.a_off(nxt, Rs, Cs, voffAn); }
;             const char* a1 = cA + (size_t)(t + 1) * kstep;
;             const char* a2 = last ? nA : cA + (size_t)(t + 2) * kstep; const char* b2 = last ? nB : cB + (size_t)(t + 2) * kstepB;
;             const char* a3 = a2 + kstep; const char* b3 = b2 + kstepB;
;             unsigned vA2[2][2];
; #pragma unroll
;             for (int h = 0; h < 2; ++h)
; #pragma unroll
;                 for (int i = 0; i < 2; ++i) { if constexpr (Sched::GATHER) vA2[h][i] = (last && has_next) ? voffAn[h][i] : voffA[h][i]; else vA2[h][i] = voffA[h][i]; }
;             PG8_LDB(B0, 0, 0); PG8_LDB(B1, 0, 1); PG8_SCHED; PG8_LDA(At, 0, 0); PG8_STAGE(PG8_SA(1, 1), a1, voffA[1]);
;             PG8_WAIT_V(8); PG8_WAIT_L(0); PG8_BAR; PG8_MMA(0, 0, At, B0); PG8_MMA(0, 1, At, B1); PG8_BAR; PG8_SCHED;
;             PG8_LDA(At, 0, 1); PG8_STAGE(PG8_SB(0, 0), b2, voffB[0]); PG8_STAGE(PG8_SB(0, 1), b2, voffB[1]); PG8_STAGE(PG8_SA(0, 0), a2, vA2[0]);
;             PG8_WAIT_V(8); PG8_WAIT_L(0); PG8_BAR; PG8_MMA(1, 0, At, B0); PG8_MMA(1, 1, At, B1); PG8_BAR; PG8_SCHED;
.LBB0_834:
	v_add_u32_e32 v10, s58, v190
	ds_read_b128 v[2:5], v10
	ds_read_b128 v[6:9], v10 offset:1024
	ds_read_b128 v[142:145], v10 offset:2048
	ds_read_b128 v[146:149], v10 offset:3072
	v_add_u32_e32 v10, s59, v190
	ds_read_b128 v[150:153], v10
	ds_read_b128 v[154:157], v10 offset:1024
	ds_read_b128 v[202:205], v10 offset:2048
	ds_read_b128 v[206:209], v10 offset:3072
	s_add_i32 s77, s26, 2
	s_add_u32 s27, s24, 0x8000
	s_addc_u32 s28, s25, 0
	s_cmp_eq_u32 s74, s26
	s_cselect_b32 s30, s20, s27
	s_cselect_b32 s31, s21, s28
	s_cselect_b32 s28, s22, s75
	s_cselect_b32 s29, s23, s76
	s_add_u32 s26, s30, 0x8000
	s_addc_u32 s27, s31, 0
	s_add_i32 m0, s45, 0xc000
	ds_read_b128 v[210:213], v198
	ds_read_b128 v[214:217], v198 offset:1024
	ds_read_b128 v[218:221], v198 offset:2048
	ds_read_b128 v[222:225], v198 offset:3072
	ds_read_b128 v[226:229], v198 offset:4096
	ds_read_b128 v[230:233], v198 offset:5120
	ds_read_b128 v[234:237], v198 offset:6144
	ds_read_b128 v[238:241], v198 offset:7168
	global_load_lds_dwordx4 v182, s[24:25]
	s_add_i32 m0, s45, 0xe000
	s_nop 0
	global_load_lds_dwordx4 v180, s[24:25]
	s_waitcnt vmcnt(8)
	s_waitcnt lgkmcnt(0)
	s_setprio 1
	v_mfma_scale_f32_16x16x128_f8f6f4 v[138:141], v[2:9], v[210:217], v[138:141], v199, v199 op_sel_hi:[0,0,0]
	v_mfma_scale_f32_16x16x128_f8f6f4 v[134:137], v[142:149], v[210:217], v[134:137], v199, v199 op_sel_hi:[0,0,0]
	v_mfma_scale_f32_16x16x128_f8f6f4 v[130:133], v[2:9], v[218:225], v[130:133], v199, v199 op_sel_hi:[0,0,0]
	v_mfma_scale_f32_16x16x128_f8f6f4 v[126:129], v[142:149], v[218:225], v[126:129], v199, v199 op_sel_hi:[0,0,0]
	v_mfma_scale_f32_16x16x128_f8f6f4 v[122:125], v[2:9], v[226:233], v[122:125], v199, v199 op_sel_hi:[0,0,0]
	v_mfma_scale_f32_16x16x128_f8f6f4 v[118:121], v[142:149], v[226:233], v[118:121], v199, v199 op_sel_hi:[0,0,0]
	v_mfma_scale_f32_16x16x128_f8f6f4 v[114:117], v[2:9], v[234:241], v[114:117], v199, v199 op_sel_hi:[0,0,0]
	v_mfma_scale_f32_16x16x128_f8f6f4 v[110:113], v[142:149], v[234:241], v[110:113], v199, v199 op_sel_hi:[0,0,0]
	s_nop 3
	s_setprio 0
	s_setprio 1
	v_mfma_scale_f32_16x16x128_f8f6f4 v[106:109], v[150:157], v[210:217], v[106:109], v199, v199 op_sel_hi:[0,0,0]
	v_mfma_scale_f32_16x16x128_f8f6f4 v[102:105], v[202:209], v[210:217], v[102:105], v199, v199 op_sel_hi:[0,0,0]
	v_mfma_scale_f32_16x16x128_f8f6f4 v[98:101], v[150:157], v[218:225], v[98:101], v199, v199 op_sel_hi:[0,0,0]
	v_mfma_scale_f32_16x16x128_f8f6f4 v[94:97], v[202:209], v[218:225], v[94:97], v199, v199 op_sel_hi:[0,0,0]
	v_mfma_scale_f32_16x16x128_f8f6f4 v[90:93], v[150:157], v[226:233], v[90:93], v199, v199 op_sel_hi:[0,0,0]
	v_mfma_scale_f32_16x16x128_f8f6f4 v[86:89], v[202:209], v[226:233], v[86:89], v199, v199 op_sel_hi:[0,0,0]
	v_mfma_scale_f32_16x16x128_f8f6f4 v[82:85], v[150:157], v[234:241], v[82:85], v199, v199 op_sel_hi:[0,0,0]
	v_mfma_scale_f32_16x16x128_f8f6f4 v[78:81], v[202:209], v[234:241], v[78:81], v199, v199 op_sel_hi:[0,0,0]
	s_setprio 0
	s_barrier
	s_add_i32 s78, s58, s44
	s_mov_b32 m0, s78
	ds_read_b128 v[210:213], v198 offset:16384
	ds_read_b128 v[214:217], v198 offset:17408
	ds_read_b128 v[218:221], v198 offset:18432
	ds_read_b128 v[222:225], v198 offset:19456
	ds_read_b128 v[226:229], v198 offset:20480
	ds_read_b128 v[230:233], v198 offset:21504
	ds_read_b128 v[234:237], v198 offset:22528
	ds_read_b128 v[238:241], v198 offset:23552
	global_load_lds_dwordx4 v158, s[28:29]
	s_add_i32 m0, s78, 0x2000
	s_add_i32 s78, s59, s44
	global_load_lds_dwordx4 v160, s[28:29]
	s_add_u32 s98, s28, s8
	s_addc_u32 s99, s29, s9
	s_mov_b32 m0, s78
	s_nop 0
	global_load_lds_dwordx4 v158, s[98:99]
	s_add_u32 s100, s28, s8
	s_addc_u32 s101, s29, s9
	s_add_i32 m0, s78, 0x2000
	s_nop 0
	global_load_lds_dwordx4 v160, s[100:101]
	s_mov_b32 m0, s45
	s_nop 0
	global_load_lds_dwordx4 v162, s[30:31]
	s_mov_b32 m0, s46
	s_nop 0
	global_load_lds_dwordx4 v164, s[30:31]
	s_waitcnt vmcnt(8)
	s_waitcnt lgkmcnt(0)
	s_setprio 1
	v_mfma_scale_f32_16x16x128_f8f6f4 v[74:77], v[2:9], v[210:217], v[74:77], v199, v199 op_sel_hi:[0,0,0]
	v_mfma_scale_f32_16x16x128_f8f6f4 v[70:73], v[142:149], v[210:217], v[70:73], v199, v199 op_sel_hi:[0,0,0]
	v_mfma_scale_f32_16x16x128_f8f6f4 v[66:69], v[2:9], v[218:225], v[66:69], v199, v199 op_sel_hi:[0,0,0]
	v_mfma_scale_f32_16x16x128_f8f6f4 v[62:65], v[142:149], v[218:225], v[62:65], v199, v199 op_sel_hi:[0,0,0]
	v_mfma_scale_f32_16x16x128_f8f6f4 v[58:61], v[2:9], v[226:233], v[58:61], v199, v199 op_sel_hi:[0,0,0]
	v_mfma_scale_f32_16x16x128_f8f6f4 v[54:57], v[142:149], v[226:233], v[54:57], v199, v199 op_sel_hi:[0,0,0]
	v_mfma_scale_f32_16x16x128_f8f6f4 v[50:53], v[2:9], v[234:241], v[50:53], v199, v199 op_sel_hi:[0,0,0]
	v_mfma_scale_f32_16x16x128_f8f6f4 v[46:49], v[142:149], v[234:241], v[46:49], v199, v199 op_sel_hi:[0,0,0]
	s_nop 3
	s_setprio 0
	s_setprio 1
	v_mfma_scale_f32_16x16x128_f8f6f4 v[42:45], v[150:157], v[210:217], v[42:45], v199, v199 op_sel_hi:[0,0,0]
	v_mfma_scale_f32_16x16x128_f8f6f4 v[38:41], v[202:209], v[210:217], v[38:41], v199, v199 op_sel_hi:[0,0,0]
	v_mfma_scale_f32_16x16x128_f8f6f4 v[34:37], v[150:157], v[218:225], v[34:37], v199, v199 op_sel_hi:[0,0,0]
	v_mfma_scale_f32_16x16x128_f8f6f4 v[30:33], v[202:209], v[218:225], v[30:33], v199, v199 op_sel_hi:[0,0,0]
	v_mfma_scale_f32_16x16x128_f8f6f4 v[26:29], v[150:157], v[226:233], v[26:29], v199, v199 op_sel_hi:[0,0,0]
	v_mfma_scale_f32_16x16x128_f8f6f4 v[22:25], v[202:209], v[226:233], v[22:25], v199, v199 op_sel_hi:[0,0,0]
	v_mfma_scale_f32_16x16x128_f8f6f4 v[18:21], v[150:157], v[234:241], v[18:21], v199, v199 op_sel_hi:[0,0,0]
	v_mfma_scale_f32_16x16x128_f8f6f4 v[14:17], v[202:209], v[234:241], v[14:17], v199, v199 op_sel_hi:[0,0,0]
	s_setprio 0
	s_barrier
; #define PG8_STAGE(bufoff, gbase, voff) do { _Pragma("unroll") for (int _i = 0; _i < 2; ++_i) \
;         __builtin_amdgcn_global_load_lds((const unsigned*)((const char*)(gbase) + (voff)[_i]), (PG8_LAS unsigned*)(lds + (bufoff) + ldsw + _i * 8192), 16, 0, 0); } while (0)
; #define PG8_WAIT_V(n) asm volatile("s_waitcnt vmcnt(" #n ")" ::: "memory")
; #define PG8_WAIT_L(n) asm volatile("s_waitcnt lgkmcnt(" #n ")" ::: "memory")
; #define PG8_BAR __builtin_amdgcn_s_barrier()
; #define PG8_SCHED __builtin_amdgcn_sched_barrier(0)
; template <class Epi, class Sched, bool ALIGN_EPI = true, bool F8 = false>
; __device__ __forceinline__ void gemm_phase(PG8_LAS unsigned char* lds, const Sched& S, const Epi& E) {
;     ...
;         for (int t = 0; t < nt; t += 2) {
;     ...
;             PG8_LDB(B0, 1, 0); PG8_LDB(B1, 1, 1); PG8_SCHED; PG8_LDA(At, 1, 0); PG8_STAGE(PG8_SA(0, 1), a2, vA2[1]);
;             PG8_WAIT_V(8); PG8_WAIT_L(0); PG8_BAR; PG8_MMA(0, 0, At, B0); PG8_MMA(0, 1, At, B1); PG8_BAR; PG8_SCHED;
;             PG8_LDA(At, 1, 1); PG8_STAGE(PG8_SB(1, 0), b3, voffB[0]); PG8_STAGE(PG8_SB(1, 1), b3, voffB[1]); PG8_STAGE(PG8_SA(1, 0), a3, vA2[0]);
;             PG8_WAIT_V(8); PG8_WAIT_L(0); PG8_BAR; PG8_MMA(1, 0, At, B0); PG8_MMA(1, 1, At, B1); PG8_BAR; PG8_SCHED;
	s_add_i32 s78, 0, 0x18000
	s_add_i32 s79, 0, 0x1c000
	v_add_u32_e32 v2, s78, v190
	v_add_u32_e32 v10, s79, v190
	ds_read_b128 v[142:145], v2
	ds_read_b128 v[146:149], v2 offset:1024
	ds_read_b128 v[150:153], v2 offset:2048
	ds_read_b128 v[154:157], v2 offset:3072
	ds_read_b128 v[2:5], v10
	ds_read_b128 v[6:9], v10 offset:1024
	ds_read_b128 v[202:205], v10 offset:2048
	ds_read_b128 v[206:209], v10 offset:3072
	s_mov_b32 m0, s47
	ds_read_b128 v[210:213], v198 offset:32768
	ds_read_b128 v[214:217], v198 offset:33792
	ds_read_b128 v[218:221], v198 offset:34816
	ds_read_b128 v[222:225], v198 offset:35840
	ds_read_b128 v[226:229], v198 offset:36864
	ds_read_b128 v[230:233], v198 offset:37888
	ds_read_b128 v[234:237], v198 offset:38912
	ds_read_b128 v[238:241], v198 offset:39936
	global_load_lds_dwordx4 v166, s[30:31]
	s_mov_b32 m0, s48
	s_nop 0
	global_load_lds_dwordx4 v168, s[30:31]
	s_waitcnt vmcnt(8)
	s_waitcnt lgkmcnt(0)
	s_setprio 1
	v_mfma_scale_f32_16x16x128_f8f6f4 v[138:141], v[142:149], v[210:217], v[138:141], v199, v199 op_sel_hi:[0,0,0]
	v_mfma_scale_f32_16x16x128_f8f6f4 v[134:137], v[150:157], v[210:217], v[134:137], v199, v199 op_sel_hi:[0,0,0]
	v_mfma_scale_f32_16x16x128_f8f6f4 v[130:133], v[142:149], v[218:225], v[130:133], v199, v199 op_sel_hi:[0,0,0]
	v_mfma_scale_f32_16x16x128_f8f6f4 v[126:129], v[150:157], v[218:225], v[126:129], v199, v199 op_sel_hi:[0,0,0]
	v_mfma_scale_f32_16x16x128_f8f6f4 v[122:125], v[142:149], v[226:233], v[122:125], v199, v199 op_sel_hi:[0,0,0]
	v_mfma_scale_f32_16x16x128_f8f6f4 v[118:121], v[150:157], v[226:233], v[118:121], v199, v199 op_sel_hi:[0,0,0]
	v_mfma_scale_f32_16x16x128_f8f6f4 v[114:117], v[142:149], v[234:241], v[114:117], v199, v199 op_sel_hi:[0,0,0]
	v_mfma_scale_f32_16x16x128_f8f6f4 v[110:113], v[150:157], v[234:241], v[110:113], v199, v199 op_sel_hi:[0,0,0]
	s_nop 3
	s_setprio 0
	s_setprio 1
	v_mfma_scale_f32_16x16x128_f8f6f4 v[106:109], v[2:9], v[210:217], v[106:109], v199, v199 op_sel_hi:[0,0,0]
	v_mfma_scale_f32_16x16x128_f8f6f4 v[102:105], v[202:209], v[210:217], v[102:105], v199, v199 op_sel_hi:[0,0,0]
	v_mfma_scale_f32_16x16x128_f8f6f4 v[98:101], v[2:9], v[218:225], v[98:101], v199, v199 op_sel_hi:[0,0,0]
	v_mfma_scale_f32_16x16x128_f8f6f4 v[94:97], v[202:209], v[218:225], v[94:97], v199, v199 op_sel_hi:[0,0,0]
	v_mfma_scale_f32_16x16x128_f8f6f4 v[90:93], v[2:9], v[226:233], v[90:93], v199, v199 op_sel_hi:[0,0,0]
	v_mfma_scale_f32_16x16x128_f8f6f4 v[86:89], v[202:209], v[226:233], v[86:89], v199, v199 op_sel_hi:[0,0,0]
	v_mfma_scale_f32_16x16x128_f8f6f4 v[82:85], v[2:9], v[234:241], v[82:85], v199, v199 op_sel_hi:[0,0,0]
	v_mfma_scale_f32_16x16x128_f8f6f4 v[78:81], v[202:209], v[234:241], v[78:81], v199, v199 op_sel_hi:[0,0,0]
	s_setprio 0
	s_barrier
	s_add_u32 s28, s28, 0x8000
	s_addc_u32 s29, s29, 0
	s_add_i32 s30, s78, s44
	s_mov_b32 m0, s30
	ds_read_b128 v[210:213], v198 offset:49152
	ds_read_b128 v[214:217], v198 offset:50176
	ds_read_b128 v[218:221], v198 offset:51200
	ds_read_b128 v[222:225], v198 offset:52224
	ds_read_b128 v[226:229], v198 offset:53248
	ds_read_b128 v[230:233], v198 offset:54272
	ds_read_b128 v[234:237], v198 offset:55296
	ds_read_b128 v[238:241], v198 offset:56320
	global_load_lds_dwordx4 v158, s[28:29]
	s_add_i32 m0, s30, 0x2000
	s_add_i32 s30, s79, s44
	global_load_lds_dwordx4 v160, s[28:29]
	s_mov_b32 m0, s30
	s_nop 0
	global_load_lds_dwordx4 v172, s[28:29]
	s_add_i32 m0, s30, 0x2000
	s_nop 0
	global_load_lds_dwordx4 v174, s[28:29]
	s_mov_b32 m0, s50
	s_nop 0
	global_load_lds_dwordx4 v162, s[26:27]
	s_mov_b32 m0, s51
	s_nop 0
	global_load_lds_dwordx4 v164, s[26:27]
	s_waitcnt vmcnt(8)
	s_waitcnt lgkmcnt(0)
	s_setprio 1
	v_mfma_scale_f32_16x16x128_f8f6f4 v[74:77], v[142:149], v[210:217], v[74:77], v199, v199 op_sel_hi:[0,0,0]
	v_mfma_scale_f32_16x16x128_f8f6f4 v[70:73], v[150:157], v[210:217], v[70:73], v199, v199 op_sel_hi:[0,0,0]
	v_mfma_scale_f32_16x16x128_f8f6f4 v[66:69], v[142:149], v[218:225], v[66:69], v199, v199 op_sel_hi:[0,0,0]
	v_mfma_scale_f32_16x16x128_f8f6f4 v[62:65], v[150:157], v[218:225], v[62:65], v199, v199 op_sel_hi:[0,0,0]
	v_mfma_scale_f32_16x16x128_f8f6f4 v[58:61], v[142:149], v[226:233], v[58:61], v199, v199 op_sel_hi:[0,0,0]
	v_mfma_scale_f32_16x16x128_f8f6f4 v[54:57], v[150:157], v[226:233], v[54:57], v199, v199 op_sel_hi:[0,0,0]
	v_mfma_scale_f32_16x16x128_f8f6f4 v[50:53], v[142:149], v[234:241], v[50:53], v199, v199 op_sel_hi:[0,0,0]
	v_mfma_scale_f32_16x16x128_f8f6f4 v[46:49], v[150:157], v[234:241], v[46:49], v199, v199 op_sel_hi:[0,0,0]
	s_nop 3
	s_setprio 0
	s_setprio 1
	v_mfma_scale_f32_16x16x128_f8f6f4 v[42:45], v[2:9], v[210:217], v[42:45], v199, v199 op_sel_hi:[0,0,0]
	v_mfma_scale_f32_16x16x128_f8f6f4 v[38:41], v[202:209], v[210:217], v[38:41], v199, v199 op_sel_hi:[0,0,0]
	v_mfma_scale_f32_16x16x128_f8f6f4 v[34:37], v[2:9], v[218:225], v[34:37], v199, v199 op_sel_hi:[0,0,0]
	v_mfma_scale_f32_16x16x128_f8f6f4 v[30:33], v[202:209], v[218:225], v[30:33], v199, v199 op_sel_hi:[0,0,0]
	v_mfma_scale_f32_16x16x128_f8f6f4 v[26:29], v[2:9], v[226:233], v[26:29], v199, v199 op_sel_hi:[0,0,0]
	v_mfma_scale_f32_16x16x128_f8f6f4 v[22:25], v[202:209], v[226:233], v[22:25], v199, v199 op_sel_hi:[0,0,0]
	v_mfma_scale_f32_16x16x128_f8f6f4 v[18:21], v[2:9], v[234:241], v[18:21], v199, v199 op_sel_hi:[0,0,0]
	v_mfma_scale_f32_16x16x128_f8f6f4 v[14:17], v[202:209], v[234:241], v[14:17], v199, v199 op_sel_hi:[0,0,0]
	s_setprio 0
	s_barrier
	s_add_u32 s75, s75, 0x10000
	s_addc_u32 s76, s76, 0
	s_add_u32 s24, s24, 0x10000
	s_addc_u32 s25, s25, 0
	s_cmp_ge_i32 s77, s72
	s_mov_b32 s26, s77
	s_cbranch_scc0 .LBB0_834
	s_branch .Lfx_23459
; #define PG8_STAGE(bufoff, gbase, voff) do { _Pragma("unroll") for (int _i = 0; _i < 2; ++_i) \
;         __builtin_amdgcn_global_load_lds((const unsigned*)((const char*)(gbase) + (voff)[_i]), (PG8_LAS unsigned*)(lds + (bufoff) + ldsw + _i * 8192), 16, 0, 0); } while (0)
; #define PG8_WAIT_V(n) asm volatile("s_waitcnt vmcnt(" #n ")" ::: "memory")
; #define PG8_WAIT_L(n) asm volatile("s_waitcnt lgkmcnt(" #n ")" ::: "memory")
; #define PG8_BAR __builtin_amdgcn_s_barrier()
; #define PG8_SCHED __builtin_amdgcn_sched_barrier(0)
; template <class Epi, class Sched, bool ALIGN_EPI = true, bool F8 = false>
; __device__ __forceinline__ void gemm_phase(PG8_LAS unsigned char* lds, const Sched& S, const Epi& E) {
;     ...
;             PG8_LDB(B0, 0, 0); PG8_LDB(B1, 0, 1); PG8_SCHED; PG8_LDA(At, 0, 0); PG8_STAGE(PG8_SA(1, 1), a1, voffA[1]);
;             PG8_WAIT_V(8); PG8_WAIT_L(0); PG8_BAR; PG8_MMA(0, 0, At, B0); PG8_MMA(0, 1, At, B1); PG8_BAR; PG8_SCHED;
;             PG8_LDA(At, 0, 1); PG8_STAGE(PG8_SB(0, 0), b2, voffB[0]); PG8_STAGE(PG8_SB(0, 1), b2, voffB[1]); PG8_STAGE(PG8_SA(0, 0), a2, vA2[0]);
;             PG8_WAIT_V(8); PG8_WAIT_L(0); PG8_BAR; PG8_MMA(1, 0, At, B0); PG8_MMA(1, 1, At, B1); PG8_BAR; PG8_SCHED;
;             PG8_LDB(B0, 1, 0); PG8_LDB(B1, 1, 1); PG8_SCHED; PG8_LDA(At, 1, 0); PG8_STAGE(PG8_SA(0, 1), a2, vA2[1]);
;             PG8_WAIT_V(8); PG8_WAIT_L(0); PG8_BAR; PG8_MMA(0, 0, At, B0); PG8_MMA(0, 1, At, B1); PG8_BAR; PG8_SCHED;
.Lh1e_23459:
.Lh1_834:
	v_add_u32_e32 v10, s58, v190
	ds_read_b128 v[2:5], v10
	ds_read_b128 v[6:9], v10 offset:1024
	ds_read_b128 v[142:145], v10 offset:2048
	ds_read_b128 v[146:149], v10 offset:3072
	v_add_u32_e32 v10, s59, v190
	ds_read_b128 v[150:153], v10
	ds_read_b128 v[154:157], v10 offset:1024
	ds_read_b128 v[202:205], v10 offset:2048
	ds_read_b128 v[206:209], v10 offset:3072
	s_add_i32 s77, s26, 2
	s_add_u32 s27, s24, 0x8000
	s_addc_u32 s28, s25, 0
	s_cmp_eq_u32 s74, s26
	s_cselect_b32 s30, s20, s27
	s_cselect_b32 s31, s21, s28
	s_cselect_b32 s28, s22, s75
	s_cselect_b32 s29, s23, s76
	s_add_u32 s26, s30, 0x8000
	s_addc_u32 s27, s31, 0
	s_add_i32 m0, s45, 0xc000
	ds_read_b128 v[210:213], v198
	ds_read_b128 v[214:217], v198 offset:1024
	ds_read_b128 v[218:221], v198 offset:2048
	ds_read_b128 v[222:225], v198 offset:3072
	ds_read_b128 v[226:229], v198 offset:4096
	ds_read_b128 v[230:233], v198 offset:5120
	ds_read_b128 v[234:237], v198 offset:6144
	ds_read_b128 v[238:241], v198 offset:7168
	global_load_lds_dwordx4 v182, s[24:25]
	s_add_i32 m0, s45, 0xe000
	s_nop 0
	global_load_lds_dwordx4 v180, s[24:25]
	s_waitcnt vmcnt(8)
	s_waitcnt lgkmcnt(0)
	s_barrier
	s_setprio 2
	v_mfma_scale_f32_16x16x128_f8f6f4 v[138:141], v[2:9], v[210:217], v[138:141], v199, v199 op_sel_hi:[0,0,0]
	v_mfma_scale_f32_16x16x128_f8f6f4 v[134:137], v[142:149], v[210:217], v[134:137], v199, v199 op_sel_hi:[0,0,0]
	v_mfma_scale_f32_16x16x128_f8f6f4 v[130:133], v[2:9], v[218:225], v[130:133], v199, v199 op_sel_hi:[0,0,0]
	v_mfma_scale_f32_16x16x128_f8f6f4 v[126:129], v[142:149], v[218:225], v[126:129], v199, v199 op_sel_hi:[0,0,0]
	v_mfma_scale_f32_16x16x128_f8f6f4 v[122:125], v[2:9], v[226:233], v[122:125], v199, v199 op_sel_hi:[0,0,0]
	v_mfma_scale_f32_16x16x128_f8f6f4 v[118:121], v[142:149], v[226:233], v[118:121], v199, v199 op_sel_hi:[0,0,0]
	v_mfma_scale_f32_16x16x128_f8f6f4 v[114:117], v[2:9], v[234:241], v[114:117], v199, v199 op_sel_hi:[0,0,0]
	v_mfma_scale_f32_16x16x128_f8f6f4 v[110:113], v[142:149], v[234:241], v[110:113], v199, v199 op_sel_hi:[0,0,0]
	s_nop 3
	s_setprio 0
	s_setprio 2
	v_mfma_scale_f32_16x16x128_f8f6f4 v[106:109], v[150:157], v[210:217], v[106:109], v199, v199 op_sel_hi:[0,0,0]
	v_mfma_scale_f32_16x16x128_f8f6f4 v[102:105], v[202:209], v[210:217], v[102:105], v199, v199 op_sel_hi:[0,0,0]
	v_mfma_scale_f32_16x16x128_f8f6f4 v[98:101], v[150:157], v[218:225], v[98:101], v199, v199 op_sel_hi:[0,0,0]
	v_mfma_scale_f32_16x16x128_f8f6f4 v[94:97], v[202:209], v[218:225], v[94:97], v199, v199 op_sel_hi:[0,0,0]
	v_mfma_scale_f32_16x16x128_f8f6f4 v[90:93], v[150:157], v[226:233], v[90:93], v199, v199 op_sel_hi:[0,0,0]
	v_mfma_scale_f32_16x16x128_f8f6f4 v[86:89], v[202:209], v[226:233], v[86:89], v199, v199 op_sel_hi:[0,0,0]
	v_mfma_scale_f32_16x16x128_f8f6f4 v[82:85], v[150:157], v[234:241], v[82:85], v199, v199 op_sel_hi:[0,0,0]
	v_mfma_scale_f32_16x16x128_f8f6f4 v[78:81], v[202:209], v[234:241], v[78:81], v199, v199 op_sel_hi:[0,0,0]
	s_setprio 0
	s_add_i32 s78, s58, s44
	s_mov_b32 m0, s78
	ds_read_b128 v[210:213], v198 offset:16384
	ds_read_b128 v[214:217], v198 offset:17408
	ds_read_b128 v[218:221], v198 offset:18432
	ds_read_b128 v[222:225], v198 offset:19456
	ds_read_b128 v[226:229], v198 offset:20480
	ds_read_b128 v[230:233], v198 offset:21504
	ds_read_b128 v[234:237], v198 offset:22528
	ds_read_b128 v[238:241], v198 offset:23552
	global_load_lds_dwordx4 v158, s[28:29]
	s_add_i32 m0, s78, 0x2000
	s_add_i32 s78, s59, s44
	global_load_lds_dwordx4 v160, s[28:29]
	s_add_u32 s98, s28, s8
	s_addc_u32 s99, s29, s9
	s_mov_b32 m0, s78
	s_nop 0
	global_load_lds_dwordx4 v158, s[98:99]
	s_add_u32 s100, s28, s8
	s_addc_u32 s101, s29, s9
	s_add_i32 m0, s78, 0x2000
	s_nop 0
	global_load_lds_dwordx4 v160, s[100:101]
	s_mov_b32 m0, s45
	s_nop 0
	global_load_lds_dwordx4 v162, s[30:31]
	s_mov_b32 m0, s46
	s_nop 0
	global_load_lds_dwordx4 v164, s[30:31]
	s_waitcnt vmcnt(8)
	s_waitcnt lgkmcnt(0)
	s_barrier
	s_setprio 2
	v_mfma_scale_f32_16x16x128_f8f6f4 v[74:77], v[2:9], v[210:217], v[74:77], v199, v199 op_sel_hi:[0,0,0]
	v_mfma_scale_f32_16x16x128_f8f6f4 v[70:73], v[142:149], v[210:217], v[70:73], v199, v199 op_sel_hi:[0,0,0]
	v_mfma_scale_f32_16x16x128_f8f6f4 v[66:69], v[2:9], v[218:225], v[66:69], v199, v199 op_sel_hi:[0,0,0]
	v_mfma_scale_f32_16x16x128_f8f6f4 v[62:65], v[142:149], v[218:225], v[62:65], v199, v199 op_sel_hi:[0,0,0]
	v_mfma_scale_f32_16x16x128_f8f6f4 v[58:61], v[2:9], v[226:233], v[58:61], v199, v199 op_sel_hi:[0,0,0]
	v_mfma_scale_f32_16x16x128_f8f6f4 v[54:57], v[142:149], v[226:233], v[54:57], v199, v199 op_sel_hi:[0,0,0]
	v_mfma_scale_f32_16x16x128_f8f6f4 v[50:53], v[2:9], v[234:241], v[50:53], v199, v199 op_sel_hi:[0,0,0]
	v_mfma_scale_f32_16x16x128_f8f6f4 v[46:49], v[142:149], v[234:241], v[46:49], v199, v199 op_sel_hi:[0,0,0]
	s_nop 3
	s_setprio 0
	s_setprio 2
	v_mfma_scale_f32_16x16x128_f8f6f4 v[42:45], v[150:157], v[210:217], v[42:45], v199, v199 op_sel_hi:[0,0,0]
	v_mfma_scale_f32_16x16x128_f8f6f4 v[38:41], v[202:209], v[210:217], v[38:41], v199, v199 op_sel_hi:[0,0,0]
	v_mfma_scale_f32_16x16x128_f8f6f4 v[34:37], v[150:157], v[218:225], v[34:37], v199, v199 op_sel_hi:[0,0,0]
	v_mfma_scale_f32_16x16x128_f8f6f4 v[30:33], v[202:209], v[218:225], v[30:33], v199, v199 op_sel_hi:[0,0,0]
	v_mfma_scale_f32_16x16x128_f8f6f4 v[26:29], v[150:157], v[226:233], v[26:29], v199, v199 op_sel_hi:[0,0,0]
	v_mfma_scale_f32_16x16x128_f8f6f4 v[22:25], v[202:209], v[226:233], v[22:25], v199, v199 op_sel_hi:[0,0,0]
	v_mfma_scale_f32_16x16x128_f8f6f4 v[18:21], v[150:157], v[234:241], v[18:21], v199, v199 op_sel_hi:[0,0,0]
	v_mfma_scale_f32_16x16x128_f8f6f4 v[14:17], v[202:209], v[234:241], v[14:17], v199, v199 op_sel_hi:[0,0,0]
	s_setprio 0
	s_add_i32 s78, 0, 0x18000
	s_add_i32 s79, 0, 0x1c000
	v_add_u32_e32 v2, s78, v190
	v_add_u32_e32 v10, s79, v190
	ds_read_b128 v[142:145], v2
	ds_read_b128 v[146:149], v2 offset:1024
	ds_read_b128 v[150:153], v2 offset:2048
	ds_read_b128 v[154:157], v2 offset:3072
	ds_read_b128 v[2:5], v10
	ds_read_b128 v[6:9], v10 offset:1024
	ds_read_b128 v[202:205], v10 offset:2048
	ds_read_b128 v[206:209], v10 offset:3072
	s_mov_b32 m0, s47
	ds_read_b128 v[210:213], v198 offset:32768
	ds_read_b128 v[214:217], v198 offset:33792
	ds_read_b128 v[218:221], v198 offset:34816
	ds_read_b128 v[222:225], v198 offset:35840
	ds_read_b128 v[226:229], v198 offset:36864
	ds_read_b128 v[230:233], v198 offset:37888
	ds_read_b128 v[234:237], v198 offset:38912
	ds_read_b128 v[238:241], v198 offset:39936
	global_load_lds_dwordx4 v166, s[30:31]
	s_mov_b32 m0, s48
	s_nop 0
	global_load_lds_dwordx4 v168, s[30:31]
	s_waitcnt vmcnt(8)
	s_waitcnt lgkmcnt(0)
	s_barrier
; #define PG8_STAGE(bufoff, gbase, voff) do { _Pragma("unroll") for (int _i = 0; _i < 2; ++_i) \
;         __builtin_amdgcn_global_load_lds((const unsigned*)((const char*)(gbase) + (voff)[_i]), (PG8_LAS unsigned*)(lds + (bufoff) + ldsw + _i * 8192), 16, 0, 0); } while (0)
; #define PG8_WAIT_V(n) asm volatile("s_waitcnt vmcnt(" #n ")" ::: "memory")
; #define PG8_WAIT_L(n) asm volatile("s_waitcnt lgkmcnt(" #n ")" ::: "memory")
; #define PG8_BAR __builtin_amdgcn_s_barrier()
; #define PG8_SCHED __builtin_amdgcn_sched_barrier(0)
; template <class Epi, class Sched, bool ALIGN_EPI = true, bool F8 = false>
; __device__ __forceinline__ void gemm_phase(PG8_LAS unsigned char* lds, const Sched& S, const Epi& E) {
;     ...
;         for (int t = 0; t < nt; t += 2) {
;     ...
;             PG8_WAIT_V(8); PG8_WAIT_L(0); PG8_BAR; PG8_MMA(0, 0, At, B0); PG8_MMA(0, 1, At, B1); PG8_BAR; PG8_SCHED;
;             PG8_LDA(At, 1, 1); PG8_STAGE(PG8_SB(1, 0), b3, voffB[0]); PG8_STAGE(PG8_SB(1, 1), b3, voffB[1]); PG8_STAGE(PG8_SA(1, 0), a3, vA2[0]);
;             PG8_WAIT_V(8); PG8_WAIT_L(0); PG8_BAR; PG8_MMA(1, 0, At, B0); PG8_MMA(1, 1, At, B1); PG8_BAR; PG8_SCHED;
	s_setprio 2
	v_mfma_scale_f32_16x16x128_f8f6f4 v[138:141], v[142:149], v[210:217], v[138:141], v199, v199 op_sel_hi:[0,0,0]
	v_mfma_scale_f32_16x16x128_f8f6f4 v[134:137], v[150:157], v[210:217], v[134:137], v199, v199 op_sel_hi:[0,0,0]
	v_mfma_scale_f32_16x16x128_f8f6f4 v[130:133], v[142:149], v[218:225], v[130:133], v199, v199 op_sel_hi:[0,0,0]
	v_mfma_scale_f32_16x16x128_f8f6f4 v[126:129], v[150:157], v[218:225], v[126:129], v199, v199 op_sel_hi:[0,0,0]
	v_mfma_scale_f32_16x16x128_f8f6f4 v[122:125], v[142:149], v[226:233], v[122:125], v199, v199 op_sel_hi:[0,0,0]
	v_mfma_scale_f32_16x16x128_f8f6f4 v[118:121], v[150:157], v[226:233], v[118:121], v199, v199 op_sel_hi:[0,0,0]
	v_mfma_scale_f32_16x16x128_f8f6f4 v[114:117], v[142:149], v[234:241], v[114:117], v199, v199 op_sel_hi:[0,0,0]
	v_mfma_scale_f32_16x16x128_f8f6f4 v[110:113], v[150:157], v[234:241], v[110:113], v199, v199 op_sel_hi:[0,0,0]
	s_nop 3
	s_setprio 0
	s_setprio 2
	v_mfma_scale_f32_16x16x128_f8f6f4 v[106:109], v[2:9], v[210:217], v[106:109], v199, v199 op_sel_hi:[0,0,0]
	v_mfma_scale_f32_16x16x128_f8f6f4 v[102:105], v[202:209], v[210:217], v[102:105], v199, v199 op_sel_hi:[0,0,0]
	v_mfma_scale_f32_16x16x128_f8f6f4 v[98:101], v[2:9], v[218:225], v[98:101], v199, v199 op_sel_hi:[0,0,0]
	v_mfma_scale_f32_16x16x128_f8f6f4 v[94:97], v[202:209], v[218:225], v[94:97], v199, v199 op_sel_hi:[0,0,0]
	v_mfma_scale_f32_16x16x128_f8f6f4 v[90:93], v[2:9], v[226:233], v[90:93], v199, v199 op_sel_hi:[0,0,0]
	v_mfma_scale_f32_16x16x128_f8f6f4 v[86:89], v[202:209], v[226:233], v[86:89], v199, v199 op_sel_hi:[0,0,0]
	v_mfma_scale_f32_16x16x128_f8f6f4 v[82:85], v[2:9], v[234:241], v[82:85], v199, v199 op_sel_hi:[0,0,0]
	v_mfma_scale_f32_16x16x128_f8f6f4 v[78:81], v[202:209], v[234:241], v[78:81], v199, v199 op_sel_hi:[0,0,0]
	s_setprio 0
	s_add_u32 s28, s28, 0x8000
	s_addc_u32 s29, s29, 0
	s_add_i32 s30, s78, s44
	s_mov_b32 m0, s30
	ds_read_b128 v[210:213], v198 offset:49152
	ds_read_b128 v[214:217], v198 offset:50176
	ds_read_b128 v[218:221], v198 offset:51200
	ds_read_b128 v[222:225], v198 offset:52224
	ds_read_b128 v[226:229], v198 offset:53248
	ds_read_b128 v[230:233], v198 offset:54272
	ds_read_b128 v[234:237], v198 offset:55296
	ds_read_b128 v[238:241], v198 offset:56320
	global_load_lds_dwordx4 v158, s[28:29]
	s_add_i32 m0, s30, 0x2000
	s_add_i32 s30, s79, s44
	global_load_lds_dwordx4 v160, s[28:29]
	s_mov_b32 m0, s30
	s_nop 0
	global_load_lds_dwordx4 v172, s[28:29]
	s_add_i32 m0, s30, 0x2000
	s_nop 0
	global_load_lds_dwordx4 v174, s[28:29]
	s_mov_b32 m0, s50
	s_nop 0
	global_load_lds_dwordx4 v162, s[26:27]
	s_mov_b32 m0, s51
	s_nop 0
	global_load_lds_dwordx4 v164, s[26:27]
	s_waitcnt vmcnt(8)
	s_waitcnt lgkmcnt(0)
	s_barrier
	s_setprio 2
	v_mfma_scale_f32_16x16x128_f8f6f4 v[74:77], v[142:149], v[210:217], v[74:77], v199, v199 op_sel_hi:[0,0,0]
	v_mfma_scale_f32_16x16x128_f8f6f4 v[70:73], v[150:157], v[210:217], v[70:73], v199, v199 op_sel_hi:[0,0,0]
	v_mfma_scale_f32_16x16x128_f8f6f4 v[66:69], v[142:149], v[218:225], v[66:69], v199, v199 op_sel_hi:[0,0,0]
	v_mfma_scale_f32_16x16x128_f8f6f4 v[62:65], v[150:157], v[218:225], v[62:65], v199, v199 op_sel_hi:[0,0,0]
	v_mfma_scale_f32_16x16x128_f8f6f4 v[58:61], v[142:149], v[226:233], v[58:61], v199, v199 op_sel_hi:[0,0,0]
	v_mfma_scale_f32_16x16x128_f8f6f4 v[54:57], v[150:157], v[226:233], v[54:57], v199, v199 op_sel_hi:[0,0,0]
	v_mfma_scale_f32_16x16x128_f8f6f4 v[50:53], v[142:149], v[234:241], v[50:53], v199, v199 op_sel_hi:[0,0,0]
	v_mfma_scale_f32_16x16x128_f8f6f4 v[46:49], v[150:157], v[234:241], v[46:49], v199, v199 op_sel_hi:[0,0,0]
	s_nop 3
	s_setprio 0
	s_setprio 2
	v_mfma_scale_f32_16x16x128_f8f6f4 v[42:45], v[2:9], v[210:217], v[42:45], v199, v199 op_sel_hi:[0,0,0]
	v_mfma_scale_f32_16x16x128_f8f6f4 v[38:41], v[202:209], v[210:217], v[38:41], v199, v199 op_sel_hi:[0,0,0]
	v_mfma_scale_f32_16x16x128_f8f6f4 v[34:37], v[2:9], v[218:225], v[34:37], v199, v199 op_sel_hi:[0,0,0]
	v_mfma_scale_f32_16x16x128_f8f6f4 v[30:33], v[202:209], v[218:225], v[30:33], v199, v199 op_sel_hi:[0,0,0]
	v_mfma_scale_f32_16x16x128_f8f6f4 v[26:29], v[2:9], v[226:233], v[26:29], v199, v199 op_sel_hi:[0,0,0]
	v_mfma_scale_f32_16x16x128_f8f6f4 v[22:25], v[202:209], v[226:233], v[22:25], v199, v199 op_sel_hi:[0,0,0]
	v_mfma_scale_f32_16x16x128_f8f6f4 v[18:21], v[2:9], v[234:241], v[18:21], v199, v199 op_sel_hi:[0,0,0]
	v_mfma_scale_f32_16x16x128_f8f6f4 v[14:17], v[202:209], v[234:241], v[14:17], v199, v199 op_sel_hi:[0,0,0]
	s_setprio 0
	s_add_u32 s75, s75, 0x10000
	s_addc_u32 s76, s76, 0
	s_add_u32 s24, s24, 0x10000
	s_addc_u32 s25, s25, 0
	s_cmp_ge_i32 s77, s72
	s_mov_b32 s26, s77
	s_cbranch_scc0 .Lh1_834

; #define PG8_STAGE(bufoff, gbase, voff) do { _Pragma("unroll") for (int _i = 0; _i < 2; ++_i) \
;         __builtin_amdgcn_global_load_lds((const unsigned*)((const char*)(gbase) + (voff)[_i]), (PG8_LAS unsigned*)(lds + (bufoff) + ldsw + _i * 8192), 16, 0, 0); } while (0)
; #define PG8_WAIT_V(n) asm volatile("s_waitcnt vmcnt(" #n ")" ::: "memory")
; #define PG8_WAIT_L(n) asm volatile("s_waitcnt lgkmcnt(" #n ")" ::: "memory")
; #define PG8_BAR __builtin_amdgcn_s_barrier()
; #define PG8_SCHED __builtin_amdgcn_sched_barrier(0)
; template <class Epi, class Sched, bool ALIGN_EPI = true, bool F8 = false>
; __device__ __forceinline__ void gemm_phase(PG8_LAS unsigned char* lds, const Sched& S, const Epi& E) {
;     ...
;         for (int t = 0; t < nt; t += 2) {
;             const bool last = (t == nt - 2);
;             if constexpr (Sched::GATHER) { if (last && has_next) S.a_off(nxt, Rs, Cs, voffAn); }
;             const char* a1 = cA + (size_t)(t + 1) * kstep;
;             const char* a2 = last ? nA : cA + (size_t)(t + 2) * kstep; const char* b2 = last ? nB : cB + (size_t)(t + 2) * kstepB;
;             const char* a3 = a2 + kstep; const char* b3 = b2 + kstepB;
;             unsigned vA2[2][2];
; #pragma unroll
;             for (int h = 0; h < 2; ++h)
; #pragma unroll
;                 for (int i = 0; i < 2; ++i) { if constexpr (Sched::GATHER) vA2[h][i] = (last && has_next) ? voffAn[h][i] : voffA[h][i]; else vA2[h][i] = voffA[h][i]; }
;             PG8_LDB(B0, 0, 0); PG8_LDB(B1, 0, 1); PG8_SCHED; PG8_LDA(At, 0, 0); PG8_STAGE(PG8_SA(1, 1), a1, voffA[1]);
;             PG8_WAIT_V(8); PG8_WAIT_L(0); PG8_BAR; PG8_MMA(0, 0, At, B0); PG8_MMA(0, 1, At, B1); PG8_BAR; PG8_SCHED;
;             PG8_LDA(At, 0, 1); PG8_STAGE(PG8_SB(0, 0), b2, voffB[0]); PG8_STAGE(PG8_SB(0, 1), b2, voffB[1]); PG8_STAGE(PG8_SA(0, 0), a2, vA2[0]);
;             PG8_WAIT_V(8); PG8_WAIT_L(0); PG8_BAR; PG8_MMA(1, 0, At, B0); PG8_MMA(1, 1, At, B1); PG8_BAR; PG8_SCHED;
.LBB0_911:
	ds_read_b128 v[18:21], v191
	ds_read_b128 v[22:25], v191 offset:1024
	ds_read_b128 v[26:29], v191 offset:2048
	ds_read_b128 v[30:33], v191 offset:3072
	ds_read_b128 v[2:5], v192
	ds_read_b128 v[6:9], v192 offset:1024
	ds_read_b128 v[10:13], v192 offset:2048
	ds_read_b128 v[14:17], v192 offset:3072
	s_add_u32 s30, s28, 0x8000
	s_addc_u32 s31, s29, 0
	s_cmp_eq_u32 s65, 12
	s_cselect_b32 s42, s22, s30
	s_cselect_b32 s43, s23, s31
	s_cselect_b32 s40, s24, s19
	s_cselect_b32 s41, s25, s21
	s_add_u32 s30, s42, 0x8000
	s_addc_u32 s31, s43, 0
	s_add_i32 m0, s27, 0xc000
	ds_read_b128 v[196:199], v193
	ds_read_b128 v[200:203], v193 offset:1024
	ds_read_b128 v[204:207], v193 offset:2048
	ds_read_b128 v[208:211], v193 offset:3072
	ds_read_b128 v[212:215], v193 offset:4096
	ds_read_b128 v[216:219], v193 offset:5120
	ds_read_b128 v[220:223], v193 offset:6144
	ds_read_b128 v[224:227], v193 offset:7168
	global_load_lds_dwordx4 v182, s[28:29]
	s_add_i32 m0, s27, 0xe000
	s_nop 0
	global_load_lds_dwordx4 v180, s[28:29]
	s_waitcnt vmcnt(8)
	s_waitcnt lgkmcnt(0)
	s_setprio 1
	v_mfma_scale_f32_16x16x128_f8f6f4 v[158:161], v[18:25], v[196:203], v[158:161], v194, v194 op_sel_hi:[0,0,0]
	v_mfma_scale_f32_16x16x128_f8f6f4 v[154:157], v[26:33], v[196:203], v[154:157], v194, v194 op_sel_hi:[0,0,0]
	v_mfma_scale_f32_16x16x128_f8f6f4 v[150:153], v[18:25], v[204:211], v[150:153], v194, v194 op_sel_hi:[0,0,0]
	v_mfma_scale_f32_16x16x128_f8f6f4 v[146:149], v[26:33], v[204:211], v[146:149], v194, v194 op_sel_hi:[0,0,0]
	v_mfma_scale_f32_16x16x128_f8f6f4 v[130:133], v[18:25], v[212:219], v[130:133], v194, v194 op_sel_hi:[0,0,0]
	v_mfma_scale_f32_16x16x128_f8f6f4 v[122:125], v[26:33], v[212:219], v[122:125], v194, v194 op_sel_hi:[0,0,0]
	v_mfma_scale_f32_16x16x128_f8f6f4 v[114:117], v[18:25], v[220:227], v[114:117], v194, v194 op_sel_hi:[0,0,0]
	v_mfma_scale_f32_16x16x128_f8f6f4 v[106:109], v[26:33], v[220:227], v[106:109], v194, v194 op_sel_hi:[0,0,0]
	s_nop 3
	s_setprio 0
	s_setprio 1
	v_mfma_scale_f32_16x16x128_f8f6f4 v[142:145], v[2:9], v[196:203], v[142:145], v194, v194 op_sel_hi:[0,0,0]
	v_mfma_scale_f32_16x16x128_f8f6f4 v[138:141], v[10:17], v[196:203], v[138:141], v194, v194 op_sel_hi:[0,0,0]
	v_mfma_scale_f32_16x16x128_f8f6f4 v[134:137], v[2:9], v[204:211], v[134:137], v194, v194 op_sel_hi:[0,0,0]
	v_mfma_scale_f32_16x16x128_f8f6f4 v[126:129], v[10:17], v[204:211], v[126:129], v194, v194 op_sel_hi:[0,0,0]
	v_mfma_scale_f32_16x16x128_f8f6f4 v[118:121], v[2:9], v[212:219], v[118:121], v194, v194 op_sel_hi:[0,0,0]
	v_mfma_scale_f32_16x16x128_f8f6f4 v[110:113], v[10:17], v[212:219], v[110:113], v194, v194 op_sel_hi:[0,0,0]
	v_mfma_scale_f32_16x16x128_f8f6f4 v[102:105], v[2:9], v[220:227], v[102:105], v194, v194 op_sel_hi:[0,0,0]
	v_mfma_scale_f32_16x16x128_f8f6f4 v[98:101], v[10:17], v[220:227], v[98:101], v194, v194 op_sel_hi:[0,0,0]
	s_setprio 0
	s_barrier
	s_add_i32 s66, s60, s48
	s_mov_b32 m0, s66
	ds_read_b128 v[196:199], v193 offset:16384
	ds_read_b128 v[200:203], v193 offset:17408
	ds_read_b128 v[204:207], v193 offset:18432
	ds_read_b128 v[208:211], v193 offset:19456
	ds_read_b128 v[212:215], v193 offset:20480
	ds_read_b128 v[216:219], v193 offset:21504
	ds_read_b128 v[220:223], v193 offset:22528
	ds_read_b128 v[224:227], v193 offset:23552
	global_load_lds_dwordx4 v162, s[40:41]
	s_add_i32 m0, s66, 0x2000
	s_add_i32 s66, s61, s48
	global_load_lds_dwordx4 v164, s[40:41]
	s_add_u32 s98, s40, s6
	s_addc_u32 s99, s41, s7
	s_mov_b32 m0, s66
	s_nop 0
	global_load_lds_dwordx4 v162, s[98:99]
	s_add_u32 s100, s40, s6
	s_addc_u32 s101, s41, s7
	s_add_i32 m0, s66, 0x2000
	s_nop 0
	global_load_lds_dwordx4 v164, s[100:101]
	s_mov_b32 m0, s27
	s_nop 0
	global_load_lds_dwordx4 v166, s[42:43]
	s_mov_b32 m0, s49
	s_nop 0
	global_load_lds_dwordx4 v168, s[42:43]
	s_waitcnt vmcnt(8)
	s_waitcnt lgkmcnt(0)
	s_setprio 1
	v_mfma_scale_f32_16x16x128_f8f6f4 v[94:97], v[18:25], v[196:203], v[94:97], v194, v194 op_sel_hi:[0,0,0]
	v_mfma_scale_f32_16x16x128_f8f6f4 v[90:93], v[26:33], v[196:203], v[90:93], v194, v194 op_sel_hi:[0,0,0]
	v_mfma_scale_f32_16x16x128_f8f6f4 v[82:85], v[18:25], v[204:211], v[82:85], v194, v194 op_sel_hi:[0,0,0]
	v_mfma_scale_f32_16x16x128_f8f6f4 v[74:77], v[26:33], v[204:211], v[74:77], v194, v194 op_sel_hi:[0,0,0]
	v_mfma_scale_f32_16x16x128_f8f6f4 v[66:69], v[18:25], v[212:219], v[66:69], v194, v194 op_sel_hi:[0,0,0]
	v_mfma_scale_f32_16x16x128_f8f6f4 v[58:61], v[26:33], v[212:219], v[58:61], v194, v194 op_sel_hi:[0,0,0]
	v_mfma_scale_f32_16x16x128_f8f6f4 v[50:53], v[18:25], v[220:227], v[50:53], v194, v194 op_sel_hi:[0,0,0]
	v_mfma_scale_f32_16x16x128_f8f6f4 v[42:45], v[26:33], v[220:227], v[42:45], v194, v194 op_sel_hi:[0,0,0]
	s_nop 3
	s_setprio 0
	s_setprio 1
	v_mfma_scale_f32_16x16x128_f8f6f4 v[86:89], v[2:9], v[196:203], v[86:89], v194, v194 op_sel_hi:[0,0,0]
	v_mfma_scale_f32_16x16x128_f8f6f4 v[78:81], v[10:17], v[196:203], v[78:81], v194, v194 op_sel_hi:[0,0,0]
	v_mfma_scale_f32_16x16x128_f8f6f4 v[70:73], v[2:9], v[204:211], v[70:73], v194, v194 op_sel_hi:[0,0,0]
	v_mfma_scale_f32_16x16x128_f8f6f4 v[62:65], v[10:17], v[204:211], v[62:65], v194, v194 op_sel_hi:[0,0,0]
	v_mfma_scale_f32_16x16x128_f8f6f4 v[54:57], v[2:9], v[212:219], v[54:57], v194, v194 op_sel_hi:[0,0,0]
	v_mfma_scale_f32_16x16x128_f8f6f4 v[46:49], v[10:17], v[212:219], v[46:49], v194, v194 op_sel_hi:[0,0,0]
	v_mfma_scale_f32_16x16x128_f8f6f4 v[38:41], v[2:9], v[220:227], v[38:41], v194, v194 op_sel_hi:[0,0,0]
	v_mfma_scale_f32_16x16x128_f8f6f4 v[34:37], v[10:17], v[220:227], v[34:37], v194, v194 op_sel_hi:[0,0,0]
	s_setprio 0
	s_barrier
; #define PG8_STAGE(bufoff, gbase, voff) do { _Pragma("unroll") for (int _i = 0; _i < 2; ++_i) \
;         __builtin_amdgcn_global_load_lds((const unsigned*)((const char*)(gbase) + (voff)[_i]), (PG8_LAS unsigned*)(lds + (bufoff) + ldsw + _i * 8192), 16, 0, 0); } while (0)
; #define PG8_WAIT_V(n) asm volatile("s_waitcnt vmcnt(" #n ")" ::: "memory")
; #define PG8_WAIT_L(n) asm volatile("s_waitcnt lgkmcnt(" #n ")" ::: "memory")
; #define PG8_BAR __builtin_amdgcn_s_barrier()
; #define PG8_SCHED __builtin_amdgcn_sched_barrier(0)
; template <class Epi, class Sched, bool ALIGN_EPI = true, bool F8 = false>
; __device__ __forceinline__ void gemm_phase(PG8_LAS unsigned char* lds, const Sched& S, const Epi& E) {
;     ...
;         for (int t = 0; t < nt; t += 2) {
;     ...
;             PG8_LDB(B0, 1, 0); PG8_LDB(B1, 1, 1); PG8_SCHED; PG8_LDA(At, 1, 0); PG8_STAGE(PG8_SA(0, 1), a2, vA2[1]);
;             PG8_WAIT_V(8); PG8_WAIT_L(0); PG8_BAR; PG8_MMA(0, 0, At, B0); PG8_MMA(0, 1, At, B1); PG8_BAR; PG8_SCHED;
;             PG8_LDA(At, 1, 1); PG8_STAGE(PG8_SB(1, 0), b3, voffB[0]); PG8_STAGE(PG8_SB(1, 1), b3, voffB[1]); PG8_STAGE(PG8_SA(1, 0), a3, vA2[0]);
;             PG8_WAIT_V(8); PG8_WAIT_L(0); PG8_BAR; PG8_MMA(1, 0, At, B0); PG8_MMA(1, 1, At, B1); PG8_BAR; PG8_SCHED;
	s_add_i32 s66, 0, 0x18000
	s_add_i32 s67, 0, 0x1c000
	v_add_u32_e32 v14, s66, v189
	v_add_u32_e32 v30, s67, v189
	ds_read_b128 v[2:5], v14
	ds_read_b128 v[6:9], v14 offset:1024
	ds_read_b128 v[10:13], v14 offset:2048
	ds_read_b128 v[14:17], v14 offset:3072
	ds_read_b128 v[18:21], v30
	ds_read_b128 v[22:25], v30 offset:1024
	ds_read_b128 v[26:29], v30 offset:2048
	ds_read_b128 v[30:33], v30 offset:3072
	s_mov_b32 m0, s50
	ds_read_b128 v[196:199], v193 offset:32768
	ds_read_b128 v[200:203], v193 offset:33792
	ds_read_b128 v[204:207], v193 offset:34816
	ds_read_b128 v[208:211], v193 offset:35840
	ds_read_b128 v[212:215], v193 offset:36864
	ds_read_b128 v[216:219], v193 offset:37888
	ds_read_b128 v[220:223], v193 offset:38912
	ds_read_b128 v[224:227], v193 offset:39936
	global_load_lds_dwordx4 v172, s[42:43]
	s_mov_b32 m0, s51
	s_nop 0
	global_load_lds_dwordx4 v174, s[42:43]
	s_waitcnt vmcnt(8)
	s_waitcnt lgkmcnt(0)
	s_setprio 1
	v_mfma_scale_f32_16x16x128_f8f6f4 v[158:161], v[2:9], v[196:203], v[158:161], v194, v194 op_sel_hi:[0,0,0]
	v_mfma_scale_f32_16x16x128_f8f6f4 v[154:157], v[10:17], v[196:203], v[154:157], v194, v194 op_sel_hi:[0,0,0]
	v_mfma_scale_f32_16x16x128_f8f6f4 v[150:153], v[2:9], v[204:211], v[150:153], v194, v194 op_sel_hi:[0,0,0]
	v_mfma_scale_f32_16x16x128_f8f6f4 v[146:149], v[10:17], v[204:211], v[146:149], v194, v194 op_sel_hi:[0,0,0]
	v_mfma_scale_f32_16x16x128_f8f6f4 v[130:133], v[2:9], v[212:219], v[130:133], v194, v194 op_sel_hi:[0,0,0]
	v_mfma_scale_f32_16x16x128_f8f6f4 v[122:125], v[10:17], v[212:219], v[122:125], v194, v194 op_sel_hi:[0,0,0]
	v_mfma_scale_f32_16x16x128_f8f6f4 v[114:117], v[2:9], v[220:227], v[114:117], v194, v194 op_sel_hi:[0,0,0]
	v_mfma_scale_f32_16x16x128_f8f6f4 v[106:109], v[10:17], v[220:227], v[106:109], v194, v194 op_sel_hi:[0,0,0]
	s_nop 3
	s_setprio 0
	s_setprio 1
	v_mfma_scale_f32_16x16x128_f8f6f4 v[142:145], v[18:25], v[196:203], v[142:145], v194, v194 op_sel_hi:[0,0,0]
	v_mfma_scale_f32_16x16x128_f8f6f4 v[138:141], v[26:33], v[196:203], v[138:141], v194, v194 op_sel_hi:[0,0,0]
	v_mfma_scale_f32_16x16x128_f8f6f4 v[134:137], v[18:25], v[204:211], v[134:137], v194, v194 op_sel_hi:[0,0,0]
	v_mfma_scale_f32_16x16x128_f8f6f4 v[126:129], v[26:33], v[204:211], v[126:129], v194, v194 op_sel_hi:[0,0,0]
	v_mfma_scale_f32_16x16x128_f8f6f4 v[118:121], v[18:25], v[212:219], v[118:121], v194, v194 op_sel_hi:[0,0,0]
	v_mfma_scale_f32_16x16x128_f8f6f4 v[110:113], v[26:33], v[212:219], v[110:113], v194, v194 op_sel_hi:[0,0,0]
	v_mfma_scale_f32_16x16x128_f8f6f4 v[102:105], v[18:25], v[220:227], v[102:105], v194, v194 op_sel_hi:[0,0,0]
	v_mfma_scale_f32_16x16x128_f8f6f4 v[98:101], v[26:33], v[220:227], v[98:101], v194, v194 op_sel_hi:[0,0,0]
	s_setprio 0
	s_barrier
	s_add_u32 s40, s40, 0x8000
	s_addc_u32 s41, s41, 0
	s_add_i32 s42, s66, s48
	s_mov_b32 m0, s42
	ds_read_b128 v[196:199], v193 offset:49152
	ds_read_b128 v[200:203], v193 offset:50176
	ds_read_b128 v[204:207], v193 offset:51200
	ds_read_b128 v[208:211], v193 offset:52224
	ds_read_b128 v[212:215], v193 offset:53248
	ds_read_b128 v[216:219], v193 offset:54272
	ds_read_b128 v[220:223], v193 offset:55296
	ds_read_b128 v[224:227], v193 offset:56320
	global_load_lds_dwordx4 v162, s[40:41]
	s_add_i32 m0, s42, 0x2000
	s_add_i32 s42, s67, s48
	global_load_lds_dwordx4 v164, s[40:41]
	s_mov_b32 m0, s42
	s_nop 0
	global_load_lds_dwordx4 v176, s[40:41]
	s_add_i32 m0, s42, 0x2000
	s_nop 0
	global_load_lds_dwordx4 v178, s[40:41]
	s_mov_b32 m0, s53
	s_nop 0
	global_load_lds_dwordx4 v166, s[30:31]
	s_mov_b32 m0, s58
	s_nop 0
	global_load_lds_dwordx4 v168, s[30:31]
	s_waitcnt vmcnt(8)
	s_waitcnt lgkmcnt(0)
	s_setprio 1
	v_mfma_scale_f32_16x16x128_f8f6f4 v[94:97], v[2:9], v[196:203], v[94:97], v194, v194 op_sel_hi:[0,0,0]
	v_mfma_scale_f32_16x16x128_f8f6f4 v[90:93], v[10:17], v[196:203], v[90:93], v194, v194 op_sel_hi:[0,0,0]
	v_mfma_scale_f32_16x16x128_f8f6f4 v[82:85], v[2:9], v[204:211], v[82:85], v194, v194 op_sel_hi:[0,0,0]
	v_mfma_scale_f32_16x16x128_f8f6f4 v[74:77], v[10:17], v[204:211], v[74:77], v194, v194 op_sel_hi:[0,0,0]
	v_mfma_scale_f32_16x16x128_f8f6f4 v[66:69], v[2:9], v[212:219], v[66:69], v194, v194 op_sel_hi:[0,0,0]
	v_mfma_scale_f32_16x16x128_f8f6f4 v[58:61], v[10:17], v[212:219], v[58:61], v194, v194 op_sel_hi:[0,0,0]
	v_mfma_scale_f32_16x16x128_f8f6f4 v[50:53], v[2:9], v[220:227], v[50:53], v194, v194 op_sel_hi:[0,0,0]
	v_mfma_scale_f32_16x16x128_f8f6f4 v[42:45], v[10:17], v[220:227], v[42:45], v194, v194 op_sel_hi:[0,0,0]
	s_nop 3
	s_setprio 0
	s_setprio 1
	v_mfma_scale_f32_16x16x128_f8f6f4 v[86:89], v[18:25], v[196:203], v[86:89], v194, v194 op_sel_hi:[0,0,0]
	v_mfma_scale_f32_16x16x128_f8f6f4 v[78:81], v[26:33], v[196:203], v[78:81], v194, v194 op_sel_hi:[0,0,0]
	v_mfma_scale_f32_16x16x128_f8f6f4 v[70:73], v[18:25], v[204:211], v[70:73], v194, v194 op_sel_hi:[0,0,0]
	v_mfma_scale_f32_16x16x128_f8f6f4 v[62:65], v[26:33], v[204:211], v[62:65], v194, v194 op_sel_hi:[0,0,0]
	v_mfma_scale_f32_16x16x128_f8f6f4 v[54:57], v[18:25], v[212:219], v[54:57], v194, v194 op_sel_hi:[0,0,0]
	v_mfma_scale_f32_16x16x128_f8f6f4 v[46:49], v[26:33], v[212:219], v[46:49], v194, v194 op_sel_hi:[0,0,0]
	v_mfma_scale_f32_16x16x128_f8f6f4 v[38:41], v[18:25], v[220:227], v[38:41], v194, v194 op_sel_hi:[0,0,0]
	v_mfma_scale_f32_16x16x128_f8f6f4 v[34:37], v[26:33], v[220:227], v[34:37], v194, v194 op_sel_hi:[0,0,0]
	s_setprio 0
	s_barrier
	s_add_i32 s65, s65, 2
	s_add_u32 s19, s19, 0x10000
	s_addc_u32 s21, s21, 0
	s_add_u32 s28, s28, 0x10000
	s_addc_u32 s29, s29, 0
	s_cmp_gt_u32 s65, 13
	s_cbranch_scc0 .LBB0_911
	s_branch .Lfx_26630
; #define PG8_STAGE(bufoff, gbase, voff) do { _Pragma("unroll") for (int _i = 0; _i < 2; ++_i) \
;         __builtin_amdgcn_global_load_lds((const unsigned*)((const char*)(gbase) + (voff)[_i]), (PG8_LAS unsigned*)(lds + (bufoff) + ldsw + _i * 8192), 16, 0, 0); } while (0)
; #define PG8_WAIT_V(n) asm volatile("s_waitcnt vmcnt(" #n ")" ::: "memory")
; #define PG8_WAIT_L(n) asm volatile("s_waitcnt lgkmcnt(" #n ")" ::: "memory")
; #define PG8_BAR __builtin_amdgcn_s_barrier()
; #define PG8_SCHED __builtin_amdgcn_sched_barrier(0)
; template <class Epi, class Sched, bool ALIGN_EPI = true, bool F8 = false>
; __device__ __forceinline__ void gemm_phase(PG8_LAS unsigned char* lds, const Sched& S, const Epi& E) {
;     ...
;             const char* a1 = cA + (size_t)(t + 1) * kstep;
;             const char* a2 = last ? nA : cA + (size_t)(t + 2) * kstep; const char* b2 = last ? nB : cB + (size_t)(t + 2) * kstepB;
;             const char* a3 = a2 + kstep; const char* b3 = b2 + kstepB;
;             unsigned vA2[2][2];
; #pragma unroll
;             for (int h = 0; h < 2; ++h)
; #pragma unroll
;                 for (int i = 0; i < 2; ++i) { if constexpr (Sched::GATHER) vA2[h][i] = (last && has_next) ? voffAn[h][i] : voffA[h][i]; else vA2[h][i] = voffA[h][i]; }
;             PG8_LDB(B0, 0, 0); PG8_LDB(B1, 0, 1); PG8_SCHED; PG8_LDA(At, 0, 0); PG8_STAGE(PG8_SA(1, 1), a1, voffA[1]);
;             PG8_WAIT_V(8); PG8_WAIT_L(0); PG8_BAR; PG8_MMA(0, 0, At, B0); PG8_MMA(0, 1, At, B1); PG8_BAR; PG8_SCHED;
;             PG8_LDA(At, 0, 1); PG8_STAGE(PG8_SB(0, 0), b2, voffB[0]); PG8_STAGE(PG8_SB(0, 1), b2, voffB[1]); PG8_STAGE(PG8_SA(0, 0), a2, vA2[0]);
;             PG8_WAIT_V(8); PG8_WAIT_L(0); PG8_BAR; PG8_MMA(1, 0, At, B0); PG8_MMA(1, 1, At, B1); PG8_BAR; PG8_SCHED;
;             PG8_LDB(B0, 1, 0); PG8_LDB(B1, 1, 1); PG8_SCHED; PG8_LDA(At, 1, 0); PG8_STAGE(PG8_SA(0, 1), a2, vA2[1]);
;             PG8_WAIT_V(8); PG8_WAIT_L(0); PG8_BAR; PG8_MMA(0, 0, At, B0); PG8_MMA(0, 1, At, B1); PG8_BAR; PG8_SCHED;
;             PG8_LDA(At, 1, 1); PG8_STAGE(PG8_SB(1, 0), b3, voffB[0]); PG8_STAGE(PG8_SB(1, 1), b3, voffB[1]); PG8_STAGE(PG8_SA(1, 0), a3, vA2[0]);
;             PG8_WAIT_V(8); PG8_WAIT_L(0); PG8_BAR; PG8_MMA(1, 0, At, B0); PG8_MMA(1, 1, At, B1); PG8_BAR; PG8_SCHED;
.Lh1e_26630:
.Lh1_911:
	ds_read_b128 v[18:21], v191
	ds_read_b128 v[22:25], v191 offset:1024
	ds_read_b128 v[26:29], v191 offset:2048
	ds_read_b128 v[30:33], v191 offset:3072
	ds_read_b128 v[2:5], v192
	ds_read_b128 v[6:9], v192 offset:1024
	ds_read_b128 v[10:13], v192 offset:2048
	ds_read_b128 v[14:17], v192 offset:3072
	s_add_u32 s30, s28, 0x8000
	s_addc_u32 s31, s29, 0
	s_cmp_eq_u32 s65, 12
	s_cselect_b32 s42, s22, s30
	s_cselect_b32 s43, s23, s31
	s_cselect_b32 s40, s24, s19
	s_cselect_b32 s41, s25, s21
	s_add_u32 s30, s42, 0x8000
	s_addc_u32 s31, s43, 0
	s_add_i32 m0, s27, 0xc000
	ds_read_b128 v[196:199], v193
	ds_read_b128 v[200:203], v193 offset:1024
	ds_read_b128 v[204:207], v193 offset:2048
	ds_read_b128 v[208:211], v193 offset:3072
	ds_read_b128 v[212:215], v193 offset:4096
	ds_read_b128 v[216:219], v193 offset:5120
	ds_read_b128 v[220:223], v193 offset:6144
	ds_read_b128 v[224:227], v193 offset:7168
	global_load_lds_dwordx4 v182, s[28:29]
	s_add_i32 m0, s27, 0xe000
	s_nop 0
	global_load_lds_dwordx4 v180, s[28:29]
	s_waitcnt vmcnt(8)
	s_waitcnt lgkmcnt(0)
	s_barrier
	s_setprio 2
	v_mfma_scale_f32_16x16x128_f8f6f4 v[158:161], v[18:25], v[196:203], v[158:161], v194, v194 op_sel_hi:[0,0,0]
	v_mfma_scale_f32_16x16x128_f8f6f4 v[154:157], v[26:33], v[196:203], v[154:157], v194, v194 op_sel_hi:[0,0,0]
	v_mfma_scale_f32_16x16x128_f8f6f4 v[150:153], v[18:25], v[204:211], v[150:153], v194, v194 op_sel_hi:[0,0,0]
	v_mfma_scale_f32_16x16x128_f8f6f4 v[146:149], v[26:33], v[204:211], v[146:149], v194, v194 op_sel_hi:[0,0,0]
	v_mfma_scale_f32_16x16x128_f8f6f4 v[130:133], v[18:25], v[212:219], v[130:133], v194, v194 op_sel_hi:[0,0,0]
	v_mfma_scale_f32_16x16x128_f8f6f4 v[122:125], v[26:33], v[212:219], v[122:125], v194, v194 op_sel_hi:[0,0,0]
	v_mfma_scale_f32_16x16x128_f8f6f4 v[114:117], v[18:25], v[220:227], v[114:117], v194, v194 op_sel_hi:[0,0,0]
	v_mfma_scale_f32_16x16x128_f8f6f4 v[106:109], v[26:33], v[220:227], v[106:109], v194, v194 op_sel_hi:[0,0,0]
	s_nop 3
	s_setprio 0
	s_setprio 2
	v_mfma_scale_f32_16x16x128_f8f6f4 v[142:145], v[2:9], v[196:203], v[142:145], v194, v194 op_sel_hi:[0,0,0]
	v_mfma_scale_f32_16x16x128_f8f6f4 v[138:141], v[10:17], v[196:203], v[138:141], v194, v194 op_sel_hi:[0,0,0]
	v_mfma_scale_f32_16x16x128_f8f6f4 v[134:137], v[2:9], v[204:211], v[134:137], v194, v194 op_sel_hi:[0,0,0]
	v_mfma_scale_f32_16x16x128_f8f6f4 v[126:129], v[10:17], v[204:211], v[126:129], v194, v194 op_sel_hi:[0,0,0]
	v_mfma_scale_f32_16x16x128_f8f6f4 v[118:121], v[2:9], v[212:219], v[118:121], v194, v194 op_sel_hi:[0,0,0]
	v_mfma_scale_f32_16x16x128_f8f6f4 v[110:113], v[10:17], v[212:219], v[110:113], v194, v194 op_sel_hi:[0,0,0]
	v_mfma_scale_f32_16x16x128_f8f6f4 v[102:105], v[2:9], v[220:227], v[102:105], v194, v194 op_sel_hi:[0,0,0]
	v_mfma_scale_f32_16x16x128_f8f6f4 v[98:101], v[10:17], v[220:227], v[98:101], v194, v194 op_sel_hi:[0,0,0]
	s_setprio 0
	s_add_i32 s66, s60, s48
	s_mov_b32 m0, s66
	ds_read_b128 v[196:199], v193 offset:16384
	ds_read_b128 v[200:203], v193 offset:17408
	ds_read_b128 v[204:207], v193 offset:18432
	ds_read_b128 v[208:211], v193 offset:19456
	ds_read_b128 v[212:215], v193 offset:20480
	ds_read_b128 v[216:219], v193 offset:21504
	ds_read_b128 v[220:223], v193 offset:22528
	ds_read_b128 v[224:227], v193 offset:23552
	global_load_lds_dwordx4 v162, s[40:41]
	s_add_i32 m0, s66, 0x2000
	s_add_i32 s66, s61, s48
	global_load_lds_dwordx4 v164, s[40:41]
	s_add_u32 s98, s40, s6
	s_addc_u32 s99, s41, s7
	s_mov_b32 m0, s66
	s_nop 0
	global_load_lds_dwordx4 v162, s[98:99]
	s_add_u32 s100, s40, s6
	s_addc_u32 s101, s41, s7
	s_add_i32 m0, s66, 0x2000
	s_nop 0
	global_load_lds_dwordx4 v164, s[100:101]
	s_mov_b32 m0, s27
	s_nop 0
	global_load_lds_dwordx4 v166, s[42:43]
	s_mov_b32 m0, s49
	s_nop 0
	global_load_lds_dwordx4 v168, s[42:43]
	s_waitcnt vmcnt(8)
	s_waitcnt lgkmcnt(0)
	s_barrier
	s_setprio 2
	v_mfma_scale_f32_16x16x128_f8f6f4 v[94:97], v[18:25], v[196:203], v[94:97], v194, v194 op_sel_hi:[0,0,0]
	v_mfma_scale_f32_16x16x128_f8f6f4 v[90:93], v[26:33], v[196:203], v[90:93], v194, v194 op_sel_hi:[0,0,0]
	v_mfma_scale_f32_16x16x128_f8f6f4 v[82:85], v[18:25], v[204:211], v[82:85], v194, v194 op_sel_hi:[0,0,0]
	v_mfma_scale_f32_16x16x128_f8f6f4 v[74:77], v[26:33], v[204:211], v[74:77], v194, v194 op_sel_hi:[0,0,0]
	v_mfma_scale_f32_16x16x128_f8f6f4 v[66:69], v[18:25], v[212:219], v[66:69], v194, v194 op_sel_hi:[0,0,0]
	v_mfma_scale_f32_16x16x128_f8f6f4 v[58:61], v[26:33], v[212:219], v[58:61], v194, v194 op_sel_hi:[0,0,0]
	v_mfma_scale_f32_16x16x128_f8f6f4 v[50:53], v[18:25], v[220:227], v[50:53], v194, v194 op_sel_hi:[0,0,0]
	v_mfma_scale_f32_16x16x128_f8f6f4 v[42:45], v[26:33], v[220:227], v[42:45], v194, v194 op_sel_hi:[0,0,0]
	s_nop 3
	s_setprio 0
	s_setprio 2
	v_mfma_scale_f32_16x16x128_f8f6f4 v[86:89], v[2:9], v[196:203], v[86:89], v194, v194 op_sel_hi:[0,0,0]
	v_mfma_scale_f32_16x16x128_f8f6f4 v[78:81], v[10:17], v[196:203], v[78:81], v194, v194 op_sel_hi:[0,0,0]
	v_mfma_scale_f32_16x16x128_f8f6f4 v[70:73], v[2:9], v[204:211], v[70:73], v194, v194 op_sel_hi:[0,0,0]
	v_mfma_scale_f32_16x16x128_f8f6f4 v[62:65], v[10:17], v[204:211], v[62:65], v194, v194 op_sel_hi:[0,0,0]
	v_mfma_scale_f32_16x16x128_f8f6f4 v[54:57], v[2:9], v[212:219], v[54:57], v194, v194 op_sel_hi:[0,0,0]
	v_mfma_scale_f32_16x16x128_f8f6f4 v[46:49], v[10:17], v[212:219], v[46:49], v194, v194 op_sel_hi:[0,0,0]
	v_mfma_scale_f32_16x16x128_f8f6f4 v[38:41], v[2:9], v[220:227], v[38:41], v194, v194 op_sel_hi:[0,0,0]
	v_mfma_scale_f32_16x16x128_f8f6f4 v[34:37], v[10:17], v[220:227], v[34:37], v194, v194 op_sel_hi:[0,0,0]
	s_setprio 0
	s_add_i32 s66, 0, 0x18000
	s_add_i32 s67, 0, 0x1c000
	v_add_u32_e32 v14, s66, v189
	v_add_u32_e32 v30, s67, v189
	ds_read_b128 v[2:5], v14
	ds_read_b128 v[6:9], v14 offset:1024
	ds_read_b128 v[10:13], v14 offset:2048
	ds_read_b128 v[14:17], v14 offset:3072
	ds_read_b128 v[18:21], v30
	ds_read_b128 v[22:25], v30 offset:1024
	ds_read_b128 v[26:29], v30 offset:2048
	ds_read_b128 v[30:33], v30 offset:3072
	s_mov_b32 m0, s50
	ds_read_b128 v[196:199], v193 offset:32768
	ds_read_b128 v[200:203], v193 offset:33792
	ds_read_b128 v[204:207], v193 offset:34816
	ds_read_b128 v[208:211], v193 offset:35840
	ds_read_b128 v[212:215], v193 offset:36864
	ds_read_b128 v[216:219], v193 offset:37888
	ds_read_b128 v[220:223], v193 offset:38912
	ds_read_b128 v[224:227], v193 offset:39936
	global_load_lds_dwordx4 v172, s[42:43]
	s_mov_b32 m0, s51
	s_nop 0
	global_load_lds_dwordx4 v174, s[42:43]
	s_waitcnt vmcnt(8)
	s_waitcnt lgkmcnt(0)
	s_barrier
; #define PG8_STAGE(bufoff, gbase, voff) do { _Pragma("unroll") for (int _i = 0; _i < 2; ++_i) \
;         __builtin_amdgcn_global_load_lds((const unsigned*)((const char*)(gbase) + (voff)[_i]), (PG8_LAS unsigned*)(lds + (bufoff) + ldsw + _i * 8192), 16, 0, 0); } while (0)
; #define PG8_WAIT_V(n) asm volatile("s_waitcnt vmcnt(" #n ")" ::: "memory")
; #define PG8_WAIT_L(n) asm volatile("s_waitcnt lgkmcnt(" #n ")" ::: "memory")
; #define PG8_BAR __builtin_amdgcn_s_barrier()
; #define PG8_SCHED __builtin_amdgcn_sched_barrier(0)
; template <class Epi, class Sched, bool ALIGN_EPI = true, bool F8 = false>
; __device__ __forceinline__ void gemm_phase(PG8_LAS unsigned char* lds, const Sched& S, const Epi& E) {
;     ...
;             PG8_LDB(B0, 1, 0); PG8_LDB(B1, 1, 1); PG8_SCHED; PG8_LDA(At, 1, 0); PG8_STAGE(PG8_SA(0, 1), a2, vA2[1]);
;             PG8_WAIT_V(8); PG8_WAIT_L(0); PG8_BAR; PG8_MMA(0, 0, At, B0); PG8_MMA(0, 1, At, B1); PG8_BAR; PG8_SCHED;
;             PG8_LDA(At, 1, 1); PG8_STAGE(PG8_SB(1, 0), b3, voffB[0]); PG8_STAGE(PG8_SB(1, 1), b3, voffB[1]); PG8_STAGE(PG8_SA(1, 0), a3, vA2[0]);
;             PG8_WAIT_V(8); PG8_WAIT_L(0); PG8_BAR; PG8_MMA(1, 0, At, B0); PG8_MMA(1, 1, At, B1); PG8_BAR; PG8_SCHED;
	s_setprio 2
	v_mfma_scale_f32_16x16x128_f8f6f4 v[158:161], v[2:9], v[196:203], v[158:161], v194, v194 op_sel_hi:[0,0,0]
	v_mfma_scale_f32_16x16x128_f8f6f4 v[154:157], v[10:17], v[196:203], v[154:157], v194, v194 op_sel_hi:[0,0,0]
	v_mfma_scale_f32_16x16x128_f8f6f4 v[150:153], v[2:9], v[204:211], v[150:153], v194, v194 op_sel_hi:[0,0,0]
	v_mfma_scale_f32_16x16x128_f8f6f4 v[146:149], v[10:17], v[204:211], v[146:149], v194, v194 op_sel_hi:[0,0,0]
	v_mfma_scale_f32_16x16x128_f8f6f4 v[130:133], v[2:9], v[212:219], v[130:133], v194, v194 op_sel_hi:[0,0,0]
	v_mfma_scale_f32_16x16x128_f8f6f4 v[122:125], v[10:17], v[212:219], v[122:125], v194, v194 op_sel_hi:[0,0,0]
	v_mfma_scale_f32_16x16x128_f8f6f4 v[114:117], v[2:9], v[220:227], v[114:117], v194, v194 op_sel_hi:[0,0,0]
	v_mfma_scale_f32_16x16x128_f8f6f4 v[106:109], v[10:17], v[220:227], v[106:109], v194, v194 op_sel_hi:[0,0,0]
	s_nop 3
	s_setprio 0
	s_setprio 2
	v_mfma_scale_f32_16x16x128_f8f6f4 v[142:145], v[18:25], v[196:203], v[142:145], v194, v194 op_sel_hi:[0,0,0]
	v_mfma_scale_f32_16x16x128_f8f6f4 v[138:141], v[26:33], v[196:203], v[138:141], v194, v194 op_sel_hi:[0,0,0]
	v_mfma_scale_f32_16x16x128_f8f6f4 v[134:137], v[18:25], v[204:211], v[134:137], v194, v194 op_sel_hi:[0,0,0]
	v_mfma_scale_f32_16x16x128_f8f6f4 v[126:129], v[26:33], v[204:211], v[126:129], v194, v194 op_sel_hi:[0,0,0]
	v_mfma_scale_f32_16x16x128_f8f6f4 v[118:121], v[18:25], v[212:219], v[118:121], v194, v194 op_sel_hi:[0,0,0]
	v_mfma_scale_f32_16x16x128_f8f6f4 v[110:113], v[26:33], v[212:219], v[110:113], v194, v194 op_sel_hi:[0,0,0]
	v_mfma_scale_f32_16x16x128_f8f6f4 v[102:105], v[18:25], v[220:227], v[102:105], v194, v194 op_sel_hi:[0,0,0]
	v_mfma_scale_f32_16x16x128_f8f6f4 v[98:101], v[26:33], v[220:227], v[98:101], v194, v194 op_sel_hi:[0,0,0]
	s_setprio 0
	s_add_u32 s40, s40, 0x8000
	s_addc_u32 s41, s41, 0
	s_add_i32 s42, s66, s48
	s_mov_b32 m0, s42
	ds_read_b128 v[196:199], v193 offset:49152
	ds_read_b128 v[200:203], v193 offset:50176
	ds_read_b128 v[204:207], v193 offset:51200
	ds_read_b128 v[208:211], v193 offset:52224
	ds_read_b128 v[212:215], v193 offset:53248
	ds_read_b128 v[216:219], v193 offset:54272
	ds_read_b128 v[220:223], v193 offset:55296
	ds_read_b128 v[224:227], v193 offset:56320
	global_load_lds_dwordx4 v162, s[40:41]
	s_add_i32 m0, s42, 0x2000
	s_add_i32 s42, s67, s48
	global_load_lds_dwordx4 v164, s[40:41]
	s_mov_b32 m0, s42
	s_nop 0
	global_load_lds_dwordx4 v176, s[40:41]
	s_add_i32 m0, s42, 0x2000
	s_nop 0
	global_load_lds_dwordx4 v178, s[40:41]
	s_mov_b32 m0, s53
	s_nop 0
	global_load_lds_dwordx4 v166, s[30:31]
	s_mov_b32 m0, s58
	s_nop 0
	global_load_lds_dwordx4 v168, s[30:31]
	s_waitcnt vmcnt(8)
	s_waitcnt lgkmcnt(0)
	s_barrier
	s_setprio 2
	v_mfma_scale_f32_16x16x128_f8f6f4 v[94:97], v[2:9], v[196:203], v[94:97], v194, v194 op_sel_hi:[0,0,0]
	v_mfma_scale_f32_16x16x128_f8f6f4 v[90:93], v[10:17], v[196:203], v[90:93], v194, v194 op_sel_hi:[0,0,0]
	v_mfma_scale_f32_16x16x128_f8f6f4 v[82:85], v[2:9], v[204:211], v[82:85], v194, v194 op_sel_hi:[0,0,0]
	v_mfma_scale_f32_16x16x128_f8f6f4 v[74:77], v[10:17], v[204:211], v[74:77], v194, v194 op_sel_hi:[0,0,0]
	v_mfma_scale_f32_16x16x128_f8f6f4 v[66:69], v[2:9], v[212:219], v[66:69], v194, v194 op_sel_hi:[0,0,0]
	v_mfma_scale_f32_16x16x128_f8f6f4 v[58:61], v[10:17], v[212:219], v[58:61], v194, v194 op_sel_hi:[0,0,0]
	v_mfma_scale_f32_16x16x128_f8f6f4 v[50:53], v[2:9], v[220:227], v[50:53], v194, v194 op_sel_hi:[0,0,0]
	v_mfma_scale_f32_16x16x128_f8f6f4 v[42:45], v[10:17], v[220:227], v[42:45], v194, v194 op_sel_hi:[0,0,0]
	s_nop 3
	s_setprio 0
	s_setprio 2
	v_mfma_scale_f32_16x16x128_f8f6f4 v[86:89], v[18:25], v[196:203], v[86:89], v194, v194 op_sel_hi:[0,0,0]
	v_mfma_scale_f32_16x16x128_f8f6f4 v[78:81], v[26:33], v[196:203], v[78:81], v194, v194 op_sel_hi:[0,0,0]
	v_mfma_scale_f32_16x16x128_f8f6f4 v[70:73], v[18:25], v[204:211], v[70:73], v194, v194 op_sel_hi:[0,0,0]
	v_mfma_scale_f32_16x16x128_f8f6f4 v[62:65], v[26:33], v[204:211], v[62:65], v194, v194 op_sel_hi:[0,0,0]
	v_mfma_scale_f32_16x16x128_f8f6f4 v[54:57], v[18:25], v[212:219], v[54:57], v194, v194 op_sel_hi:[0,0,0]
	v_mfma_scale_f32_16x16x128_f8f6f4 v[46:49], v[26:33], v[212:219], v[46:49], v194, v194 op_sel_hi:[0,0,0]
	v_mfma_scale_f32_16x16x128_f8f6f4 v[38:41], v[18:25], v[220:227], v[38:41], v194, v194 op_sel_hi:[0,0,0]
	v_mfma_scale_f32_16x16x128_f8f6f4 v[34:37], v[26:33], v[220:227], v[34:37], v194, v194 op_sel_hi:[0,0,0]
	s_setprio 0
	s_add_i32 s65, s65, 2
	s_add_u32 s19, s19, 0x10000
	s_addc_u32 s21, s21, 0
	s_add_u32 s28, s28, 0x10000
	s_addc_u32 s29, s29, 0
	s_cmp_gt_u32 s65, 13
	s_cbranch_scc0 .Lh1_911

; #define PG8_STAGE(bufoff, gbase, voff) do { _Pragma("unroll") for (int _i = 0; _i < 2; ++_i) \
;         __builtin_amdgcn_global_load_lds((const unsigned*)((const char*)(gbase) + (voff)[_i]), (PG8_LAS unsigned*)(lds + (bufoff) + ldsw + _i * 8192), 16, 0, 0); } while (0)
; #define PG8_WAIT_V(n) asm volatile("s_waitcnt vmcnt(" #n ")" ::: "memory")
; #define PG8_WAIT_L(n) asm volatile("s_waitcnt lgkmcnt(" #n ")" ::: "memory")
; #define PG8_BAR __builtin_amdgcn_s_barrier()
; #define PG8_SCHED __builtin_amdgcn_sched_barrier(0)
; template <class Epi, class Sched, bool ALIGN_EPI = true, bool F8 = false>
; __device__ __forceinline__ void gemm_phase(PG8_LAS unsigned char* lds, const Sched& S, const Epi& E) {
;     ...
;             const char* a1 = cA + (size_t)(t + 1) * kstep;
;             const char* a2 = last ? nA : cA + (size_t)(t + 2) * kstep; const char* b2 = last ? nB : cB + (size_t)(t + 2) * kstepB;
;             const char* a3 = a2 + kstep; const char* b3 = b2 + kstepB;
;             unsigned vA2[2][2];
; #pragma unroll
;             for (int h = 0; h < 2; ++h)
; #pragma unroll
;                 for (int i = 0; i < 2; ++i) { if constexpr (Sched::GATHER) vA2[h][i] = (last && has_next) ? voffAn[h][i] : voffA[h][i]; else vA2[h][i] = voffA[h][i]; }
;             PG8_LDB(B0, 0, 0); PG8_LDB(B1, 0, 1); PG8_SCHED; PG8_LDA(At, 0, 0); PG8_STAGE(PG8_SA(1, 1), a1, voffA[1]);
;             PG8_WAIT_V(8); PG8_WAIT_L(0); PG8_BAR; PG8_MMA(0, 0, At, B0); PG8_MMA(0, 1, At, B1); PG8_BAR; PG8_SCHED;
;             PG8_LDA(At, 0, 1); PG8_STAGE(PG8_SB(0, 0), b2, voffB[0]); PG8_STAGE(PG8_SB(0, 1), b2, voffB[1]); PG8_STAGE(PG8_SA(0, 0), a2, vA2[0]);
;             PG8_WAIT_V(8); PG8_WAIT_L(0); PG8_BAR; PG8_MMA(1, 0, At, B0); PG8_MMA(1, 1, At, B1); PG8_BAR; PG8_SCHED;
;             PG8_LDB(B0, 1, 0); PG8_LDB(B1, 1, 1); PG8_SCHED; PG8_LDA(At, 1, 0); PG8_STAGE(PG8_SA(0, 1), a2, vA2[1]);
;             PG8_WAIT_V(8); PG8_WAIT_L(0); PG8_BAR; PG8_MMA(0, 0, At, B0); PG8_MMA(0, 1, At, B1); PG8_BAR; PG8_SCHED;
.LBB0_1138:
	ds_read_b128 v[18:21], v189
	ds_read_b128 v[22:25], v189 offset:1024
	ds_read_b128 v[26:29], v189 offset:2048
	ds_read_b128 v[30:33], v189 offset:3072
	ds_read_b128 v[2:5], v190
	ds_read_b128 v[6:9], v190 offset:1024
	ds_read_b128 v[10:13], v190 offset:2048
	ds_read_b128 v[14:17], v190 offset:3072
	s_add_u32 s26, s24, 0x8000
	s_addc_u32 s27, s25, 0
	s_cmp_eq_u32 s68, 4
	s_cselect_b32 s30, s16, s26
	s_cselect_b32 s31, s17, s27
	s_cselect_b32 s28, s18, s23
	s_cselect_b32 s29, s19, s67
	s_add_u32 s26, s30, 0x8000
	s_addc_u32 s27, s31, 0
	s_add_i32 m0, s44, 0xc000
	ds_read_b128 v[194:197], v191
	ds_read_b128 v[198:201], v191 offset:1024
	ds_read_b128 v[202:205], v191 offset:2048
	ds_read_b128 v[206:209], v191 offset:3072
	ds_read_b128 v[210:213], v191 offset:4096
	ds_read_b128 v[214:217], v191 offset:5120
	ds_read_b128 v[218:221], v191 offset:6144
	ds_read_b128 v[222:225], v191 offset:7168
	global_load_lds_dwordx4 v184, s[24:25]
	s_add_i32 m0, s44, 0xe000
	s_nop 0
	global_load_lds_dwordx4 v182, s[24:25]
	s_waitcnt vmcnt(8)
	s_waitcnt lgkmcnt(0)
	s_setprio 1
	v_mfma_scale_f32_16x16x128_f8f6f4 v[158:161], v[18:25], v[194:201], v[158:161], v192, v192 op_sel_hi:[0,0,0]
	v_mfma_scale_f32_16x16x128_f8f6f4 v[154:157], v[26:33], v[194:201], v[154:157], v192, v192 op_sel_hi:[0,0,0]
	v_mfma_scale_f32_16x16x128_f8f6f4 v[142:145], v[18:25], v[202:209], v[142:145], v192, v192 op_sel_hi:[0,0,0]
	v_mfma_scale_f32_16x16x128_f8f6f4 v[138:141], v[26:33], v[202:209], v[138:141], v192, v192 op_sel_hi:[0,0,0]
	v_mfma_scale_f32_16x16x128_f8f6f4 v[126:129], v[18:25], v[210:217], v[126:129], v192, v192 op_sel_hi:[0,0,0]
	v_mfma_scale_f32_16x16x128_f8f6f4 v[122:125], v[26:33], v[210:217], v[122:125], v192, v192 op_sel_hi:[0,0,0]
	v_mfma_scale_f32_16x16x128_f8f6f4 v[110:113], v[18:25], v[218:225], v[110:113], v192, v192 op_sel_hi:[0,0,0]
	v_mfma_scale_f32_16x16x128_f8f6f4 v[106:109], v[26:33], v[218:225], v[106:109], v192, v192 op_sel_hi:[0,0,0]
	s_nop 3
	s_setprio 0
	s_setprio 1
	v_mfma_scale_f32_16x16x128_f8f6f4 v[150:153], v[2:9], v[194:201], v[150:153], v192, v192 op_sel_hi:[0,0,0]
	v_mfma_scale_f32_16x16x128_f8f6f4 v[146:149], v[10:17], v[194:201], v[146:149], v192, v192 op_sel_hi:[0,0,0]
	v_mfma_scale_f32_16x16x128_f8f6f4 v[134:137], v[2:9], v[202:209], v[134:137], v192, v192 op_sel_hi:[0,0,0]
	v_mfma_scale_f32_16x16x128_f8f6f4 v[130:133], v[10:17], v[202:209], v[130:133], v192, v192 op_sel_hi:[0,0,0]
	v_mfma_scale_f32_16x16x128_f8f6f4 v[118:121], v[2:9], v[210:217], v[118:121], v192, v192 op_sel_hi:[0,0,0]
	v_mfma_scale_f32_16x16x128_f8f6f4 v[114:117], v[10:17], v[210:217], v[114:117], v192, v192 op_sel_hi:[0,0,0]
	v_mfma_scale_f32_16x16x128_f8f6f4 v[102:105], v[2:9], v[218:225], v[102:105], v192, v192 op_sel_hi:[0,0,0]
	v_mfma_scale_f32_16x16x128_f8f6f4 v[98:101], v[10:17], v[218:225], v[98:101], v192, v192 op_sel_hi:[0,0,0]
	s_setprio 0
	s_barrier
	s_add_i32 s69, s53, s43
	s_mov_b32 m0, s69
	ds_read_b128 v[194:197], v191 offset:16384
	ds_read_b128 v[198:201], v191 offset:17408
	ds_read_b128 v[202:205], v191 offset:18432
	ds_read_b128 v[206:209], v191 offset:19456
	ds_read_b128 v[210:213], v191 offset:20480
	ds_read_b128 v[214:217], v191 offset:21504
	ds_read_b128 v[218:221], v191 offset:22528
	ds_read_b128 v[222:225], v191 offset:23552
	global_load_lds_dwordx4 v164, s[28:29]
	s_add_i32 m0, s69, 0x2000
	s_add_i32 s69, s58, s43
	global_load_lds_dwordx4 v166, s[28:29]
	s_add_u32 s98, s28, s4
	s_addc_u32 s99, s29, s5
	s_mov_b32 m0, s69
	s_nop 0
	global_load_lds_dwordx4 v164, s[98:99]
	s_add_u32 s100, s28, s4
	s_addc_u32 s101, s29, s5
	s_add_i32 m0, s69, 0x2000
	s_nop 0
	global_load_lds_dwordx4 v166, s[100:101]
	s_mov_b32 m0, s44
	s_nop 0
	global_load_lds_dwordx4 v168, s[30:31]
	s_mov_b32 m0, s45
	s_nop 0
	global_load_lds_dwordx4 v170, s[30:31]
	s_waitcnt vmcnt(8)
	s_waitcnt lgkmcnt(0)
	s_setprio 1
	v_mfma_scale_f32_16x16x128_f8f6f4 v[94:97], v[18:25], v[194:201], v[94:97], v192, v192 op_sel_hi:[0,0,0]
	v_mfma_scale_f32_16x16x128_f8f6f4 v[90:93], v[26:33], v[194:201], v[90:93], v192, v192 op_sel_hi:[0,0,0]
	v_mfma_scale_f32_16x16x128_f8f6f4 v[78:81], v[18:25], v[202:209], v[78:81], v192, v192 op_sel_hi:[0,0,0]
	v_mfma_scale_f32_16x16x128_f8f6f4 v[74:77], v[26:33], v[202:209], v[74:77], v192, v192 op_sel_hi:[0,0,0]
	v_mfma_scale_f32_16x16x128_f8f6f4 v[62:65], v[18:25], v[210:217], v[62:65], v192, v192 op_sel_hi:[0,0,0]
	v_mfma_scale_f32_16x16x128_f8f6f4 v[58:61], v[26:33], v[210:217], v[58:61], v192, v192 op_sel_hi:[0,0,0]
	v_mfma_scale_f32_16x16x128_f8f6f4 v[46:49], v[18:25], v[218:225], v[46:49], v192, v192 op_sel_hi:[0,0,0]
	v_mfma_scale_f32_16x16x128_f8f6f4 v[42:45], v[26:33], v[218:225], v[42:45], v192, v192 op_sel_hi:[0,0,0]
	s_nop 3
	s_setprio 0
	s_setprio 1
	v_mfma_scale_f32_16x16x128_f8f6f4 v[86:89], v[2:9], v[194:201], v[86:89], v192, v192 op_sel_hi:[0,0,0]
	v_mfma_scale_f32_16x16x128_f8f6f4 v[82:85], v[10:17], v[194:201], v[82:85], v192, v192 op_sel_hi:[0,0,0]
	v_mfma_scale_f32_16x16x128_f8f6f4 v[70:73], v[2:9], v[202:209], v[70:73], v192, v192 op_sel_hi:[0,0,0]
	v_mfma_scale_f32_16x16x128_f8f6f4 v[66:69], v[10:17], v[202:209], v[66:69], v192, v192 op_sel_hi:[0,0,0]
	v_mfma_scale_f32_16x16x128_f8f6f4 v[54:57], v[2:9], v[210:217], v[54:57], v192, v192 op_sel_hi:[0,0,0]
	v_mfma_scale_f32_16x16x128_f8f6f4 v[50:53], v[10:17], v[210:217], v[50:53], v192, v192 op_sel_hi:[0,0,0]
	v_mfma_scale_f32_16x16x128_f8f6f4 v[38:41], v[2:9], v[218:225], v[38:41], v192, v192 op_sel_hi:[0,0,0]
	v_mfma_scale_f32_16x16x128_f8f6f4 v[34:37], v[10:17], v[218:225], v[34:37], v192, v192 op_sel_hi:[0,0,0]
	s_setprio 0
	s_barrier
; #define PG8_STAGE(bufoff, gbase, voff) do { _Pragma("unroll") for (int _i = 0; _i < 2; ++_i) \
;         __builtin_amdgcn_global_load_lds((const unsigned*)((const char*)(gbase) + (voff)[_i]), (PG8_LAS unsigned*)(lds + (bufoff) + ldsw + _i * 8192), 16, 0, 0); } while (0)
; #define PG8_WAIT_V(n) asm volatile("s_waitcnt vmcnt(" #n ")" ::: "memory")
; #define PG8_WAIT_L(n) asm volatile("s_waitcnt lgkmcnt(" #n ")" ::: "memory")
; #define PG8_BAR __builtin_amdgcn_s_barrier()
; #define PG8_SCHED __builtin_amdgcn_sched_barrier(0)
; template <class Epi, class Sched, bool ALIGN_EPI = true, bool F8 = false>
; __device__ __forceinline__ void gemm_phase(PG8_LAS unsigned char* lds, const Sched& S, const Epi& E) {
;     ...
;             PG8_LDB(B0, 1, 0); PG8_LDB(B1, 1, 1); PG8_SCHED; PG8_LDA(At, 1, 0); PG8_STAGE(PG8_SA(0, 1), a2, vA2[1]);
;             PG8_WAIT_V(8); PG8_WAIT_L(0); PG8_BAR; PG8_MMA(0, 0, At, B0); PG8_MMA(0, 1, At, B1); PG8_BAR; PG8_SCHED;
;             PG8_LDA(At, 1, 1); PG8_STAGE(PG8_SB(1, 0), b3, voffB[0]); PG8_STAGE(PG8_SB(1, 1), b3, voffB[1]); PG8_STAGE(PG8_SA(1, 0), a3, vA2[0]);
;             PG8_WAIT_V(8); PG8_WAIT_L(0); PG8_BAR; PG8_MMA(1, 0, At, B0); PG8_MMA(1, 1, At, B1); PG8_BAR; PG8_SCHED;
	s_add_i32 s69, 0, 0x18000
	s_add_i32 s70, 0, 0x1c000
	v_add_u32_e32 v14, s69, v187
	v_add_u32_e32 v30, s70, v187
	ds_read_b128 v[2:5], v14
	ds_read_b128 v[6:9], v14 offset:1024
	ds_read_b128 v[10:13], v14 offset:2048
	ds_read_b128 v[14:17], v14 offset:3072
	ds_read_b128 v[18:21], v30
	ds_read_b128 v[22:25], v30 offset:1024
	ds_read_b128 v[26:29], v30 offset:2048
	ds_read_b128 v[30:33], v30 offset:3072
	s_mov_b32 m0, s46
	ds_read_b128 v[194:197], v191 offset:32768
	ds_read_b128 v[198:201], v191 offset:33792
	ds_read_b128 v[202:205], v191 offset:34816
	ds_read_b128 v[206:209], v191 offset:35840
	ds_read_b128 v[210:213], v191 offset:36864
	ds_read_b128 v[214:217], v191 offset:37888
	ds_read_b128 v[218:221], v191 offset:38912
	ds_read_b128 v[222:225], v191 offset:39936
	global_load_lds_dwordx4 v172, s[30:31]
	s_mov_b32 m0, s47
	s_nop 0
	global_load_lds_dwordx4 v174, s[30:31]
	s_waitcnt vmcnt(8)
	s_waitcnt lgkmcnt(0)
	s_setprio 1
	v_mfma_scale_f32_16x16x128_f8f6f4 v[158:161], v[2:9], v[194:201], v[158:161], v192, v192 op_sel_hi:[0,0,0]
	v_mfma_scale_f32_16x16x128_f8f6f4 v[154:157], v[10:17], v[194:201], v[154:157], v192, v192 op_sel_hi:[0,0,0]
	v_mfma_scale_f32_16x16x128_f8f6f4 v[142:145], v[2:9], v[202:209], v[142:145], v192, v192 op_sel_hi:[0,0,0]
	v_mfma_scale_f32_16x16x128_f8f6f4 v[138:141], v[10:17], v[202:209], v[138:141], v192, v192 op_sel_hi:[0,0,0]
	v_mfma_scale_f32_16x16x128_f8f6f4 v[126:129], v[2:9], v[210:217], v[126:129], v192, v192 op_sel_hi:[0,0,0]
	v_mfma_scale_f32_16x16x128_f8f6f4 v[122:125], v[10:17], v[210:217], v[122:125], v192, v192 op_sel_hi:[0,0,0]
	v_mfma_scale_f32_16x16x128_f8f6f4 v[110:113], v[2:9], v[218:225], v[110:113], v192, v192 op_sel_hi:[0,0,0]
	v_mfma_scale_f32_16x16x128_f8f6f4 v[106:109], v[10:17], v[218:225], v[106:109], v192, v192 op_sel_hi:[0,0,0]
	s_nop 3
	s_setprio 0
	s_setprio 1
	v_mfma_scale_f32_16x16x128_f8f6f4 v[150:153], v[18:25], v[194:201], v[150:153], v192, v192 op_sel_hi:[0,0,0]
	v_mfma_scale_f32_16x16x128_f8f6f4 v[146:149], v[26:33], v[194:201], v[146:149], v192, v192 op_sel_hi:[0,0,0]
	v_mfma_scale_f32_16x16x128_f8f6f4 v[134:137], v[18:25], v[202:209], v[134:137], v192, v192 op_sel_hi:[0,0,0]
	v_mfma_scale_f32_16x16x128_f8f6f4 v[130:133], v[26:33], v[202:209], v[130:133], v192, v192 op_sel_hi:[0,0,0]
	v_mfma_scale_f32_16x16x128_f8f6f4 v[118:121], v[18:25], v[210:217], v[118:121], v192, v192 op_sel_hi:[0,0,0]
	v_mfma_scale_f32_16x16x128_f8f6f4 v[114:117], v[26:33], v[210:217], v[114:117], v192, v192 op_sel_hi:[0,0,0]
	v_mfma_scale_f32_16x16x128_f8f6f4 v[102:105], v[18:25], v[218:225], v[102:105], v192, v192 op_sel_hi:[0,0,0]
	v_mfma_scale_f32_16x16x128_f8f6f4 v[98:101], v[26:33], v[218:225], v[98:101], v192, v192 op_sel_hi:[0,0,0]
	s_setprio 0
	s_barrier
	s_add_u32 s28, s28, 0x8000
	s_addc_u32 s29, s29, 0
	s_add_i32 s30, s69, s43
	s_mov_b32 m0, s30
	ds_read_b128 v[194:197], v191 offset:49152
	ds_read_b128 v[198:201], v191 offset:50176
	ds_read_b128 v[202:205], v191 offset:51200
	ds_read_b128 v[206:209], v191 offset:52224
	ds_read_b128 v[210:213], v191 offset:53248
	ds_read_b128 v[214:217], v191 offset:54272
	ds_read_b128 v[218:221], v191 offset:55296
	ds_read_b128 v[222:225], v191 offset:56320
	global_load_lds_dwordx4 v164, s[28:29]
	s_add_i32 m0, s30, 0x2000
	s_add_i32 s30, s70, s43
	global_load_lds_dwordx4 v166, s[28:29]
	s_mov_b32 m0, s30
	s_nop 0
	global_load_lds_dwordx4 v178, s[28:29]
	s_add_i32 m0, s30, 0x2000
	s_nop 0
	global_load_lds_dwordx4 v180, s[28:29]
	s_mov_b32 m0, s51
	s_nop 0
	global_load_lds_dwordx4 v168, s[26:27]
	s_mov_b32 m0, s52
	s_nop 0
	global_load_lds_dwordx4 v170, s[26:27]
	s_waitcnt vmcnt(8)
	s_waitcnt lgkmcnt(0)
	s_setprio 1
	v_mfma_scale_f32_16x16x128_f8f6f4 v[94:97], v[2:9], v[194:201], v[94:97], v192, v192 op_sel_hi:[0,0,0]
	v_mfma_scale_f32_16x16x128_f8f6f4 v[90:93], v[10:17], v[194:201], v[90:93], v192, v192 op_sel_hi:[0,0,0]
	v_mfma_scale_f32_16x16x128_f8f6f4 v[78:81], v[2:9], v[202:209], v[78:81], v192, v192 op_sel_hi:[0,0,0]
	v_mfma_scale_f32_16x16x128_f8f6f4 v[74:77], v[10:17], v[202:209], v[74:77], v192, v192 op_sel_hi:[0,0,0]
	v_mfma_scale_f32_16x16x128_f8f6f4 v[62:65], v[2:9], v[210:217], v[62:65], v192, v192 op_sel_hi:[0,0,0]
	v_mfma_scale_f32_16x16x128_f8f6f4 v[58:61], v[10:17], v[210:217], v[58:61], v192, v192 op_sel_hi:[0,0,0]
	v_mfma_scale_f32_16x16x128_f8f6f4 v[46:49], v[2:9], v[218:225], v[46:49], v192, v192 op_sel_hi:[0,0,0]
	v_mfma_scale_f32_16x16x128_f8f6f4 v[42:45], v[10:17], v[218:225], v[42:45], v192, v192 op_sel_hi:[0,0,0]
	s_nop 3
	s_setprio 0
	s_setprio 1
	v_mfma_scale_f32_16x16x128_f8f6f4 v[86:89], v[18:25], v[194:201], v[86:89], v192, v192 op_sel_hi:[0,0,0]
	v_mfma_scale_f32_16x16x128_f8f6f4 v[82:85], v[26:33], v[194:201], v[82:85], v192, v192 op_sel_hi:[0,0,0]
	v_mfma_scale_f32_16x16x128_f8f6f4 v[70:73], v[18:25], v[202:209], v[70:73], v192, v192 op_sel_hi:[0,0,0]
	v_mfma_scale_f32_16x16x128_f8f6f4 v[66:69], v[26:33], v[202:209], v[66:69], v192, v192 op_sel_hi:[0,0,0]
	v_mfma_scale_f32_16x16x128_f8f6f4 v[54:57], v[18:25], v[210:217], v[54:57], v192, v192 op_sel_hi:[0,0,0]
	v_mfma_scale_f32_16x16x128_f8f6f4 v[50:53], v[26:33], v[210:217], v[50:53], v192, v192 op_sel_hi:[0,0,0]
	v_mfma_scale_f32_16x16x128_f8f6f4 v[38:41], v[18:25], v[218:225], v[38:41], v192, v192 op_sel_hi:[0,0,0]
	v_mfma_scale_f32_16x16x128_f8f6f4 v[34:37], v[26:33], v[218:225], v[34:37], v192, v192 op_sel_hi:[0,0,0]
	s_setprio 0
	s_barrier
	s_add_i32 s68, s68, 2
	s_add_u32 s23, s23, 0x10000
	s_addc_u32 s67, s67, 0
	s_add_u32 s24, s24, 0x10000
	s_addc_u32 s25, s25, 0
	s_cmp_gt_u32 s68, 5
	s_cbranch_scc0 .LBB0_1138
	s_branch .Lfx_33571
; #define PG8_STAGE(bufoff, gbase, voff) do { _Pragma("unroll") for (int _i = 0; _i < 2; ++_i) \
;         __builtin_amdgcn_global_load_lds((const unsigned*)((const char*)(gbase) + (voff)[_i]), (PG8_LAS unsigned*)(lds + (bufoff) + ldsw + _i * 8192), 16, 0, 0); } while (0)
; #define PG8_WAIT_V(n) asm volatile("s_waitcnt vmcnt(" #n ")" ::: "memory")
; #define PG8_WAIT_L(n) asm volatile("s_waitcnt lgkmcnt(" #n ")" ::: "memory")
; #define PG8_BAR __builtin_amdgcn_s_barrier()
; #define PG8_SCHED __builtin_amdgcn_sched_barrier(0)
; template <class Epi, class Sched, bool ALIGN_EPI = true, bool F8 = false>
; __device__ __forceinline__ void gemm_phase(PG8_LAS unsigned char* lds, const Sched& S, const Epi& E) {
;     ...
;             const char* a1 = cA + (size_t)(t + 1) * kstep;
;             const char* a2 = last ? nA : cA + (size_t)(t + 2) * kstep; const char* b2 = last ? nB : cB + (size_t)(t + 2) * kstepB;
;             const char* a3 = a2 + kstep; const char* b3 = b2 + kstepB;
;             unsigned vA2[2][2];
; #pragma unroll
;             for (int h = 0; h < 2; ++h)
; #pragma unroll
;                 for (int i = 0; i < 2; ++i) { if constexpr (Sched::GATHER) vA2[h][i] = (last && has_next) ? voffAn[h][i] : voffA[h][i]; else vA2[h][i] = voffA[h][i]; }
;             PG8_LDB(B0, 0, 0); PG8_LDB(B1, 0, 1); PG8_SCHED; PG8_LDA(At, 0, 0); PG8_STAGE(PG8_SA(1, 1), a1, voffA[1]);
;             PG8_WAIT_V(8); PG8_WAIT_L(0); PG8_BAR; PG8_MMA(0, 0, At, B0); PG8_MMA(0, 1, At, B1); PG8_BAR; PG8_SCHED;
;             PG8_LDA(At, 0, 1); PG8_STAGE(PG8_SB(0, 0), b2, voffB[0]); PG8_STAGE(PG8_SB(0, 1), b2, voffB[1]); PG8_STAGE(PG8_SA(0, 0), a2, vA2[0]);
;             PG8_WAIT_V(8); PG8_WAIT_L(0); PG8_BAR; PG8_MMA(1, 0, At, B0); PG8_MMA(1, 1, At, B1); PG8_BAR; PG8_SCHED;
;             PG8_LDB(B0, 1, 0); PG8_LDB(B1, 1, 1); PG8_SCHED; PG8_LDA(At, 1, 0); PG8_STAGE(PG8_SA(0, 1), a2, vA2[1]);
;             PG8_WAIT_V(8); PG8_WAIT_L(0); PG8_BAR; PG8_MMA(0, 0, At, B0); PG8_MMA(0, 1, At, B1); PG8_BAR; PG8_SCHED;
.Lh1e_33571:
.Lh1_1138:
	ds_read_b128 v[18:21], v189
	ds_read_b128 v[22:25], v189 offset:1024
	ds_read_b128 v[26:29], v189 offset:2048
	ds_read_b128 v[30:33], v189 offset:3072
	ds_read_b128 v[2:5], v190
	ds_read_b128 v[6:9], v190 offset:1024
	ds_read_b128 v[10:13], v190 offset:2048
	ds_read_b128 v[14:17], v190 offset:3072
	s_add_u32 s26, s24, 0x8000
	s_addc_u32 s27, s25, 0
	s_cmp_eq_u32 s68, 4
	s_cselect_b32 s30, s16, s26
	s_cselect_b32 s31, s17, s27
	s_cselect_b32 s28, s18, s23
	s_cselect_b32 s29, s19, s67
	s_add_u32 s26, s30, 0x8000
	s_addc_u32 s27, s31, 0
	s_add_i32 m0, s44, 0xc000
	ds_read_b128 v[194:197], v191
	ds_read_b128 v[198:201], v191 offset:1024
	ds_read_b128 v[202:205], v191 offset:2048
	ds_read_b128 v[206:209], v191 offset:3072
	ds_read_b128 v[210:213], v191 offset:4096
	ds_read_b128 v[214:217], v191 offset:5120
	ds_read_b128 v[218:221], v191 offset:6144
	ds_read_b128 v[222:225], v191 offset:7168
	global_load_lds_dwordx4 v184, s[24:25]
	s_add_i32 m0, s44, 0xe000
	s_nop 0
	global_load_lds_dwordx4 v182, s[24:25]
	s_waitcnt vmcnt(8)
	s_waitcnt lgkmcnt(0)
	s_barrier
	s_setprio 2
	v_mfma_scale_f32_16x16x128_f8f6f4 v[158:161], v[18:25], v[194:201], v[158:161], v192, v192 op_sel_hi:[0,0,0]
	v_mfma_scale_f32_16x16x128_f8f6f4 v[154:157], v[26:33], v[194:201], v[154:157], v192, v192 op_sel_hi:[0,0,0]
	v_mfma_scale_f32_16x16x128_f8f6f4 v[142:145], v[18:25], v[202:209], v[142:145], v192, v192 op_sel_hi:[0,0,0]
	v_mfma_scale_f32_16x16x128_f8f6f4 v[138:141], v[26:33], v[202:209], v[138:141], v192, v192 op_sel_hi:[0,0,0]
	v_mfma_scale_f32_16x16x128_f8f6f4 v[126:129], v[18:25], v[210:217], v[126:129], v192, v192 op_sel_hi:[0,0,0]
	v_mfma_scale_f32_16x16x128_f8f6f4 v[122:125], v[26:33], v[210:217], v[122:125], v192, v192 op_sel_hi:[0,0,0]
	v_mfma_scale_f32_16x16x128_f8f6f4 v[110:113], v[18:25], v[218:225], v[110:113], v192, v192 op_sel_hi:[0,0,0]
	v_mfma_scale_f32_16x16x128_f8f6f4 v[106:109], v[26:33], v[218:225], v[106:109], v192, v192 op_sel_hi:[0,0,0]
	s_nop 3
	s_setprio 0
	s_setprio 2
	v_mfma_scale_f32_16x16x128_f8f6f4 v[150:153], v[2:9], v[194:201], v[150:153], v192, v192 op_sel_hi:[0,0,0]
	v_mfma_scale_f32_16x16x128_f8f6f4 v[146:149], v[10:17], v[194:201], v[146:149], v192, v192 op_sel_hi:[0,0,0]
	v_mfma_scale_f32_16x16x128_f8f6f4 v[134:137], v[2:9], v[202:209], v[134:137], v192, v192 op_sel_hi:[0,0,0]
	v_mfma_scale_f32_16x16x128_f8f6f4 v[130:133], v[10:17], v[202:209], v[130:133], v192, v192 op_sel_hi:[0,0,0]
	v_mfma_scale_f32_16x16x128_f8f6f4 v[118:121], v[2:9], v[210:217], v[118:121], v192, v192 op_sel_hi:[0,0,0]
	v_mfma_scale_f32_16x16x128_f8f6f4 v[114:117], v[10:17], v[210:217], v[114:117], v192, v192 op_sel_hi:[0,0,0]
	v_mfma_scale_f32_16x16x128_f8f6f4 v[102:105], v[2:9], v[218:225], v[102:105], v192, v192 op_sel_hi:[0,0,0]
	v_mfma_scale_f32_16x16x128_f8f6f4 v[98:101], v[10:17], v[218:225], v[98:101], v192, v192 op_sel_hi:[0,0,0]
	s_setprio 0
	s_add_i32 s69, s53, s43
	s_mov_b32 m0, s69
	ds_read_b128 v[194:197], v191 offset:16384
	ds_read_b128 v[198:201], v191 offset:17408
	ds_read_b128 v[202:205], v191 offset:18432
	ds_read_b128 v[206:209], v191 offset:19456
	ds_read_b128 v[210:213], v191 offset:20480
	ds_read_b128 v[214:217], v191 offset:21504
	ds_read_b128 v[218:221], v191 offset:22528
	ds_read_b128 v[222:225], v191 offset:23552
	global_load_lds_dwordx4 v164, s[28:29]
	s_add_i32 m0, s69, 0x2000
	s_add_i32 s69, s58, s43
	global_load_lds_dwordx4 v166, s[28:29]
	s_add_u32 s98, s28, s4
	s_addc_u32 s99, s29, s5
	s_mov_b32 m0, s69
	s_nop 0
	global_load_lds_dwordx4 v164, s[98:99]
	s_add_u32 s100, s28, s4
	s_addc_u32 s101, s29, s5
	s_add_i32 m0, s69, 0x2000
	s_nop 0
	global_load_lds_dwordx4 v166, s[100:101]
	s_mov_b32 m0, s44
	s_nop 0
	global_load_lds_dwordx4 v168, s[30:31]
	s_mov_b32 m0, s45
	s_nop 0
	global_load_lds_dwordx4 v170, s[30:31]
	s_waitcnt vmcnt(8)
	s_waitcnt lgkmcnt(0)
	s_barrier
	s_setprio 2
	v_mfma_scale_f32_16x16x128_f8f6f4 v[94:97], v[18:25], v[194:201], v[94:97], v192, v192 op_sel_hi:[0,0,0]
	v_mfma_scale_f32_16x16x128_f8f6f4 v[90:93], v[26:33], v[194:201], v[90:93], v192, v192 op_sel_hi:[0,0,0]
	v_mfma_scale_f32_16x16x128_f8f6f4 v[78:81], v[18:25], v[202:209], v[78:81], v192, v192 op_sel_hi:[0,0,0]
	v_mfma_scale_f32_16x16x128_f8f6f4 v[74:77], v[26:33], v[202:209], v[74:77], v192, v192 op_sel_hi:[0,0,0]
	v_mfma_scale_f32_16x16x128_f8f6f4 v[62:65], v[18:25], v[210:217], v[62:65], v192, v192 op_sel_hi:[0,0,0]
	v_mfma_scale_f32_16x16x128_f8f6f4 v[58:61], v[26:33], v[210:217], v[58:61], v192, v192 op_sel_hi:[0,0,0]
	v_mfma_scale_f32_16x16x128_f8f6f4 v[46:49], v[18:25], v[218:225], v[46:49], v192, v192 op_sel_hi:[0,0,0]
	v_mfma_scale_f32_16x16x128_f8f6f4 v[42:45], v[26:33], v[218:225], v[42:45], v192, v192 op_sel_hi:[0,0,0]
	s_nop 3
	s_setprio 0
	s_setprio 2
	v_mfma_scale_f32_16x16x128_f8f6f4 v[86:89], v[2:9], v[194:201], v[86:89], v192, v192 op_sel_hi:[0,0,0]
	v_mfma_scale_f32_16x16x128_f8f6f4 v[82:85], v[10:17], v[194:201], v[82:85], v192, v192 op_sel_hi:[0,0,0]
	v_mfma_scale_f32_16x16x128_f8f6f4 v[70:73], v[2:9], v[202:209], v[70:73], v192, v192 op_sel_hi:[0,0,0]
	v_mfma_scale_f32_16x16x128_f8f6f4 v[66:69], v[10:17], v[202:209], v[66:69], v192, v192 op_sel_hi:[0,0,0]
	v_mfma_scale_f32_16x16x128_f8f6f4 v[54:57], v[2:9], v[210:217], v[54:57], v192, v192 op_sel_hi:[0,0,0]
	v_mfma_scale_f32_16x16x128_f8f6f4 v[50:53], v[10:17], v[210:217], v[50:53], v192, v192 op_sel_hi:[0,0,0]
	v_mfma_scale_f32_16x16x128_f8f6f4 v[38:41], v[2:9], v[218:225], v[38:41], v192, v192 op_sel_hi:[0,0,0]
	v_mfma_scale_f32_16x16x128_f8f6f4 v[34:37], v[10:17], v[218:225], v[34:37], v192, v192 op_sel_hi:[0,0,0]
	s_setprio 0
	s_add_i32 s69, 0, 0x18000
	s_add_i32 s70, 0, 0x1c000
	v_add_u32_e32 v14, s69, v187
	v_add_u32_e32 v30, s70, v187
	ds_read_b128 v[2:5], v14
	ds_read_b128 v[6:9], v14 offset:1024
	ds_read_b128 v[10:13], v14 offset:2048
	ds_read_b128 v[14:17], v14 offset:3072
	ds_read_b128 v[18:21], v30
	ds_read_b128 v[22:25], v30 offset:1024
	ds_read_b128 v[26:29], v30 offset:2048
	ds_read_b128 v[30:33], v30 offset:3072
	s_mov_b32 m0, s46
	ds_read_b128 v[194:197], v191 offset:32768
	ds_read_b128 v[198:201], v191 offset:33792
	ds_read_b128 v[202:205], v191 offset:34816
	ds_read_b128 v[206:209], v191 offset:35840
	ds_read_b128 v[210:213], v191 offset:36864
	ds_read_b128 v[214:217], v191 offset:37888
	ds_read_b128 v[218:221], v191 offset:38912
	ds_read_b128 v[222:225], v191 offset:39936
	global_load_lds_dwordx4 v172, s[30:31]
	s_mov_b32 m0, s47
	s_nop 0
	global_load_lds_dwordx4 v174, s[30:31]
	s_waitcnt vmcnt(8)
	s_waitcnt lgkmcnt(0)
	s_barrier
; #define PG8_STAGE(bufoff, gbase, voff) do { _Pragma("unroll") for (int _i = 0; _i < 2; ++_i) \
;         __builtin_amdgcn_global_load_lds((const unsigned*)((const char*)(gbase) + (voff)[_i]), (PG8_LAS unsigned*)(lds + (bufoff) + ldsw + _i * 8192), 16, 0, 0); } while (0)
; #define PG8_WAIT_V(n) asm volatile("s_waitcnt vmcnt(" #n ")" ::: "memory")
; #define PG8_WAIT_L(n) asm volatile("s_waitcnt lgkmcnt(" #n ")" ::: "memory")
; #define PG8_BAR __builtin_amdgcn_s_barrier()
; #define PG8_SCHED __builtin_amdgcn_sched_barrier(0)
; template <class Epi, class Sched, bool ALIGN_EPI = true, bool F8 = false>
; __device__ __forceinline__ void gemm_phase(PG8_LAS unsigned char* lds, const Sched& S, const Epi& E) {
;     ...
;             PG8_LDB(B0, 1, 0); PG8_LDB(B1, 1, 1); PG8_SCHED; PG8_LDA(At, 1, 0); PG8_STAGE(PG8_SA(0, 1), a2, vA2[1]);
;             PG8_WAIT_V(8); PG8_WAIT_L(0); PG8_BAR; PG8_MMA(0, 0, At, B0); PG8_MMA(0, 1, At, B1); PG8_BAR; PG8_SCHED;
;             PG8_LDA(At, 1, 1); PG8_STAGE(PG8_SB(1, 0), b3, voffB[0]); PG8_STAGE(PG8_SB(1, 1), b3, voffB[1]); PG8_STAGE(PG8_SA(1, 0), a3, vA2[0]);
;             PG8_WAIT_V(8); PG8_WAIT_L(0); PG8_BAR; PG8_MMA(1, 0, At, B0); PG8_MMA(1, 1, At, B1); PG8_BAR; PG8_SCHED;
	s_setprio 2
	v_mfma_scale_f32_16x16x128_f8f6f4 v[158:161], v[2:9], v[194:201], v[158:161], v192, v192 op_sel_hi:[0,0,0]
	v_mfma_scale_f32_16x16x128_f8f6f4 v[154:157], v[10:17], v[194:201], v[154:157], v192, v192 op_sel_hi:[0,0,0]
	v_mfma_scale_f32_16x16x128_f8f6f4 v[142:145], v[2:9], v[202:209], v[142:145], v192, v192 op_sel_hi:[0,0,0]
	v_mfma_scale_f32_16x16x128_f8f6f4 v[138:141], v[10:17], v[202:209], v[138:141], v192, v192 op_sel_hi:[0,0,0]
	v_mfma_scale_f32_16x16x128_f8f6f4 v[126:129], v[2:9], v[210:217], v[126:129], v192, v192 op_sel_hi:[0,0,0]
	v_mfma_scale_f32_16x16x128_f8f6f4 v[122:125], v[10:17], v[210:217], v[122:125], v192, v192 op_sel_hi:[0,0,0]
	v_mfma_scale_f32_16x16x128_f8f6f4 v[110:113], v[2:9], v[218:225], v[110:113], v192, v192 op_sel_hi:[0,0,0]
	v_mfma_scale_f32_16x16x128_f8f6f4 v[106:109], v[10:17], v[218:225], v[106:109], v192, v192 op_sel_hi:[0,0,0]
	s_nop 3
	s_setprio 0
	s_setprio 2
	v_mfma_scale_f32_16x16x128_f8f6f4 v[150:153], v[18:25], v[194:201], v[150:153], v192, v192 op_sel_hi:[0,0,0]
	v_mfma_scale_f32_16x16x128_f8f6f4 v[146:149], v[26:33], v[194:201], v[146:149], v192, v192 op_sel_hi:[0,0,0]
	v_mfma_scale_f32_16x16x128_f8f6f4 v[134:137], v[18:25], v[202:209], v[134:137], v192, v192 op_sel_hi:[0,0,0]
	v_mfma_scale_f32_16x16x128_f8f6f4 v[130:133], v[26:33], v[202:209], v[130:133], v192, v192 op_sel_hi:[0,0,0]
	v_mfma_scale_f32_16x16x128_f8f6f4 v[118:121], v[18:25], v[210:217], v[118:121], v192, v192 op_sel_hi:[0,0,0]
	v_mfma_scale_f32_16x16x128_f8f6f4 v[114:117], v[26:33], v[210:217], v[114:117], v192, v192 op_sel_hi:[0,0,0]
	v_mfma_scale_f32_16x16x128_f8f6f4 v[102:105], v[18:25], v[218:225], v[102:105], v192, v192 op_sel_hi:[0,0,0]
	v_mfma_scale_f32_16x16x128_f8f6f4 v[98:101], v[26:33], v[218:225], v[98:101], v192, v192 op_sel_hi:[0,0,0]
	s_setprio 0
	s_add_u32 s28, s28, 0x8000
	s_addc_u32 s29, s29, 0
	s_add_i32 s30, s69, s43
	s_mov_b32 m0, s30
	ds_read_b128 v[194:197], v191 offset:49152
	ds_read_b128 v[198:201], v191 offset:50176
	ds_read_b128 v[202:205], v191 offset:51200
	ds_read_b128 v[206:209], v191 offset:52224
	ds_read_b128 v[210:213], v191 offset:53248
	ds_read_b128 v[214:217], v191 offset:54272
	ds_read_b128 v[218:221], v191 offset:55296
	ds_read_b128 v[222:225], v191 offset:56320
	global_load_lds_dwordx4 v164, s[28:29]
	s_add_i32 m0, s30, 0x2000
	s_add_i32 s30, s70, s43
	global_load_lds_dwordx4 v166, s[28:29]
	s_mov_b32 m0, s30
	s_nop 0
	global_load_lds_dwordx4 v178, s[28:29]
	s_add_i32 m0, s30, 0x2000
	s_nop 0
	global_load_lds_dwordx4 v180, s[28:29]
	s_mov_b32 m0, s51
	s_nop 0
	global_load_lds_dwordx4 v168, s[26:27]
	s_mov_b32 m0, s52
	s_nop 0
	global_load_lds_dwordx4 v170, s[26:27]
	s_waitcnt vmcnt(8)
	s_waitcnt lgkmcnt(0)
	s_barrier
	s_setprio 2
	v_mfma_scale_f32_16x16x128_f8f6f4 v[94:97], v[2:9], v[194:201], v[94:97], v192, v192 op_sel_hi:[0,0,0]
	v_mfma_scale_f32_16x16x128_f8f6f4 v[90:93], v[10:17], v[194:201], v[90:93], v192, v192 op_sel_hi:[0,0,0]
	v_mfma_scale_f32_16x16x128_f8f6f4 v[78:81], v[2:9], v[202:209], v[78:81], v192, v192 op_sel_hi:[0,0,0]
	v_mfma_scale_f32_16x16x128_f8f6f4 v[74:77], v[10:17], v[202:209], v[74:77], v192, v192 op_sel_hi:[0,0,0]
	v_mfma_scale_f32_16x16x128_f8f6f4 v[62:65], v[2:9], v[210:217], v[62:65], v192, v192 op_sel_hi:[0,0,0]
	v_mfma_scale_f32_16x16x128_f8f6f4 v[58:61], v[10:17], v[210:217], v[58:61], v192, v192 op_sel_hi:[0,0,0]
	v_mfma_scale_f32_16x16x128_f8f6f4 v[46:49], v[2:9], v[218:225], v[46:49], v192, v192 op_sel_hi:[0,0,0]
	v_mfma_scale_f32_16x16x128_f8f6f4 v[42:45], v[10:17], v[218:225], v[42:45], v192, v192 op_sel_hi:[0,0,0]
	s_nop 3
	s_setprio 0
	s_setprio 2
	v_mfma_scale_f32_16x16x128_f8f6f4 v[86:89], v[18:25], v[194:201], v[86:89], v192, v192 op_sel_hi:[0,0,0]
	v_mfma_scale_f32_16x16x128_f8f6f4 v[82:85], v[26:33], v[194:201], v[82:85], v192, v192 op_sel_hi:[0,0,0]
	v_mfma_scale_f32_16x16x128_f8f6f4 v[70:73], v[18:25], v[202:209], v[70:73], v192, v192 op_sel_hi:[0,0,0]
	v_mfma_scale_f32_16x16x128_f8f6f4 v[66:69], v[26:33], v[202:209], v[66:69], v192, v192 op_sel_hi:[0,0,0]
	v_mfma_scale_f32_16x16x128_f8f6f4 v[54:57], v[18:25], v[210:217], v[54:57], v192, v192 op_sel_hi:[0,0,0]
	v_mfma_scale_f32_16x16x128_f8f6f4 v[50:53], v[26:33], v[210:217], v[50:53], v192, v192 op_sel_hi:[0,0,0]
	v_mfma_scale_f32_16x16x128_f8f6f4 v[38:41], v[18:25], v[218:225], v[38:41], v192, v192 op_sel_hi:[0,0,0]
	v_mfma_scale_f32_16x16x128_f8f6f4 v[34:37], v[26:33], v[218:225], v[34:37], v192, v192 op_sel_hi:[0,0,0]
	s_setprio 0
	s_add_i32 s68, s68, 2
	s_add_u32 s23, s23, 0x10000
	s_addc_u32 s67, s67, 0
	s_add_u32 s24, s24, 0x10000
	s_addc_u32 s25, s25, 0
	s_cmp_gt_u32 s68, 5
	s_cbranch_scc0 .Lh1_1138
